# ret_out second sweep: all operand loads of a thread requested up front (counted vmcnt); MoE gate/up epilogue lookups batched; combine-phase norm gains loaded once
# speedup vs baseline: 1.0578x; 1.0142x over previous
.LBB0_1596:
	s_or_b64 exec, exec, s[8:9]
	v_mul_f32_e32 v34, 0x3d000000, v20

.LBB0_1609:
	ds_read_b128 v[148:151], v143
	ds_read_b128 v[152:155], v143 offset:1024
	ds_read_b128 v[156:159], v143 offset:2048
	ds_read_b128 v[160:163], v143 offset:3072
	s_add_u32 s48, s79, s44
	s_addc_u32 s49, s80, s45
	s_add_u32 s46, s44, 0x100
	s_addc_u32 s47, s45, 0
	s_cmp_eq_u32 s81, 12
	s_cselect_b32 s49, s37, s49
	s_cselect_b32 s48, s39, s48
	s_cselect_b32 s82, 0, s46
	s_cselect_b32 s83, s9, s3
	s_add_i32 m0, s56, 0xc000
	ds_read_b128 v[168:171], v144 offset:1024
	ds_read_b128 v[172:175], v144 offset:2048
	ds_read_b128 v[164:167], v144
	ds_read_b32 v66, v136 offset:512
	ds_read_b128 v[176:179], v144 offset:3072
	ds_read_b128 v[180:183], v144 offset:4096
	ds_read_b128 v[184:187], v144 offset:5120
	ds_read_b128 v[188:191], v144 offset:6144
	ds_read_b128 v[192:195], v144 offset:7168
	s_add_u32 s44, s26, s44
	s_waitcnt lgkmcnt(0)
	v_add_u32_e32 v66, v66, v1
	s_addc_u32 s45, s27, s45
	global_load_lds_dwordx4 v66, s[44:45]
	ds_read_b32 v66, v136 offset:768
	s_add_i32 m0, s56, 0xe000
	s_waitcnt lgkmcnt(0)
	v_add_u32_e32 v66, v66, v1
	global_load_lds_dwordx4 v66, s[44:45]
	s_waitcnt lgkmcnt(8)
	s_barrier
	s_waitcnt lgkmcnt(0)
	s_setprio 1
	v_mfma_scale_f32_16x16x128_f8f6f4 v[126:129], v[148:155], v[164:171], v[126:129], v145, v145 op_sel_hi:[0,0,0]
	v_mfma_scale_f32_16x16x128_f8f6f4 v[118:121], v[156:163], v[164:171], v[118:121], v145, v145 op_sel_hi:[0,0,0]
	v_mfma_scale_f32_16x16x128_f8f6f4 v[110:113], v[148:155], v[172:179], v[110:113], v145, v145 op_sel_hi:[0,0,0]
	v_mfma_scale_f32_16x16x128_f8f6f4 v[102:105], v[156:163], v[172:179], v[102:105], v145, v145 op_sel_hi:[0,0,0]
	v_mfma_scale_f32_16x16x128_f8f6f4 v[212:215], v[148:155], v[180:187], v[94:97], v145, v145 op_sel_hi:[0,0,0]
	v_mfma_scale_f32_16x16x128_f8f6f4 v[216:219], v[156:163], v[180:187], v[86:89], v145, v145 op_sel_hi:[0,0,0]
	v_mfma_scale_f32_16x16x128_f8f6f4 v[220:223], v[148:155], v[188:195], v[78:81], v145, v145 op_sel_hi:[0,0,0]
	v_mfma_scale_f32_16x16x128_f8f6f4 v[224:227], v[156:163], v[188:195], v[204:207], v145, v145 op_sel_hi:[0,0,0]
	s_setprio 0
	s_barrier
	s_add_i32 s44, s68, s55
	v_lshl_add_u64 v[134:135], s[48:49], 0, v[130:131]
	s_mov_b32 m0, s44
	ds_read_b128 v[196:199], v146
	ds_read_b128 v[200:203], v146 offset:1024
	ds_read_b128 v[204:207], v146 offset:2048
	ds_read_b128 v[208:211], v146 offset:3072
	global_load_lds_dwordx4 v[134:135], off
	v_lshl_add_u64 v[66:67], v[134:135], 0, s[10:11]
	s_add_i32 m0, s44, 0x2000
	s_nop 0
	global_load_lds_dwordx4 v[66:67], off
	s_barrier
	s_waitcnt lgkmcnt(0)
	s_setprio 1
	s_waitcnt lgkmcnt(0)
	v_mfma_scale_f32_16x16x128_f8f6f4 v[122:125], v[196:203], v[164:171], v[122:125], v145, v145 op_sel_hi:[0,0,0]
	v_mfma_scale_f32_16x16x128_f8f6f4 v[114:117], v[204:211], v[164:171], v[114:117], v145, v145 op_sel_hi:[0,0,0]
	v_mfma_scale_f32_16x16x128_f8f6f4 v[106:109], v[196:203], v[172:179], v[106:109], v145, v145 op_sel_hi:[0,0,0]
	v_mfma_scale_f32_16x16x128_f8f6f4 v[98:101], v[204:211], v[172:179], v[98:101], v145, v145 op_sel_hi:[0,0,0]
	v_mfma_scale_f32_16x16x128_f8f6f4 v[172:175], v[196:203], v[180:187], v[90:93], v145, v145 op_sel_hi:[0,0,0]
	v_mfma_scale_f32_16x16x128_f8f6f4 v[176:179], v[204:211], v[180:187], v[82:85], v145, v145 op_sel_hi:[0,0,0]
	v_mfma_scale_f32_16x16x128_f8f6f4 v[180:183], v[196:203], v[188:195], v[74:77], v145, v145 op_sel_hi:[0,0,0]
	v_mfma_scale_f32_16x16x128_f8f6f4 v[184:187], v[204:211], v[188:195], v[10:13], v145, v145 op_sel_hi:[0,0,0]
	s_setprio 0
	v_lshl_add_u32 v137, s83, 2, v253
	s_barrier
	ds_read_b128 v[66:69], v144 offset:16384
	ds_read_b128 v[70:73], v144 offset:17408
	s_nop 0
	ds_read_b128 v[74:77], v144 offset:18432
	ds_read_b128 v[78:81], v144 offset:19456
	ds_read_b128 v[82:85], v144 offset:20480
	ds_read_b128 v[86:89], v144 offset:21504
	ds_read_b32 v10, v137
	ds_read_b128 v[90:93], v144 offset:22528
	ds_read_b128 v[94:97], v144 offset:23552
	s_add_u32 s44, s96, s82
	s_addc_u32 s45, s97, 0
	s_waitcnt lgkmcnt(0)
	v_add_u32_e32 v10, v10, v1
	s_mov_b32 m0, s56
	s_nop 0
	global_load_lds_dwordx4 v10, s[44:45]
	ds_read_b32 v10, v137 offset:256
	s_mov_b32 m0, s58
	s_waitcnt lgkmcnt(0)
	v_add_u32_e32 v10, v10, v1
	global_load_lds_dwordx4 v10, s[44:45]
	s_barrier
	s_waitcnt lgkmcnt(0)
	s_setprio 1
	v_mfma_scale_f32_16x16x128_f8f6f4 v[62:65], v[148:155], v[66:73], v[62:65], v145, v145 op_sel_hi:[0,0,0]
	v_mfma_scale_f32_16x16x128_f8f6f4 v[54:57], v[156:163], v[66:73], v[54:57], v145, v145 op_sel_hi:[0,0,0]
	v_mfma_scale_f32_16x16x128_f8f6f4 v[46:49], v[148:155], v[74:81], v[46:49], v145, v145 op_sel_hi:[0,0,0]
	v_mfma_scale_f32_16x16x128_f8f6f4 v[244:247], v[156:163], v[90:97], v[244:247], v145, v145 op_sel_hi:[0,0,0]
	v_mfma_scale_f32_16x16x128_f8f6f4 v[228:231], v[156:163], v[74:81], v[38:41], v145, v145 op_sel_hi:[0,0,0]
	v_mfma_scale_f32_16x16x128_f8f6f4 v[232:235], v[148:155], v[82:89], v[30:33], v145, v145 op_sel_hi:[0,0,0]
	v_mfma_scale_f32_16x16x128_f8f6f4 v[236:239], v[156:163], v[82:89], v[22:25], v145, v145 op_sel_hi:[0,0,0]
	v_mfma_scale_f32_16x16x128_f8f6f4 v[240:243], v[148:155], v[90:97], v[14:17], v145, v145 op_sel_hi:[0,0,0]
	s_setprio 0
	s_barrier
	s_add_i32 s48, s69, s55
	v_lshl_add_u64 v[10:11], v[134:135], 0, s[12:13]
	s_mov_b32 m0, s48
	s_nop 0
	global_load_lds_dwordx4 v[10:11], off
	v_lshl_add_u64 v[10:11], v[134:135], 0, s[14:15]
	s_add_i32 m0, s48, 0x2000
	s_nop 0
	global_load_lds_dwordx4 v[10:11], off
	s_waitcnt vmcnt(6)
	s_barrier
	s_setprio 1
	v_mfma_scale_f32_16x16x128_f8f6f4 v[58:61], v[196:203], v[66:73], v[58:61], v145, v145 op_sel_hi:[0,0,0]
	v_mfma_scale_f32_16x16x128_f8f6f4 v[50:53], v[204:211], v[66:73], v[50:53], v145, v145 op_sel_hi:[0,0,0]
	v_mfma_scale_f32_16x16x128_f8f6f4 v[42:45], v[196:203], v[74:81], v[42:45], v145, v145 op_sel_hi:[0,0,0]
	v_mfma_scale_f32_16x16x128_f8f6f4 v[248:251], v[204:211], v[74:81], v[34:37], v145, v145 op_sel_hi:[0,0,0]
	v_mfma_scale_f32_16x16x128_f8f6f4 v[138:141], v[196:203], v[82:89], v[26:29], v145, v145 op_sel_hi:[0,0,0]
	v_mfma_scale_f32_16x16x128_f8f6f4 v[66:69], v[204:211], v[82:89], v[18:21], v145, v145 op_sel_hi:[0,0,0]
	v_mfma_scale_f32_16x16x128_f8f6f4 v[70:73], v[196:203], v[90:97], v[6:9], v145, v145 op_sel_hi:[0,0,0]
	v_mfma_scale_f32_16x16x128_f8f6f4 v[208:211], v[204:211], v[90:97], v[2:5], v145, v145 op_sel_hi:[0,0,0]
	s_setprio 0
	s_add_i32 s48, 0, 0x18000
	v_add_u32_e32 v10, s48, v142
	s_barrier
	s_nop 2
	ds_read_b128 v[2:5], v10
	ds_read_b128 v[6:9], v10 offset:1024
	ds_read_b128 v[148:151], v10 offset:2048
	ds_read_b128 v[152:155], v10 offset:3072
	ds_read_b128 v[10:13], v144 offset:32768
	ds_read_b128 v[14:17], v144 offset:33792
	ds_read_b128 v[18:21], v144 offset:34816
	ds_read_b128 v[22:25], v144 offset:35840
	ds_read_b32 v74, v137 offset:512
	ds_read_b128 v[26:29], v144 offset:36864
	ds_read_b128 v[30:33], v144 offset:37888
	ds_read_b128 v[34:37], v144 offset:38912
	ds_read_b128 v[38:41], v144 offset:39936
	s_waitcnt lgkmcnt(0)
	v_add_u32_e32 v74, v74, v1
	s_mov_b32 m0, s59
	s_nop 0
	global_load_lds_dwordx4 v74, s[44:45]
	ds_read_b32 v74, v137 offset:768
	s_mov_b32 m0, s60
	s_waitcnt lgkmcnt(0)
	v_add_u32_e32 v74, v74, v1
	global_load_lds_dwordx4 v74, s[44:45]
	s_waitcnt lgkmcnt(8)
	s_barrier
	s_waitcnt lgkmcnt(0)
	s_setprio 1
	v_mfma_scale_f32_16x16x128_f8f6f4 v[126:129], v[2:9], v[10:17], v[126:129], v145, v145 op_sel_hi:[0,0,0]
	v_mfma_scale_f32_16x16x128_f8f6f4 v[118:121], v[148:155], v[10:17], v[118:121], v145, v145 op_sel_hi:[0,0,0]
	v_mfma_scale_f32_16x16x128_f8f6f4 v[110:113], v[2:9], v[18:25], v[110:113], v145, v145 op_sel_hi:[0,0,0]
	v_mfma_scale_f32_16x16x128_f8f6f4 v[102:105], v[148:155], v[18:25], v[102:105], v145, v145 op_sel_hi:[0,0,0]
	v_mfma_scale_f32_16x16x128_f8f6f4 v[94:97], v[2:9], v[26:33], v[212:215], v145, v145 op_sel_hi:[0,0,0]
	v_mfma_scale_f32_16x16x128_f8f6f4 v[86:89], v[148:155], v[26:33], v[216:219], v145, v145 op_sel_hi:[0,0,0]
	v_mfma_scale_f32_16x16x128_f8f6f4 v[78:81], v[2:9], v[34:41], v[220:223], v145, v145 op_sel_hi:[0,0,0]
	v_mfma_scale_f32_16x16x128_f8f6f4 v[204:207], v[148:155], v[34:41], v[224:227], v145, v145 op_sel_hi:[0,0,0]
	s_setprio 0
	s_barrier
	s_add_i32 s49, 0, 0x1c000
	v_add_u32_e32 v74, s49, v142
	s_add_i32 s48, s48, s55
	ds_read_b128 v[156:159], v74
	ds_read_b128 v[160:163], v74 offset:1024
	ds_read_b128 v[164:167], v74 offset:2048
	ds_read_b128 v[168:171], v74 offset:3072
	v_lshl_add_u64 v[74:75], v[134:135], 0, s[22:23]
	s_mov_b32 m0, s48
	s_nop 0
	global_load_lds_dwordx4 v[74:75], off
	v_lshl_add_u64 v[74:75], v[134:135], 0, s[24:25]
	s_add_i32 m0, s48, 0x2000
	s_nop 0
	global_load_lds_dwordx4 v[74:75], off
	s_barrier
	s_waitcnt lgkmcnt(0)
	s_setprio 1
	s_waitcnt lgkmcnt(0)
	v_mfma_scale_f32_16x16x128_f8f6f4 v[122:125], v[156:163], v[10:17], v[122:125], v145, v145 op_sel_hi:[0,0,0]
	v_mfma_scale_f32_16x16x128_f8f6f4 v[114:117], v[164:171], v[10:17], v[114:117], v145, v145 op_sel_hi:[0,0,0]
	v_mfma_scale_f32_16x16x128_f8f6f4 v[106:109], v[156:163], v[18:25], v[106:109], v145, v145 op_sel_hi:[0,0,0]
	v_mfma_scale_f32_16x16x128_f8f6f4 v[98:101], v[164:171], v[18:25], v[98:101], v145, v145 op_sel_hi:[0,0,0]
	v_mfma_scale_f32_16x16x128_f8f6f4 v[90:93], v[156:163], v[26:33], v[172:175], v145, v145 op_sel_hi:[0,0,0]
	v_mfma_scale_f32_16x16x128_f8f6f4 v[82:85], v[164:171], v[26:33], v[176:179], v145, v145 op_sel_hi:[0,0,0]
	v_mfma_scale_f32_16x16x128_f8f6f4 v[74:77], v[156:163], v[34:41], v[180:183], v145, v145 op_sel_hi:[0,0,0]
	v_mfma_scale_f32_16x16x128_f8f6f4 v[10:13], v[164:171], v[34:41], v[184:187], v145, v145 op_sel_hi:[0,0,0]
	s_setprio 0
	s_barrier
	s_nop 1
	ds_read_b128 v[172:175], v144 offset:49152
	ds_read_b128 v[176:179], v144 offset:50176
	ds_read_b128 v[180:183], v144 offset:51200
	ds_read_b128 v[184:187], v144 offset:52224
	ds_read_b32 v14, v137
	ds_read_b128 v[188:191], v144 offset:53248
	ds_read_b128 v[192:195], v144 offset:54272
	ds_read_b128 v[196:199], v144 offset:55296
	ds_read_b128 v[200:203], v144 offset:56320
	s_waitcnt lgkmcnt(0)
	v_add_u32_e32 v132, v14, v1
	v_lshl_add_u64 v[14:15], s[44:45], 0, v[132:133]
	v_lshl_add_u64 v[14:15], v[14:15], 0, s[22:23]
	s_mov_b32 m0, s62
	s_nop 0
	global_load_lds_dwordx4 v[14:15], off
	ds_read_b32 v14, v137 offset:256
	s_mov_b32 m0, s63
	s_waitcnt lgkmcnt(0)
	v_add_u32_e32 v132, v14, v1
	v_lshl_add_u64 v[14:15], s[44:45], 0, v[132:133]
	v_lshl_add_u64 v[14:15], v[14:15], 0, s[22:23]
	global_load_lds_dwordx4 v[14:15], off
	s_barrier
	s_waitcnt lgkmcnt(0)
	s_setprio 1
	v_mfma_scale_f32_16x16x128_f8f6f4 v[62:65], v[2:9], v[172:179], v[62:65], v145, v145 op_sel_hi:[0,0,0]
	v_mfma_scale_f32_16x16x128_f8f6f4 v[54:57], v[148:155], v[172:179], v[54:57], v145, v145 op_sel_hi:[0,0,0]
	v_mfma_scale_f32_16x16x128_f8f6f4 v[46:49], v[2:9], v[180:187], v[46:49], v145, v145 op_sel_hi:[0,0,0]
	v_mfma_scale_f32_16x16x128_f8f6f4 v[38:41], v[148:155], v[180:187], v[228:231], v145, v145 op_sel_hi:[0,0,0]
	v_mfma_scale_f32_16x16x128_f8f6f4 v[30:33], v[2:9], v[188:195], v[232:235], v145, v145 op_sel_hi:[0,0,0]
	v_mfma_scale_f32_16x16x128_f8f6f4 v[22:25], v[148:155], v[188:195], v[236:239], v145, v145 op_sel_hi:[0,0,0]
	v_mfma_scale_f32_16x16x128_f8f6f4 v[14:17], v[2:9], v[196:203], v[240:243], v145, v145 op_sel_hi:[0,0,0]
	v_mfma_scale_f32_16x16x128_f8f6f4 v[244:247], v[148:155], v[196:203], v[244:247], v145, v145 op_sel_hi:[0,0,0]
	s_setprio 0
	s_barrier
	s_add_i32 s44, s49, s55
	v_lshl_add_u64 v[2:3], v[134:135], 0, s[28:29]
	s_mov_b32 m0, s44
	s_nop 0
	global_load_lds_dwordx4 v[2:3], off
	v_lshl_add_u64 v[2:3], v[134:135], 0, s[30:31]
	s_add_i32 m0, s44, 0x2000
	s_nop 0
	global_load_lds_dwordx4 v[2:3], off
	s_waitcnt vmcnt(6)
	s_barrier
	s_setprio 1
	v_mfma_scale_f32_16x16x128_f8f6f4 v[58:61], v[156:163], v[172:179], v[58:61], v145, v145 op_sel_hi:[0,0,0]
	v_mfma_scale_f32_16x16x128_f8f6f4 v[50:53], v[164:171], v[172:179], v[50:53], v145, v145 op_sel_hi:[0,0,0]
	v_mfma_scale_f32_16x16x128_f8f6f4 v[42:45], v[156:163], v[180:187], v[42:45], v145, v145 op_sel_hi:[0,0,0]
	v_mfma_scale_f32_16x16x128_f8f6f4 v[34:37], v[164:171], v[180:187], v[248:251], v145, v145 op_sel_hi:[0,0,0]
	v_mfma_scale_f32_16x16x128_f8f6f4 v[26:29], v[156:163], v[188:195], v[138:141], v145, v145 op_sel_hi:[0,0,0]
	v_mfma_scale_f32_16x16x128_f8f6f4 v[18:21], v[164:171], v[188:195], v[66:69], v145, v145 op_sel_hi:[0,0,0]
	v_mfma_scale_f32_16x16x128_f8f6f4 v[6:9], v[156:163], v[196:203], v[70:73], v145, v145 op_sel_hi:[0,0,0]
	v_mfma_scale_f32_16x16x128_f8f6f4 v[2:5], v[164:171], v[196:203], v[208:211], v145, v145 op_sel_hi:[0,0,0]
	s_setprio 0
	s_add_i32 s81, s81, 2
	s_cmp_gt_u32 s81, 13
	s_mov_b64 s[44:45], s[46:47]
	s_barrier
	s_cbranch_scc0 .LBB0_1609
	v_mov_b32_e32 v151, v0
	s_lshl_b32 s44, s78, 8
	v_mov_b32_e32 v138, 0
	v_ashrrev_i32_e32 v153, 8, v151
	v_and_b32_e32 v149, 15, v151
	v_lshlrev_b32_e32 v152, 6, v153
	v_or_b32_e32 v136, v152, v149
	v_bfe_u32 v150, v151, 6, 2
	v_bfe_u32 v154, v151, 4, 2
	v_add_u32_e32 v66, s44, v136
	v_cmp_lt_i32_e32 vcc, v66, v252
	v_ashrrev_i32_e32 v137, 31, v136
	v_or3_b32 v148, v150, s2, v154
	v_mov_b32_e32 v140, 0
	s_ashr_i32 s9, s8, 31
	s_ashr_i32 s45, s44, 31
	s_lshl_b64 s[48:49], s[8:9], 16
	s_add_u32 s3, s51, s48
	s_addc_u32 s9, s52, s49
	s_lshl_b64 s[48:49], s[44:45], 2
	s_add_u32 s48, s3, s48
	s_addc_u32 s49, s9, s49
	v_lshl_add_u64 v[176:177], v[136:137], 2, s[48:49]
	v_add_u32_e32 v179, s44, v136
	s_mov_b64 s[46:47], exec
	v_add_u32_e32 v178, 0, v179
	v_cmp_lt_i32_e32 vcc, v178, v252
	s_and_b64 exec, s[46:47], vcc
	global_load_dword v160, v[176:177], off
	v_add_u32_e32 v178, 16, v179
	v_cmp_lt_i32_e32 vcc, v178, v252
	s_and_b64 exec, s[46:47], vcc
	global_load_dword v161, v[176:177], off offset:64
	v_add_u32_e32 v178, 32, v179
	v_cmp_lt_i32_e32 vcc, v178, v252
	s_and_b64 exec, s[46:47], vcc
	global_load_dword v162, v[176:177], off offset:128
	v_add_u32_e32 v178, 48, v179
	v_cmp_lt_i32_e32 vcc, v178, v252
	s_and_b64 exec, s[46:47], vcc
	global_load_dword v163, v[176:177], off offset:192
	v_add_u32_e32 v178, 128, v179
	v_cmp_lt_i32_e32 vcc, v178, v252
	s_and_b64 exec, s[46:47], vcc
	global_load_dword v164, v[176:177], off offset:512
	v_add_u32_e32 v178, 144, v179
	v_cmp_lt_i32_e32 vcc, v178, v252
	s_and_b64 exec, s[46:47], vcc
	global_load_dword v165, v[176:177], off offset:576
	v_add_u32_e32 v178, 160, v179
	v_cmp_lt_i32_e32 vcc, v178, v252
	s_and_b64 exec, s[46:47], vcc
	global_load_dword v166, v[176:177], off offset:640
	v_add_u32_e32 v178, 176, v179
	v_cmp_lt_i32_e32 vcc, v178, v252
	s_and_b64 exec, s[46:47], vcc
	global_load_dword v167, v[176:177], off offset:704
	s_mov_b64 exec, s[46:47]
	s_waitcnt vmcnt(0)
	v_add_u32_e32 v178, 0, v179
	v_cmp_lt_i32_e32 vcc, v178, v252
	s_and_b64 exec, s[46:47], vcc
	v_lshrrev_b32_e32 v180, 1, v160
	v_mov_b32_e32 v181, v133
	v_lshl_add_u64 v[180:181], v[180:181], 2, s[18:19]
	global_load_dword v168, v[180:181], off
	v_add_u32_e32 v178, 16, v179
	v_cmp_lt_i32_e32 vcc, v178, v252
	s_and_b64 exec, s[46:47], vcc
	v_lshrrev_b32_e32 v180, 1, v161
	v_mov_b32_e32 v181, v133
	v_lshl_add_u64 v[180:181], v[180:181], 2, s[18:19]
	global_load_dword v169, v[180:181], off
	v_add_u32_e32 v178, 32, v179
	v_cmp_lt_i32_e32 vcc, v178, v252
	s_and_b64 exec, s[46:47], vcc
	v_lshrrev_b32_e32 v180, 1, v162
	v_mov_b32_e32 v181, v133
	v_lshl_add_u64 v[180:181], v[180:181], 2, s[18:19]
	global_load_dword v170, v[180:181], off
	v_add_u32_e32 v178, 48, v179
	v_cmp_lt_i32_e32 vcc, v178, v252
	s_and_b64 exec, s[46:47], vcc
	v_lshrrev_b32_e32 v180, 1, v163
	v_mov_b32_e32 v181, v133
	v_lshl_add_u64 v[180:181], v[180:181], 2, s[18:19]
	global_load_dword v171, v[180:181], off
	v_add_u32_e32 v178, 128, v179
	v_cmp_lt_i32_e32 vcc, v178, v252
	s_and_b64 exec, s[46:47], vcc
	v_lshrrev_b32_e32 v180, 1, v164
	v_mov_b32_e32 v181, v133
	v_lshl_add_u64 v[180:181], v[180:181], 2, s[18:19]
	global_load_dword v172, v[180:181], off
	v_add_u32_e32 v178, 144, v179
	v_cmp_lt_i32_e32 vcc, v178, v252
	s_and_b64 exec, s[46:47], vcc
	v_lshrrev_b32_e32 v180, 1, v165
	v_mov_b32_e32 v181, v133
	v_lshl_add_u64 v[180:181], v[180:181], 2, s[18:19]
	global_load_dword v173, v[180:181], off
	v_add_u32_e32 v178, 160, v179
	v_cmp_lt_i32_e32 vcc, v178, v252
	s_and_b64 exec, s[46:47], vcc
	v_lshrrev_b32_e32 v180, 1, v166
	v_mov_b32_e32 v181, v133
	v_lshl_add_u64 v[180:181], v[180:181], 2, s[18:19]
	global_load_dword v174, v[180:181], off
	v_add_u32_e32 v178, 176, v179
	v_cmp_lt_i32_e32 vcc, v178, v252
	s_and_b64 exec, s[46:47], vcc
	v_lshrrev_b32_e32 v180, 1, v167
	v_mov_b32_e32 v181, v133
	v_lshl_add_u64 v[180:181], v[180:181], 2, s[18:19]
	global_load_dword v175, v[180:181], off
	s_mov_b64 exec, s[46:47]
	s_waitcnt vmcnt(0)
	v_cmp_lt_i32_e32 vcc, v66, v252
	s_and_saveexec_b64 s[46:47], vcc
	s_cbranch_execz .LBB0_1614
	s_ashr_i32 s9, s8, 31
	s_ashr_i32 s45, s44, 31
	s_lshl_b64 s[48:49], s[8:9], 16
	s_add_u32 s3, s51, s48
	s_addc_u32 s9, s52, s49
	s_lshl_b64 s[48:49], s[44:45], 2
	s_add_u32 s48, s3, s48
	s_addc_u32 s49, s9, s49
	v_lshl_add_u64 v[66:67], v[136:137], 2, s[48:49]
	v_mov_b32_e32 v134, v160
	v_cmp_eq_u32_e32 vcc, 0, v148
	v_lshrrev_b32_e32 v132, 1, v134
	v_lshl_add_u64 v[66:67], v[132:133], 2, s[18:19]
	v_mov_b32_e32 v132, v168
	s_and_saveexec_b64 s[48:49], vcc
	s_cbranch_execz .LBB0_1613
	v_mov_b32_e32 v135, v133
	v_add_u32_e32 v68, s57, v136
	v_lshl_add_u64 v[66:67], v[134:135], 2, s[20:21]
	global_store_dword v[66:67], v68, off
.LBB0_1613:
	s_or_b64 exec, exec, s[48:49]
	v_mul_f32_e32 v140, 0x3d000000, v132
.LBB0_1614:
	s_or_b64 exec, exec, s[46:47]
	v_lshlrev_b32_e32 v141, 2, v154
	v_pk_mul_f32 v[68:69], v[126:127], v[140:141] op_sel_hi:[1,0]
	v_pk_mul_f32 v[70:71], v[124:125], v[140:141] op_sel_hi:[1,0]
	v_mul_f32_e32 v72, 0xbfb8aa3b, v68
	v_exp_f32_e32 v124, v72
	v_lshl_or_b32 v66, v153, 2, v150
	v_mul_lo_u32 v66, v66, s70
	v_add_u32_e32 v139, s71, v66
	v_lshlrev_b32_e32 v66, 3, v149
	v_mul_f32_e32 v72, 0xbfb8aa3b, v69
	v_and_b32_e32 v132, 24, v66
	v_pk_mul_f32 v[66:67], v[128:129], v[140:141] op_sel_hi:[1,0]
	v_exp_f32_e32 v125, v72
	v_pk_mul_f32 v[72:73], v[122:123], v[140:141] op_sel_hi:[1,0]
	v_add_f32_e32 v122, 1.0, v124
	v_rcp_f32_e32 v122, v122
	v_mul_f32_e32 v124, 0xbfb8aa3b, v66
	v_exp_f32_e32 v124, v124
	v_add_f32_e32 v123, 1.0, v125
	v_mul_f32_e32 v68, v68, v122
	v_mul_f32_e32 v68, v72, v68
	v_add_f32_e32 v72, 1.0, v124
	v_rcp_f32_e32 v123, v123
	v_rcp_f32_e32 v72, v72
	v_mul_f32_e32 v122, 0xbfb8aa3b, v67
	v_exp_f32_e32 v122, v122
	v_mul_f32_e32 v69, v69, v123
	v_mul_f32_e32 v66, v66, v72
	v_mul_f32_e32 v69, v73, v69
	v_mul_f32_e32 v66, v70, v66
	v_add_f32_e32 v70, 1.0, v122
	v_mov_b32_e32 v122, v133
	v_rcp_f32_e32 v70, v70
	v_cvt_pk_fp8_f32 v122, v68, v69
	v_pk_mul_f32 v[68:69], v[118:119], v[140:141] op_sel_hi:[1,0]
	v_bfe_u32 v151, v151, 2, 4
	v_mul_f32_e32 v72, 0xbfb8aa3b, v68
	v_exp_f32_e32 v72, v72
	v_mul_f32_e32 v67, v67, v70
	v_mul_f32_e32 v67, v71, v67
	v_cvt_pk_fp8_f32 v122, v66, v67 op_sel:[0,0,1]
	v_add_f32_e32 v66, 1.0, v72
	v_rcp_f32_e32 v118, v66
	v_pk_mul_f32 v[66:67], v[120:121], v[140:141] op_sel_hi:[1,0]
	v_pk_mul_f32 v[72:73], v[114:115], v[140:141] op_sel_hi:[1,0]
	v_mul_f32_e32 v114, 0xbfb8aa3b, v69
	v_mul_f32_e32 v115, 0xbfb8aa3b, v66
	v_exp_f32_e32 v114, v114
	v_exp_f32_e32 v115, v115
	v_mul_f32_e32 v68, v68, v118
	v_mul_f32_e32 v68, v72, v68
	v_add_f32_e32 v72, 1.0, v114
	v_add_f32_e32 v114, 1.0, v115
	v_mul_f32_e32 v115, 0xbfb8aa3b, v67
	v_rcp_f32_e32 v72, v72
	v_exp_f32_e32 v115, v115
	v_rcp_f32_e32 v114, v114
	v_pk_mul_f32 v[70:71], v[116:117], v[140:141] op_sel_hi:[1,0]
	v_mul_f32_e32 v69, v69, v72
	v_add_f32_e32 v72, 1.0, v115
	v_rcp_f32_e32 v72, v72
	v_mul_f32_e32 v69, v73, v69
	v_mov_b32_e32 v73, v133
	v_cvt_pk_fp8_f32 v73, v68, v69
	v_mul_f32_e32 v66, v66, v114
	v_mul_f32_e32 v67, v67, v72
	v_mul_f32_e32 v66, v70, v66
	v_mul_f32_e32 v67, v71, v67
	v_cvt_pk_fp8_f32 v73, v66, v67 op_sel:[0,0,1]
	v_or_b32_e32 v152, v151, v152
	v_mad_u32_u24 v66, v149, 40, v139
	v_add_u32_e32 v119, v66, v141
	v_mad_u32_u24 v66, v151, 40, v139
	v_add_u32_e32 v114, s57, v152
	ds_write2_b32 v119, v122, v73 offset1:4
	v_add_u32_e32 v118, v66, v132
	v_ashrrev_i32_e32 v115, 31, v114
	ds_read_b64 v[66:67], v118
	v_lshlrev_b64 v[68:69], 9, v[114:115]
	s_lshl_b32 s2, s2, 7
	v_lshl_add_u64 v[68:69], s[16:17], 0, v[68:69]
	s_ashr_i32 s3, s2, 31
	v_lshlrev_b32_e32 v134, 5, v150
	v_mov_b32_e32 v135, v133
	v_lshl_add_u64 v[68:69], v[68:69], 0, s[2:3]
	v_lshl_add_u64 v[68:69], v[68:69], 0, v[134:135]
	v_lshl_add_u64 v[68:69], v[68:69], 0, v[132:133]
	v_or_b32_e32 v115, 16, v136
	s_waitcnt lgkmcnt(0)
	global_store_dwordx2 v[68:69], v[66:67], off
	v_add_u32_e32 v66, s44, v115
	v_cmp_lt_i32_e32 vcc, v66, v252
	s_and_saveexec_b64 s[46:47], vcc
	s_cbranch_execz .LBB0_1618
	s_ashr_i32 s9, s8, 31
	s_ashr_i32 s45, s44, 31
	s_lshl_b64 s[48:49], s[8:9], 16
	s_add_u32 s9, s51, s48
	s_addc_u32 s37, s52, s49
	s_lshl_b64 s[48:49], s[44:45], 2
	s_add_u32 s48, s9, s48
	s_addc_u32 s49, s37, s49
	v_lshl_add_u64 v[66:67], v[136:137], 2, s[48:49]
	v_mov_b32_e32 v116, v161
	v_mov_b32_e32 v67, v133
	v_cmp_eq_u32_e32 vcc, 0, v148
	v_lshrrev_b32_e32 v66, 1, v116
	v_lshl_add_u64 v[66:67], v[66:67], 2, s[18:19]
	v_mov_b32_e32 v120, v169
	s_and_saveexec_b64 s[48:49], vcc
	s_cbranch_execz .LBB0_1617
	v_mov_b32_e32 v117, v133
	v_add_u32_e32 v68, s57, v115
	v_lshl_add_u64 v[66:67], v[116:117], 2, s[20:21]
	global_store_dword v[66:67], v68, off
.LBB0_1617:
	s_or_b64 exec, exec, s[48:49]
	v_mul_f32_e32 v138, 0x3d000000, v120
.LBB0_1618:
	s_or_b64 exec, exec, s[46:47]
	v_pk_mul_f32 v[68:69], v[110:111], v[138:139] op_sel_hi:[1,0]
	v_pk_mul_f32 v[70:71], v[108:109], v[138:139] op_sel_hi:[1,0]
	v_mul_f32_e32 v72, 0xbfb8aa3b, v68
	v_exp_f32_e32 v108, v72
	v_mul_f32_e32 v72, 0xbfb8aa3b, v69
	v_pk_mul_f32 v[66:67], v[112:113], v[138:139] op_sel_hi:[1,0]
	v_exp_f32_e32 v109, v72
	v_pk_mul_f32 v[72:73], v[106:107], v[138:139] op_sel_hi:[1,0]
	v_add_f32_e32 v106, 1.0, v108
	v_rcp_f32_e32 v106, v106
	v_mul_f32_e32 v108, 0xbfb8aa3b, v66
	v_exp_f32_e32 v108, v108
	v_add_f32_e32 v107, 1.0, v109
	v_mul_f32_e32 v68, v68, v106
	v_mul_f32_e32 v68, v72, v68
	v_add_f32_e32 v72, 1.0, v108
	v_rcp_f32_e32 v107, v107
	v_rcp_f32_e32 v72, v72
	v_mul_f32_e32 v106, 0xbfb8aa3b, v67
	v_exp_f32_e32 v106, v106
	v_mul_f32_e32 v69, v69, v107
	v_mul_f32_e32 v66, v66, v72
	v_mul_f32_e32 v69, v73, v69
	v_mul_f32_e32 v66, v70, v66
	v_add_f32_e32 v70, 1.0, v106
	v_mov_b32_e32 v106, v133
	v_rcp_f32_e32 v70, v70
	v_cvt_pk_fp8_f32 v106, v68, v69
	v_pk_mul_f32 v[68:69], v[102:103], v[138:139] op_sel_hi:[1,0]
	v_mul_f32_e32 v67, v67, v70
	v_mul_f32_e32 v72, 0xbfb8aa3b, v68
	v_exp_f32_e32 v72, v72
	v_mul_f32_e32 v67, v71, v67
	v_cvt_pk_fp8_f32 v106, v66, v67 op_sel:[0,0,1]
	v_pk_mul_f32 v[70:71], v[100:101], v[138:139] op_sel_hi:[1,0]
	v_add_f32_e32 v66, 1.0, v72
	v_rcp_f32_e32 v102, v66
	v_pk_mul_f32 v[66:67], v[104:105], v[138:139] op_sel_hi:[1,0]
	v_pk_mul_f32 v[72:73], v[98:99], v[138:139] op_sel_hi:[1,0]
	v_mul_f32_e32 v98, 0xbfb8aa3b, v69
	v_mul_f32_e32 v99, 0xbfb8aa3b, v66
	v_exp_f32_e32 v98, v98
	v_exp_f32_e32 v99, v99
	v_mul_f32_e32 v68, v68, v102
	v_mul_f32_e32 v68, v72, v68
	v_add_f32_e32 v72, 1.0, v98
	v_add_f32_e32 v98, 1.0, v99
	v_mul_f32_e32 v99, 0xbfb8aa3b, v67
	v_rcp_f32_e32 v72, v72
	v_exp_f32_e32 v99, v99
	v_rcp_f32_e32 v98, v98
	v_or_b32_e32 v101, 32, v136
	v_mul_f32_e32 v69, v69, v72
	v_add_f32_e32 v72, 1.0, v99
	v_rcp_f32_e32 v72, v72
	v_mul_f32_e32 v69, v73, v69
	v_mov_b32_e32 v73, v133
	v_cvt_pk_fp8_f32 v73, v68, v69
	v_mul_f32_e32 v66, v66, v98
	v_mul_f32_e32 v67, v67, v72
	v_mul_f32_e32 v66, v70, v66
	v_mul_f32_e32 v67, v71, v67
	v_cvt_pk_fp8_f32 v73, v66, v67 op_sel:[0,0,1]
	v_add_u32_e32 v99, 0x400, v119
	v_add_u32_e32 v68, 16, v114
	v_ashrrev_i32_e32 v69, 31, v68
	ds_write2_b32 v99, v106, v73 offset0:64 offset1:68
	ds_read_b64 v[66:67], v118 offset:1280
	v_lshlrev_b64 v[68:69], 9, v[68:69]
	v_lshl_add_u64 v[68:69], s[16:17], 0, v[68:69]
	v_lshl_add_u64 v[68:69], v[68:69], 0, s[2:3]
	v_lshl_add_u64 v[68:69], v[68:69], 0, v[134:135]
	v_lshl_add_u64 v[68:69], v[68:69], 0, v[132:133]
	s_waitcnt lgkmcnt(0)
	global_store_dwordx2 v[68:69], v[66:67], off
	v_add_u32_e32 v66, s44, v101
	v_cmp_lt_i32_e32 vcc, v66, v252
	v_mov_b32_e32 v98, 0
	v_mov_b32_e32 v100, 0
	s_and_saveexec_b64 s[46:47], vcc
	s_cbranch_execz .LBB0_1622
	s_ashr_i32 s9, s8, 31
	s_ashr_i32 s45, s44, 31
	s_lshl_b64 s[48:49], s[8:9], 16
	s_add_u32 s9, s51, s48
	s_addc_u32 s37, s52, s49
	s_lshl_b64 s[48:49], s[44:45], 2
	s_add_u32 s48, s9, s48
	s_addc_u32 s49, s37, s49
	v_lshl_add_u64 v[66:67], v[136:137], 2, s[48:49]
	v_mov_b32_e32 v100, v162
	v_mov_b32_e32 v67, v133
	v_cmp_eq_u32_e32 vcc, 0, v148
	v_lshrrev_b32_e32 v66, 1, v100
	v_lshl_add_u64 v[66:67], v[66:67], 2, s[18:19]
	v_mov_b32_e32 v102, v170
	s_and_saveexec_b64 s[48:49], vcc
	s_cbranch_execz .LBB0_1621
	v_add_u32_e32 v68, s57, v101
	v_mov_b32_e32 v101, v133
	v_lshl_add_u64 v[66:67], v[100:101], 2, s[20:21]
	global_store_dword v[66:67], v68, off
.LBB0_1621:
	s_or_b64 exec, exec, s[48:49]
	v_mul_f32_e32 v100, 0x3d000000, v102
.LBB0_1622:
	s_or_b64 exec, exec, s[46:47]
	v_pk_mul_f32 v[68:69], v[94:95], v[100:101] op_sel_hi:[1,0]
	v_pk_mul_f32 v[70:71], v[92:93], v[100:101] op_sel_hi:[1,0]
	v_mul_f32_e32 v72, 0xbfb8aa3b, v68
	v_exp_f32_e32 v92, v72
	v_mul_f32_e32 v72, 0xbfb8aa3b, v69
	v_pk_mul_f32 v[66:67], v[96:97], v[100:101] op_sel_hi:[1,0]
	v_exp_f32_e32 v93, v72
	v_pk_mul_f32 v[72:73], v[90:91], v[100:101] op_sel_hi:[1,0]
	v_add_f32_e32 v90, 1.0, v92
	v_rcp_f32_e32 v90, v90
	v_mul_f32_e32 v92, 0xbfb8aa3b, v66
	v_exp_f32_e32 v92, v92
	v_add_f32_e32 v91, 1.0, v93
	v_mul_f32_e32 v68, v68, v90
	v_mul_f32_e32 v68, v72, v68
	v_add_f32_e32 v72, 1.0, v92
	v_rcp_f32_e32 v91, v91
	v_rcp_f32_e32 v72, v72
	v_mul_f32_e32 v90, 0xbfb8aa3b, v67
	v_exp_f32_e32 v90, v90
	v_mul_f32_e32 v69, v69, v91
	v_mul_f32_e32 v66, v66, v72
	v_mul_f32_e32 v69, v73, v69
	v_mul_f32_e32 v66, v70, v66
	v_add_f32_e32 v70, 1.0, v90
	v_mov_b32_e32 v90, v133
	v_rcp_f32_e32 v70, v70
	v_cvt_pk_fp8_f32 v90, v68, v69
	v_pk_mul_f32 v[68:69], v[86:87], v[100:101] op_sel_hi:[1,0]
	v_mul_f32_e32 v67, v67, v70
	v_mul_f32_e32 v72, 0xbfb8aa3b, v68
	v_exp_f32_e32 v72, v72
	v_mul_f32_e32 v67, v71, v67
	v_cvt_pk_fp8_f32 v90, v66, v67 op_sel:[0,0,1]
	v_pk_mul_f32 v[70:71], v[84:85], v[100:101] op_sel_hi:[1,0]
	v_add_f32_e32 v66, 1.0, v72
	v_rcp_f32_e32 v86, v66
	v_pk_mul_f32 v[66:67], v[88:89], v[100:101] op_sel_hi:[1,0]
	v_pk_mul_f32 v[72:73], v[82:83], v[100:101] op_sel_hi:[1,0]
	v_mul_f32_e32 v82, 0xbfb8aa3b, v69
	v_mul_f32_e32 v83, 0xbfb8aa3b, v66
	v_exp_f32_e32 v82, v82
	v_exp_f32_e32 v83, v83
	v_mul_f32_e32 v68, v68, v86
	v_mul_f32_e32 v68, v72, v68
	v_add_f32_e32 v72, 1.0, v82
	v_add_f32_e32 v82, 1.0, v83
	v_mul_f32_e32 v83, 0xbfb8aa3b, v67
	v_rcp_f32_e32 v72, v72
	v_exp_f32_e32 v83, v83
	v_rcp_f32_e32 v82, v82
	v_mul_f32_e32 v69, v69, v72
	v_add_f32_e32 v72, 1.0, v83
	v_rcp_f32_e32 v72, v72
	v_mul_f32_e32 v69, v73, v69
	v_mov_b32_e32 v73, v133
	v_cvt_pk_fp8_f32 v73, v68, v69
	v_mul_f32_e32 v66, v66, v82
	v_mul_f32_e32 v67, v67, v72
	v_mul_f32_e32 v66, v70, v66
	v_mul_f32_e32 v67, v71, v67
	v_cvt_pk_fp8_f32 v73, v66, v67 op_sel:[0,0,1]
	v_add_u32_e32 v68, 32, v114
	v_ashrrev_i32_e32 v69, 31, v68
	v_lshlrev_b64 v[68:69], 9, v[68:69]
	ds_write2_b32 v119, v90, v73 offset1:4
	ds_read_b64 v[66:67], v118
	v_lshl_add_u64 v[68:69], s[16:17], 0, v[68:69]
	v_lshl_add_u64 v[68:69], v[68:69], 0, s[2:3]
	v_lshl_add_u64 v[68:69], v[68:69], 0, v[134:135]
	v_lshl_add_u64 v[68:69], v[68:69], 0, v[132:133]
	v_or_b32_e32 v83, 48, v136
	s_waitcnt lgkmcnt(0)
	global_store_dwordx2 v[68:69], v[66:67], off
	v_add_u32_e32 v66, s44, v83
	v_cmp_lt_i32_e32 vcc, v66, v252
	s_and_saveexec_b64 s[46:47], vcc
	s_cbranch_execz .LBB0_1626
	s_ashr_i32 s9, s8, 31
	s_ashr_i32 s45, s44, 31
	s_lshl_b64 s[48:49], s[8:9], 16
	s_add_u32 s9, s51, s48
	s_addc_u32 s37, s52, s49
	s_lshl_b64 s[48:49], s[44:45], 2
	s_add_u32 s48, s9, s48
	s_addc_u32 s49, s37, s49
	v_lshl_add_u64 v[66:67], v[136:137], 2, s[48:49]
	v_mov_b32_e32 v82, v163
	v_mov_b32_e32 v67, v133
	v_cmp_eq_u32_e32 vcc, 0, v148
	v_lshrrev_b32_e32 v66, 1, v82
	v_lshl_add_u64 v[66:67], v[66:67], 2, s[18:19]
	v_mov_b32_e32 v84, v171
	s_and_saveexec_b64 s[48:49], vcc
	s_cbranch_execz .LBB0_1625
	v_add_u32_e32 v68, s57, v83
	v_mov_b32_e32 v83, v133
	v_lshl_add_u64 v[66:67], v[82:83], 2, s[20:21]
	global_store_dword v[66:67], v68, off
.LBB0_1625:
	s_or_b64 exec, exec, s[48:49]
	v_mul_f32_e32 v98, 0x3d000000, v84
.LBB0_1626:
	s_or_b64 exec, exec, s[46:47]
	v_pk_mul_f32 v[68:69], v[78:79], v[98:99] op_sel_hi:[1,0]
	v_pk_mul_f32 v[70:71], v[76:77], v[98:99] op_sel_hi:[1,0]
	v_mul_f32_e32 v72, 0xbfb8aa3b, v68
	v_exp_f32_e32 v76, v72
	v_mul_f32_e32 v72, 0xbfb8aa3b, v69
	v_pk_mul_f32 v[66:67], v[80:81], v[98:99] op_sel_hi:[1,0]
	v_exp_f32_e32 v77, v72
	v_pk_mul_f32 v[72:73], v[74:75], v[98:99] op_sel_hi:[1,0]
	v_add_f32_e32 v74, 1.0, v76
	v_rcp_f32_e32 v74, v74
	v_mul_f32_e32 v76, 0xbfb8aa3b, v66
	v_exp_f32_e32 v76, v76
	v_add_f32_e32 v75, 1.0, v77
	v_mul_f32_e32 v68, v68, v74
	v_mul_f32_e32 v68, v72, v68
	v_add_f32_e32 v72, 1.0, v76
	v_rcp_f32_e32 v75, v75
	v_rcp_f32_e32 v72, v72
	v_mul_f32_e32 v74, 0xbfb8aa3b, v67
	v_exp_f32_e32 v74, v74
	v_mul_f32_e32 v69, v69, v75
	v_mul_f32_e32 v66, v66, v72
	v_mul_f32_e32 v69, v73, v69
	v_mul_f32_e32 v66, v70, v66
	v_add_f32_e32 v70, 1.0, v74
	v_mov_b32_e32 v72, v133
	v_rcp_f32_e32 v70, v70
	v_cvt_pk_fp8_f32 v72, v68, v69
	v_pk_mul_f32 v[68:69], v[204:205], v[98:99] op_sel_hi:[1,0]
	v_pk_mul_f32 v[10:11], v[10:11], v[98:99] op_sel_hi:[1,0]
	v_mul_f32_e32 v73, 0xbfb8aa3b, v68
	v_exp_f32_e32 v73, v73
	v_mul_f32_e32 v67, v67, v70
	v_mul_f32_e32 v67, v71, v67
	v_cvt_pk_fp8_f32 v72, v66, v67 op_sel:[0,0,1]
	v_add_f32_e32 v66, 1.0, v73
	v_rcp_f32_e32 v70, v66
	v_pk_mul_f32 v[66:67], v[206:207], v[98:99] op_sel_hi:[1,0]
	v_pk_mul_f32 v[12:13], v[12:13], v[98:99] op_sel_hi:[1,0]
	v_mul_f32_e32 v71, 0xbfb8aa3b, v66
	v_mul_f32_e32 v68, v68, v70
	v_mul_f32_e32 v70, 0xbfb8aa3b, v69
	v_exp_f32_e32 v70, v70
	v_exp_f32_e32 v71, v71
	v_mul_f32_e32 v10, v10, v68
	v_add_f32_e32 v68, 1.0, v70
	v_rcp_f32_e32 v68, v68
	v_add_f32_e32 v70, 1.0, v71
	v_mul_f32_e32 v71, 0xbfb8aa3b, v67
	v_exp_f32_e32 v71, v71
	v_mul_f32_e32 v68, v69, v68
	v_mul_f32_e32 v11, v11, v68
	v_rcp_f32_e32 v70, v70
	v_add_f32_e32 v68, 1.0, v71
	v_rcp_f32_e32 v68, v68
	v_mov_b32_e32 v69, v133
	v_cvt_pk_fp8_f32 v69, v10, v11
	v_mul_f32_e32 v66, v66, v70
	v_mul_f32_e32 v11, v67, v68
	v_mul_f32_e32 v10, v12, v66
	v_mul_f32_e32 v11, v13, v11
	v_cvt_pk_fp8_f32 v69, v10, v11 op_sel:[0,0,1]
	v_add_u32_e32 v12, 48, v114
	v_ashrrev_i32_e32 v13, 31, v12
	v_lshlrev_b64 v[12:13], 9, v[12:13]
	ds_write2_b32 v99, v72, v69 offset0:64 offset1:68
	ds_read_b64 v[10:11], v118 offset:1280
	v_lshl_add_u64 v[12:13], s[16:17], 0, v[12:13]
	v_lshl_add_u64 v[12:13], v[12:13], 0, s[2:3]
	v_lshl_add_u64 v[12:13], v[12:13], 0, v[134:135]
	v_lshl_add_u64 v[12:13], v[12:13], 0, v[132:133]
	v_add_u32_e32 v67, 0x80, v136
	s_waitcnt lgkmcnt(0)
	global_store_dwordx2 v[12:13], v[10:11], off
	v_add_u32_e32 v10, s44, v67
	v_cmp_lt_i32_e32 vcc, v10, v252
	v_mov_b32_e32 v66, 0
	v_mov_b32_e32 v68, 0
	s_and_saveexec_b64 s[46:47], vcc
	s_cbranch_execz .LBB0_1630
	s_ashr_i32 s9, s8, 31
	s_ashr_i32 s45, s44, 31
	s_lshl_b64 s[48:49], s[8:9], 16
	s_add_u32 s9, s51, s48
	s_addc_u32 s37, s52, s49
	s_lshl_b64 s[48:49], s[44:45], 2
	s_add_u32 s48, s9, s48
	s_addc_u32 s49, s37, s49
	v_lshl_add_u64 v[10:11], v[136:137], 2, s[48:49]
	v_mov_b32_e32 v68, v164
	v_mov_b32_e32 v11, v133
	v_cmp_eq_u32_e32 vcc, 0, v148
	v_lshrrev_b32_e32 v10, 1, v68
	v_lshl_add_u64 v[10:11], v[10:11], 2, s[18:19]
	v_mov_b32_e32 v70, v172
	s_and_saveexec_b64 s[48:49], vcc
	s_cbranch_execz .LBB0_1629
	v_mov_b32_e32 v69, v133
	v_add_u32_e32 v12, s57, v67
	v_lshl_add_u64 v[10:11], v[68:69], 2, s[20:21]
	global_store_dword v[10:11], v12, off
.LBB0_1629:
	s_or_b64 exec, exec, s[48:49]
	v_mul_f32_e32 v68, 0x3d000000, v70
.LBB0_1630:
	s_or_b64 exec, exec, s[46:47]
	v_pk_mul_f32 v[12:13], v[62:63], v[68:69] op_sel_hi:[1,0]
	v_pk_mul_f32 v[10:11], v[64:65], v[68:69] op_sel_hi:[1,0]
	v_mul_f32_e32 v62, 0xbfb8aa3b, v12
	v_exp_f32_e32 v62, v62
	v_mul_f32_e32 v63, 0xbfb8aa3b, v13
	v_exp_f32_e32 v63, v63
	v_mul_f32_e32 v64, 0xbfb8aa3b, v10
	v_add_f32_e32 v62, 1.0, v62
	v_rcp_f32_e32 v62, v62
	v_exp_f32_e32 v64, v64
	v_pk_mul_f32 v[58:59], v[58:59], v[68:69] op_sel_hi:[1,0]
	v_add_f32_e32 v63, 1.0, v63
	v_mul_f32_e32 v12, v12, v62
	v_rcp_f32_e32 v63, v63
	v_mul_f32_e32 v12, v58, v12
	v_add_f32_e32 v58, 1.0, v64
	v_mul_f32_e32 v62, 0xbfb8aa3b, v11
	v_rcp_f32_e32 v58, v58
	v_exp_f32_e32 v62, v62
	v_mul_f32_e32 v13, v13, v63
	v_mul_f32_e32 v13, v59, v13
	v_mul_f32_e32 v10, v10, v58
	v_add_f32_e32 v58, 1.0, v62
	v_mov_b32_e32 v59, v133
	v_rcp_f32_e32 v58, v58
	v_cvt_pk_fp8_f32 v59, v12, v13
	v_pk_mul_f32 v[12:13], v[54:55], v[68:69] op_sel_hi:[1,0]
	v_pk_mul_f32 v[60:61], v[60:61], v[68:69] op_sel_hi:[1,0]
	v_mul_f32_e32 v54, 0xbfb8aa3b, v12
	v_exp_f32_e32 v54, v54
	v_mul_f32_e32 v11, v11, v58
	v_mul_f32_e32 v10, v60, v10
	v_mul_f32_e32 v11, v61, v11
	v_cvt_pk_fp8_f32 v59, v10, v11 op_sel:[0,0,1]
	v_add_f32_e32 v10, 1.0, v54
	v_rcp_f32_e32 v54, v10
	v_pk_mul_f32 v[10:11], v[56:57], v[68:69] op_sel_hi:[1,0]
	v_pk_mul_f32 v[50:51], v[50:51], v[68:69] op_sel_hi:[1,0]
	v_mul_f32_e32 v55, 0xbfb8aa3b, v10
	v_mul_f32_e32 v12, v12, v54
	v_mul_f32_e32 v54, 0xbfb8aa3b, v13
	v_exp_f32_e32 v54, v54
	v_exp_f32_e32 v55, v55
	v_mul_f32_e32 v12, v50, v12
	v_pk_mul_f32 v[52:53], v[52:53], v[68:69] op_sel_hi:[1,0]
	v_add_f32_e32 v50, 1.0, v54
	v_add_f32_e32 v54, 1.0, v55
	v_mul_f32_e32 v55, 0xbfb8aa3b, v11
	v_rcp_f32_e32 v50, v50
	v_exp_f32_e32 v55, v55
	v_rcp_f32_e32 v54, v54
	v_mul_f32_e32 v13, v13, v50
	v_add_f32_e32 v50, 1.0, v55
	v_rcp_f32_e32 v50, v50
	v_mul_f32_e32 v13, v51, v13
	v_mov_b32_e32 v51, v133
	v_cvt_pk_fp8_f32 v51, v12, v13
	v_mul_f32_e32 v10, v10, v54
	v_mul_f32_e32 v11, v11, v50
	v_mul_f32_e32 v10, v52, v10
	v_mul_f32_e32 v11, v53, v11
	v_cvt_pk_fp8_f32 v51, v10, v11 op_sel:[0,0,1]
	v_add_u32_e32 v12, 0x80, v114
	v_ashrrev_i32_e32 v13, 31, v12
	v_lshlrev_b64 v[12:13], 9, v[12:13]
	ds_write2_b32 v119, v59, v51 offset1:4
	ds_read_b64 v[10:11], v118
	v_lshl_add_u64 v[12:13], s[16:17], 0, v[12:13]
	v_lshl_add_u64 v[12:13], v[12:13], 0, s[2:3]
	v_lshl_add_u64 v[12:13], v[12:13], 0, v[134:135]
	v_lshl_add_u64 v[12:13], v[12:13], 0, v[132:133]
	v_add_u32_e32 v51, 0x90, v136
	s_waitcnt lgkmcnt(0)
	global_store_dwordx2 v[12:13], v[10:11], off
	v_add_u32_e32 v10, s44, v51
	v_cmp_lt_i32_e32 vcc, v10, v252
	s_and_saveexec_b64 s[46:47], vcc
	s_cbranch_execz .LBB0_1634
	s_ashr_i32 s9, s8, 31
	s_ashr_i32 s45, s44, 31
	s_lshl_b64 s[48:49], s[8:9], 16
	s_add_u32 s9, s51, s48
	s_addc_u32 s37, s52, s49
	s_lshl_b64 s[48:49], s[44:45], 2
	s_add_u32 s48, s9, s48
	s_addc_u32 s49, s37, s49
	v_lshl_add_u64 v[10:11], v[136:137], 2, s[48:49]
	v_mov_b32_e32 v50, v165
	v_mov_b32_e32 v11, v133
	v_cmp_eq_u32_e32 vcc, 0, v148
	v_lshrrev_b32_e32 v10, 1, v50
	v_lshl_add_u64 v[10:11], v[10:11], 2, s[18:19]
	v_mov_b32_e32 v52, v173
	s_and_saveexec_b64 s[48:49], vcc
	s_cbranch_execz .LBB0_1633
	v_add_u32_e32 v12, s57, v51
	v_mov_b32_e32 v51, v133
	v_lshl_add_u64 v[10:11], v[50:51], 2, s[20:21]
	global_store_dword v[10:11], v12, off
.LBB0_1633:
	s_or_b64 exec, exec, s[48:49]
	v_mul_f32_e32 v66, 0x3d000000, v52
.LBB0_1634:
	s_or_b64 exec, exec, s[46:47]
	v_pk_mul_f32 v[12:13], v[46:47], v[66:67] op_sel_hi:[1,0]
	v_pk_mul_f32 v[10:11], v[48:49], v[66:67] op_sel_hi:[1,0]
	v_mul_f32_e32 v46, 0xbfb8aa3b, v12
	v_exp_f32_e32 v46, v46
	v_mul_f32_e32 v47, 0xbfb8aa3b, v13
	v_exp_f32_e32 v47, v47
	v_mul_f32_e32 v48, 0xbfb8aa3b, v10
	v_add_f32_e32 v46, 1.0, v46
	v_rcp_f32_e32 v46, v46
	v_exp_f32_e32 v48, v48
	v_pk_mul_f32 v[42:43], v[42:43], v[66:67] op_sel_hi:[1,0]
	v_add_f32_e32 v47, 1.0, v47
	v_mul_f32_e32 v12, v12, v46
	v_rcp_f32_e32 v47, v47
	v_mul_f32_e32 v12, v42, v12
	v_add_f32_e32 v42, 1.0, v48
	v_mul_f32_e32 v46, 0xbfb8aa3b, v11
	v_rcp_f32_e32 v42, v42
	v_exp_f32_e32 v46, v46
	v_mul_f32_e32 v13, v13, v47
	v_mul_f32_e32 v13, v43, v13
	v_mul_f32_e32 v10, v10, v42
	v_add_f32_e32 v42, 1.0, v46
	v_mov_b32_e32 v43, v133
	v_rcp_f32_e32 v42, v42
	v_cvt_pk_fp8_f32 v43, v12, v13
	v_pk_mul_f32 v[12:13], v[38:39], v[66:67] op_sel_hi:[1,0]
	v_pk_mul_f32 v[44:45], v[44:45], v[66:67] op_sel_hi:[1,0]
	v_mul_f32_e32 v38, 0xbfb8aa3b, v12
	v_exp_f32_e32 v38, v38
	v_mul_f32_e32 v11, v11, v42
	v_mul_f32_e32 v10, v44, v10
	v_mul_f32_e32 v11, v45, v11
	v_cvt_pk_fp8_f32 v43, v10, v11 op_sel:[0,0,1]
	v_add_f32_e32 v10, 1.0, v38
	v_rcp_f32_e32 v38, v10
	v_pk_mul_f32 v[10:11], v[40:41], v[66:67] op_sel_hi:[1,0]
	v_pk_mul_f32 v[34:35], v[34:35], v[66:67] op_sel_hi:[1,0]
	v_mul_f32_e32 v39, 0xbfb8aa3b, v10
	v_mul_f32_e32 v12, v12, v38
	v_mul_f32_e32 v38, 0xbfb8aa3b, v13
	v_exp_f32_e32 v38, v38
	v_exp_f32_e32 v39, v39
	v_mul_f32_e32 v12, v34, v12
	v_pk_mul_f32 v[36:37], v[36:37], v[66:67] op_sel_hi:[1,0]
	v_add_f32_e32 v34, 1.0, v38
	v_add_f32_e32 v38, 1.0, v39
	v_mul_f32_e32 v39, 0xbfb8aa3b, v11
	v_rcp_f32_e32 v34, v34
	v_exp_f32_e32 v39, v39
	v_rcp_f32_e32 v38, v38
	v_mul_f32_e32 v13, v13, v34
	v_add_f32_e32 v34, 1.0, v39
	v_rcp_f32_e32 v34, v34
	v_mul_f32_e32 v13, v35, v13
	v_mov_b32_e32 v35, v133
	v_cvt_pk_fp8_f32 v35, v12, v13
	v_mul_f32_e32 v10, v10, v38
	v_mul_f32_e32 v11, v11, v34
	v_mul_f32_e32 v10, v36, v10
	v_mul_f32_e32 v11, v37, v11
	v_cvt_pk_fp8_f32 v35, v10, v11 op_sel:[0,0,1]
	v_add_u32_e32 v12, 0x90, v114
	v_ashrrev_i32_e32 v13, 31, v12
	v_lshlrev_b64 v[12:13], 9, v[12:13]
	ds_write2_b32 v99, v43, v35 offset0:64 offset1:68
	ds_read_b64 v[10:11], v118 offset:1280
	v_lshl_add_u64 v[12:13], s[16:17], 0, v[12:13]
	v_lshl_add_u64 v[12:13], v[12:13], 0, s[2:3]
	v_lshl_add_u64 v[12:13], v[12:13], 0, v[134:135]
	v_lshl_add_u64 v[12:13], v[12:13], 0, v[132:133]
	v_add_u32_e32 v35, 0xa0, v136
	s_waitcnt lgkmcnt(0)
	global_store_dwordx2 v[12:13], v[10:11], off
	v_add_u32_e32 v10, s44, v35
	v_cmp_lt_i32_e32 vcc, v10, v252
	v_mov_b32_e32 v34, 0
	v_mov_b32_e32 v36, 0
	s_and_saveexec_b64 s[46:47], vcc
	s_cbranch_execz .LBB0_1638
	s_ashr_i32 s9, s8, 31
	s_ashr_i32 s45, s44, 31
	s_lshl_b64 s[48:49], s[8:9], 16
	s_add_u32 s9, s51, s48
	s_addc_u32 s37, s52, s49
	s_lshl_b64 s[48:49], s[44:45], 2
	s_add_u32 s48, s9, s48
	s_addc_u32 s49, s37, s49
	v_lshl_add_u64 v[10:11], v[136:137], 2, s[48:49]
	v_mov_b32_e32 v36, v166
	v_mov_b32_e32 v11, v133
	v_cmp_eq_u32_e32 vcc, 0, v148
	v_lshrrev_b32_e32 v10, 1, v36
	v_lshl_add_u64 v[10:11], v[10:11], 2, s[18:19]
	v_mov_b32_e32 v38, v174
	s_and_saveexec_b64 s[48:49], vcc
	s_cbranch_execz .LBB0_1637
	v_mov_b32_e32 v37, v133
	v_add_u32_e32 v12, s57, v35
	v_lshl_add_u64 v[10:11], v[36:37], 2, s[20:21]
	global_store_dword v[10:11], v12, off
.LBB0_1637:
	s_or_b64 exec, exec, s[48:49]
	v_mul_f32_e32 v36, 0x3d000000, v38
.LBB0_1638:
	s_or_b64 exec, exec, s[46:47]
	v_pk_mul_f32 v[12:13], v[30:31], v[36:37] op_sel_hi:[1,0]
	v_pk_mul_f32 v[10:11], v[32:33], v[36:37] op_sel_hi:[1,0]
	v_mul_f32_e32 v30, 0xbfb8aa3b, v12
	v_exp_f32_e32 v30, v30
	v_mul_f32_e32 v31, 0xbfb8aa3b, v13
	v_exp_f32_e32 v31, v31
	v_mul_f32_e32 v32, 0xbfb8aa3b, v10
	v_add_f32_e32 v30, 1.0, v30
	v_rcp_f32_e32 v30, v30
	v_exp_f32_e32 v32, v32
	v_pk_mul_f32 v[26:27], v[26:27], v[36:37] op_sel_hi:[1,0]
	v_add_f32_e32 v31, 1.0, v31
	v_mul_f32_e32 v12, v12, v30
	v_rcp_f32_e32 v31, v31
	v_mul_f32_e32 v12, v26, v12
	v_add_f32_e32 v26, 1.0, v32
	v_mul_f32_e32 v30, 0xbfb8aa3b, v11
	v_rcp_f32_e32 v26, v26
	v_exp_f32_e32 v30, v30
	v_mul_f32_e32 v13, v13, v31
	v_mul_f32_e32 v13, v27, v13
	v_mul_f32_e32 v10, v10, v26
	v_add_f32_e32 v26, 1.0, v30
	v_mov_b32_e32 v27, v133
	v_rcp_f32_e32 v26, v26
	v_cvt_pk_fp8_f32 v27, v12, v13
	v_pk_mul_f32 v[12:13], v[22:23], v[36:37] op_sel_hi:[1,0]
	v_pk_mul_f32 v[28:29], v[28:29], v[36:37] op_sel_hi:[1,0]
	v_mul_f32_e32 v22, 0xbfb8aa3b, v12
	v_exp_f32_e32 v22, v22
	v_mul_f32_e32 v11, v11, v26
	v_mul_f32_e32 v10, v28, v10
	v_mul_f32_e32 v11, v29, v11
	v_cvt_pk_fp8_f32 v27, v10, v11 op_sel:[0,0,1]
	v_add_f32_e32 v10, 1.0, v22
	v_rcp_f32_e32 v22, v10
	v_pk_mul_f32 v[10:11], v[24:25], v[36:37] op_sel_hi:[1,0]
	v_pk_mul_f32 v[18:19], v[18:19], v[36:37] op_sel_hi:[1,0]
	v_mul_f32_e32 v23, 0xbfb8aa3b, v10
	v_mul_f32_e32 v12, v12, v22
	v_mul_f32_e32 v22, 0xbfb8aa3b, v13
	v_exp_f32_e32 v22, v22
	v_exp_f32_e32 v23, v23
	v_mul_f32_e32 v12, v18, v12
	v_pk_mul_f32 v[20:21], v[20:21], v[36:37] op_sel_hi:[1,0]
	v_add_f32_e32 v18, 1.0, v22
	v_add_f32_e32 v22, 1.0, v23
	v_mul_f32_e32 v23, 0xbfb8aa3b, v11
	v_rcp_f32_e32 v18, v18
	v_exp_f32_e32 v23, v23
	v_rcp_f32_e32 v22, v22
	v_mul_f32_e32 v13, v13, v18
	v_add_f32_e32 v18, 1.0, v23
	v_rcp_f32_e32 v18, v18
	v_mul_f32_e32 v13, v19, v13
	v_mov_b32_e32 v19, v133
	v_cvt_pk_fp8_f32 v19, v12, v13
	v_mul_f32_e32 v10, v10, v22
	v_mul_f32_e32 v11, v11, v18
	v_mul_f32_e32 v10, v20, v10
	v_mul_f32_e32 v11, v21, v11
	v_cvt_pk_fp8_f32 v19, v10, v11 op_sel:[0,0,1]
	v_add_u32_e32 v12, 0xa0, v114
	v_ashrrev_i32_e32 v13, 31, v12
	v_lshlrev_b64 v[12:13], 9, v[12:13]
	ds_write2_b32 v119, v27, v19 offset1:4
	ds_read_b64 v[10:11], v118
	v_lshl_add_u64 v[12:13], s[16:17], 0, v[12:13]
	v_lshl_add_u64 v[12:13], v[12:13], 0, s[2:3]
	v_lshl_add_u64 v[12:13], v[12:13], 0, v[134:135]
	v_lshl_add_u64 v[12:13], v[12:13], 0, v[132:133]
	v_add_u32_e32 v19, 0xb0, v136
	s_waitcnt lgkmcnt(0)
	global_store_dwordx2 v[12:13], v[10:11], off
	v_add_u32_e32 v10, s44, v19
	v_cmp_lt_i32_e32 vcc, v10, v252
	s_and_saveexec_b64 s[46:47], vcc
	s_cbranch_execz .LBB0_1597
	s_ashr_i32 s9, s8, 31
	s_ashr_i32 s45, s44, 31
	s_lshl_b64 s[8:9], s[8:9], 16
	s_add_u32 s37, s51, s8
	s_addc_u32 s39, s52, s9
	s_lshl_b64 s[8:9], s[44:45], 2
	s_add_u32 s8, s37, s8
	s_addc_u32 s9, s39, s9
	v_lshl_add_u64 v[10:11], v[136:137], 2, s[8:9]
	v_mov_b32_e32 v18, v167
	v_mov_b32_e32 v11, v133
	v_cmp_eq_u32_e32 vcc, 0, v148
	v_lshrrev_b32_e32 v10, 1, v18
	v_lshl_add_u64 v[10:11], v[10:11], 2, s[18:19]
	v_mov_b32_e32 v20, v175
	s_and_saveexec_b64 s[8:9], vcc
	s_cbranch_execz .LBB0_1596
	v_add_u32_e32 v12, s57, v19
	v_mov_b32_e32 v19, v133
	v_lshl_add_u64 v[10:11], v[18:19], 2, s[20:21]
	global_store_dword v[10:11], v12, off
	s_branch .LBB0_1596

.LBB0_1780:
	s_or_b64 exec, exec, s[12:13]
	v_readlane_b32 s36, v254, 2
	v_readlane_b32 s40, v254, 6
	v_readlane_b32 s41, v254, 7
	v_readlane_b32 s42, v254, 8
	v_readlane_b32 s43, v254, 9
	s_mov_b64 s[12:13], s[40:41]
	s_add_u32 s12, s12, 0x2000
	s_addc_u32 s13, s13, 0
	v_mbcnt_lo_u32_b32 v1, -1, 0
	v_lshl_add_u64 v[84:85], s[12:13], 0, v[2:3]
	v_mbcnt_hi_u32_b32 v2, -1, v1
	v_and_b32_e32 v3, 64, v2
	v_xor_b32_e32 v1, 32, v2
	v_add_u32_e32 v3, 64, v3
	v_lshl_add_u64 v[86:87], s[12:13], 0, v[4:5]
	v_cmp_lt_i32_e32 vcc, v1, v3
	v_xor_b32_e32 v4, 16, v2
	v_readlane_b32 s37, v254, 3
	v_cndmask_b32_e32 v1, v2, v1, vcc
	v_cmp_lt_i32_e32 vcc, v4, v3
	v_readlane_b32 s38, v254, 4
	v_readlane_b32 s39, v254, 5
	v_cndmask_b32_e32 v4, v2, v4, vcc
	v_lshlrev_b32_e32 v104, 2, v4
	v_xor_b32_e32 v4, 8, v2
	v_cmp_lt_i32_e32 vcc, v4, v3
	v_readlane_b32 s44, v254, 10
	v_readlane_b32 s45, v254, 11
	v_cndmask_b32_e32 v4, v2, v4, vcc
	v_lshlrev_b32_e32 v105, 2, v4
	v_xor_b32_e32 v4, 4, v2
	v_cmp_lt_i32_e32 vcc, v4, v3
	v_readlane_b32 s46, v254, 12
	v_readlane_b32 s47, v254, 13
	v_cndmask_b32_e32 v4, v2, v4, vcc
	v_lshlrev_b32_e32 v106, 2, v4
	v_xor_b32_e32 v4, 2, v2
	v_cmp_lt_i32_e32 vcc, v4, v3
	v_readlane_b32 s48, v254, 14
	v_readlane_b32 s49, v254, 15
	v_cndmask_b32_e32 v4, v2, v4, vcc
	v_lshlrev_b32_e32 v107, 2, v4
	v_xor_b32_e32 v4, 1, v2
	v_cmp_lt_i32_e32 vcc, v4, v3
	v_readlane_b32 s50, v254, 16
	v_readlane_b32 s51, v254, 17
	v_cndmask_b32_e32 v2, v2, v4, vcc
	v_lshlrev_b32_e32 v108, 2, v2
	v_lshlrev_b64 v[2:3], 11, v[102:103]
	s_mov_b64 s[14:15], s[42:43]
	v_or_b32_e32 v14, 0x400, v68
	v_mov_b32_e32 v15, v67
	v_or_b32_e32 v2, v2, v66
	v_readlane_b32 s36, v254, 18
	v_lshl_add_u64 v[78:79], s[12:13], 0, v[14:15]
	v_or_b32_e32 v14, 0x800, v68
	v_lshl_add_u64 v[92:93], s[0:1], 0, v[66:67]
	v_lshl_add_u64 v[2:3], s[88:89], 0, v[2:3]
	s_mov_b64 s[0:1], 0x51d10000
	v_ashrrev_i32_e32 v11, 31, v10
	v_readlane_b32 s50, v254, 32
	v_readlane_b32 s51, v254, 33
	v_lshl_add_u64 v[80:81], s[12:13], 0, v[14:15]
	v_or_b32_e32 v14, 0xc00, v68
	v_lshl_add_u64 v[94:95], v[2:3], 0, s[0:1]
	s_ashr_i32 s11, s10, 31
	v_lshlrev_b64 v[2:3], 13, v[10:11]
	s_mov_b64 s[14:15], s[50:51]
	v_lshl_add_u64 v[76:77], s[12:13], 0, v[68:69]
	v_lshl_add_u64 v[82:83], s[12:13], 0, v[14:15]
	v_lshl_add_u64 v[88:89], s[12:13], 0, v[6:7]
	v_lshl_add_u64 v[90:91], s[12:13], 0, v[8:9]
	global_load_dwordx4 v[160:163], v[76:77], off
	global_load_dwordx4 v[164:167], v[78:79], off
	global_load_dwordx4 v[168:171], v[80:81], off
	global_load_dwordx4 v[172:175], v[82:83], off
	global_load_dwordx4 v[176:179], v[84:85], off
	global_load_dwordx4 v[180:183], v[86:87], off
	global_load_dwordx4 v[184:187], v[88:89], off
	global_load_dwordx4 v[188:191], v[90:91], off
	s_lshl_b64 s[12:13], s[10:11], 11
	v_lshl_add_u64 v[96:97], s[14:15], 0, v[2:3]
	s_lshl_b64 s[14:15], s[10:11], 13
	s_lshl_b32 s11, s92, 4
	s_add_i32 s16, s16, s11
	v_add_lshl_u32 v98, s16, v12, 1
	v_mov_b64_e32 v[2:3], v[62:63]
	v_mov_b64_e32 v[6:7], v[58:59]
	v_mov_b64_e32 v[10:11], v[54:55]
	v_mov_b64_e32 v[14:15], v[50:51]
	v_mov_b64_e32 v[18:19], v[46:47]
	v_mov_b64_e32 v[22:23], v[42:43]
	v_mov_b64_e32 v[26:27], v[38:39]
	v_mov_b64_e32 v[30:31], v[34:35]
	v_lshlrev_b32_e32 v1, 2, v1
	s_mov_b64 s[16:17], 0
	s_movk_i32 s23, 0x4000
	s_movk_i32 s24, 0x3fff
	v_mov_b32_e32 v109, 0x358637bd
	s_mov_b32 s25, 0x800000
	s_waitcnt vmcnt(7)
	v_mov_b32_e32 v66, v141
	s_waitcnt vmcnt(6)
	v_mov_b32_e32 v111, v139
	s_waitcnt vmcnt(5)
	v_mov_b32_e32 v113, v136
	s_waitcnt vmcnt(4)
	v_mov_b32_e32 v115, v134
	s_waitcnt vmcnt(3)
	v_mov_b32_e32 v117, v132
	s_waitcnt vmcnt(2)
	v_mov_b32_e32 v119, v130
	s_waitcnt vmcnt(1)
	v_mov_b32_e32 v121, v128
	s_waitcnt vmcnt(0)
	v_mov_b32_e32 v123, v126
	v_mov_b32_e32 v110, v142
	v_mov_b32_e32 v112, v140
	v_mov_b32_e32 v114, v137
	v_mov_b32_e32 v116, v135
	v_mov_b32_e32 v118, v133
	v_mov_b32_e32 v120, v131
	v_mov_b32_e32 v122, v129
	v_mov_b32_e32 v124, v127
	v_mov_b64_e32 v[4:5], v[64:65]
	v_mov_b64_e32 v[8:9], v[60:61]
	v_mov_b64_e32 v[12:13], v[56:57]
	v_mov_b64_e32 v[16:17], v[52:53]
	v_mov_b64_e32 v[20:21], v[48:49]
	v_mov_b64_e32 v[24:25], v[44:45]
	v_mov_b64_e32 v[28:29], v[40:41]
	v_mov_b64_e32 v[32:33], v[36:37]
	v_readlane_b32 s37, v254, 19
	v_readlane_b32 s38, v254, 20
	v_readlane_b32 s39, v254, 21
	v_readlane_b32 s40, v254, 22
	v_readlane_b32 s41, v254, 23
	v_readlane_b32 s42, v254, 24
	v_readlane_b32 s43, v254, 25
	v_readlane_b32 s44, v254, 26
	v_readlane_b32 s45, v254, 27
	v_readlane_b32 s46, v254, 28
	v_readlane_b32 s47, v254, 29
	v_readlane_b32 s48, v254, 30
	v_readlane_b32 s49, v254, 31
	s_branch .LBB0_1783

.LBB0_1782:
	s_or_b64 exec, exec, s[18:19]
	v_cvt_pk_f32_fp8_e32 v[144:145], v141
	v_cvt_pk_f32_fp8_e32 v[146:147], v142
	v_cvt_pk_f32_fp8_sdwa v[148:149], v141 src0_sel:WORD_1
	v_mul_f32_e32 v102, 0x3e800000, v101
	v_cvt_pk_f32_fp8_sdwa v[142:143], v142 src0_sel:WORD_1
	v_mul_f32_e32 v100, 0x3e800000, v100
	v_pk_mul_f32 v[144:145], v[102:103], v[144:145] op_sel_hi:[0,1]
	v_pk_fma_f32 v[144:145], v[100:101], v[146:147], v[144:145] op_sel_hi:[0,1,1]
	v_pk_add_f32 v[62:63], v[62:63], v[144:145]
	v_pk_mul_f32 v[144:145], v[102:103], v[148:149] op_sel_hi:[0,1]
	v_pk_fma_f32 v[142:143], v[100:101], v[142:143], v[144:145] op_sel_hi:[0,1,1]
	v_cvt_pk_f32_fp8_e32 v[144:145], v139
	v_cvt_pk_f32_fp8_e32 v[146:147], v140
	v_cvt_pk_f32_fp8_sdwa v[148:149], v139 src0_sel:WORD_1
	v_cvt_pk_f32_fp8_sdwa v[140:141], v140 src0_sel:WORD_1
	v_pk_mul_f32 v[144:145], v[102:103], v[144:145] op_sel_hi:[0,1]
	v_pk_fma_f32 v[144:145], v[100:101], v[146:147], v[144:145] op_sel_hi:[0,1,1]
	v_pk_add_f32 v[58:59], v[58:59], v[144:145]
	v_pk_mul_f32 v[144:145], v[102:103], v[148:149] op_sel_hi:[0,1]
	v_pk_fma_f32 v[140:141], v[100:101], v[140:141], v[144:145] op_sel_hi:[0,1,1]
	v_pk_add_f32 v[60:61], v[60:61], v[140:141]
	v_cvt_pk_f32_fp8_e32 v[140:141], v136
	v_cvt_pk_f32_fp8_e32 v[144:145], v137
	v_cvt_pk_f32_fp8_sdwa v[146:147], v137 src0_sel:WORD_1
	v_cvt_pk_f32_fp8_sdwa v[136:137], v136 src0_sel:WORD_1
	v_pk_mul_f32 v[140:141], v[102:103], v[140:141] op_sel_hi:[0,1]
	v_pk_fma_f32 v[140:141], v[100:101], v[144:145], v[140:141] op_sel_hi:[0,1,1]
	v_pk_add_f32 v[54:55], v[54:55], v[140:141]
	v_pk_mul_f32 v[136:137], v[102:103], v[136:137] op_sel_hi:[0,1]
	v_pk_fma_f32 v[136:137], v[100:101], v[146:147], v[136:137] op_sel_hi:[0,1,1]
	v_pk_add_f32 v[56:57], v[56:57], v[136:137]
	v_cvt_pk_f32_fp8_e32 v[136:137], v134
	v_cvt_pk_f32_fp8_e32 v[140:141], v135
	v_cvt_pk_f32_fp8_sdwa v[144:145], v135 src0_sel:WORD_1
	v_cvt_pk_f32_fp8_sdwa v[134:135], v134 src0_sel:WORD_1
	v_pk_mul_f32 v[136:137], v[102:103], v[136:137] op_sel_hi:[0,1]
	v_pk_fma_f32 v[136:137], v[100:101], v[140:141], v[136:137] op_sel_hi:[0,1,1]
	v_pk_add_f32 v[50:51], v[50:51], v[136:137]
	v_pk_mul_f32 v[134:135], v[102:103], v[134:135] op_sel_hi:[0,1]
	v_pk_fma_f32 v[134:135], v[100:101], v[144:145], v[134:135] op_sel_hi:[0,1,1]
	v_pk_add_f32 v[52:53], v[52:53], v[134:135]
	v_cvt_pk_f32_fp8_e32 v[134:135], v132
	v_cvt_pk_f32_fp8_e32 v[136:137], v133
	v_cvt_pk_f32_fp8_sdwa v[140:141], v133 src0_sel:WORD_1
	v_cvt_pk_f32_fp8_sdwa v[132:133], v132 src0_sel:WORD_1
	v_pk_mul_f32 v[134:135], v[102:103], v[134:135] op_sel_hi:[0,1]
	v_pk_fma_f32 v[134:135], v[100:101], v[136:137], v[134:135] op_sel_hi:[0,1,1]
	v_pk_add_f32 v[46:47], v[46:47], v[134:135]
	v_pk_mul_f32 v[132:133], v[102:103], v[132:133] op_sel_hi:[0,1]
	v_pk_fma_f32 v[132:133], v[100:101], v[140:141], v[132:133] op_sel_hi:[0,1,1]
	v_cvt_pk_f32_fp8_e32 v[134:135], v130
	v_cvt_pk_f32_fp8_e32 v[136:137], v131
	v_cvt_pk_f32_fp8_sdwa v[140:141], v131 src0_sel:WORD_1
	v_cvt_pk_f32_fp8_sdwa v[130:131], v130 src0_sel:WORD_1
	v_pk_mul_f32 v[134:135], v[102:103], v[134:135] op_sel_hi:[0,1]
	v_pk_fma_f32 v[134:135], v[100:101], v[136:137], v[134:135] op_sel_hi:[0,1,1]
	v_pk_add_f32 v[42:43], v[42:43], v[134:135]
	v_pk_mul_f32 v[130:131], v[102:103], v[130:131] op_sel_hi:[0,1]
	v_pk_fma_f32 v[130:131], v[100:101], v[140:141], v[130:131] op_sel_hi:[0,1,1]
	v_pk_add_f32 v[44:45], v[44:45], v[130:131]
	v_cvt_pk_f32_fp8_e32 v[130:131], v128
	v_cvt_pk_f32_fp8_e32 v[134:135], v129
	v_cvt_pk_f32_fp8_sdwa v[136:137], v129 src0_sel:WORD_1
	v_cvt_pk_f32_fp8_sdwa v[128:129], v128 src0_sel:WORD_1
	v_pk_mul_f32 v[130:131], v[102:103], v[130:131] op_sel_hi:[0,1]
	v_pk_fma_f32 v[130:131], v[100:101], v[134:135], v[130:131] op_sel_hi:[0,1,1]
	v_pk_add_f32 v[38:39], v[38:39], v[130:131]
	v_pk_mul_f32 v[128:129], v[102:103], v[128:129] op_sel_hi:[0,1]
	v_pk_fma_f32 v[128:129], v[100:101], v[136:137], v[128:129] op_sel_hi:[0,1,1]
	v_pk_add_f32 v[40:41], v[40:41], v[128:129]
	v_cvt_pk_f32_fp8_e32 v[128:129], v126
	v_cvt_pk_f32_fp8_e32 v[130:131], v127
	v_cvt_pk_f32_fp8_sdwa v[134:135], v127 src0_sel:WORD_1
	v_cvt_pk_f32_fp8_sdwa v[126:127], v126 src0_sel:WORD_1
	v_pk_add_f32 v[64:65], v[64:65], v[142:143]
	v_lshl_add_u64 v[142:143], v[72:73], 0, v[68:69]
	v_pk_mul_f32 v[128:129], v[102:103], v[128:129] op_sel_hi:[0,1]
	v_pk_mul_f32 v[102:103], v[102:103], v[126:127] op_sel_hi:[0,1]
	v_pk_add_f32 v[48:49], v[48:49], v[132:133]
	v_add_co_u32_e64 v132, s[0:1], s22, v142
	v_pk_fma_f32 v[128:129], v[100:101], v[130:131], v[128:129] op_sel_hi:[0,1,1]
	v_pk_fma_f32 v[100:101], v[100:101], v[134:135], v[102:103] op_sel_hi:[0,1,1]
	v_mov_b32_e32 v102, v47
	v_mov_b32_e32 v103, v43
	v_addc_co_u32_e64 v133, s[0:1], 0, v143, s[0:1]
	v_pk_add_f32 v[34:35], v[34:35], v[128:129]
	v_pk_add_f32 v[36:37], v[36:37], v[100:101]
	v_mov_b32_e32 v100, v46
	v_mov_b32_e32 v101, v42
	v_pk_mul_f32 v[102:103], v[102:103], v[102:103]
	global_store_dwordx4 v[142:143], v[62:65], off
	global_store_dwordx4 v[142:143], v[58:61], off offset:1024
	global_store_dwordx4 v[142:143], v[54:57], off offset:2048
	global_store_dwordx4 v[142:143], v[50:53], off offset:3072
	global_store_dwordx4 v[132:133], v[46:49], off
	global_store_dwordx4 v[132:133], v[42:45], off offset:1024
	global_store_dwordx4 v[132:133], v[38:41], off offset:2048
	global_store_dwordx4 v[132:133], v[34:37], off offset:3072
	v_pk_fma_f32 v[100:101], v[100:101], v[100:101], v[102:103]
	v_mov_b32_e32 v102, v48
	v_mov_b32_e32 v103, v44
	v_pk_fma_f32 v[146:147], v[102:103], v[102:103], v[100:101]
	v_mov_b64_e32 v[100:101], v[160:161]
	v_mov_b64_e32 v[102:103], v[162:163]
	v_pk_mul_f32 v[128:129], v[62:63], v[62:63]
	v_pk_mul_f32 v[126:127], v[64:65], v[64:65]
	v_pk_mul_f32 v[132:133], v[58:59], v[58:59]
	v_add_f32_e32 v128, v128, v129
	v_pk_mul_f32 v[130:131], v[60:61], v[60:61]
	v_pk_mul_f32 v[136:137], v[54:55], v[54:55]
	v_add_f32_e32 v132, v132, v133
	v_add_f32_e32 v126, v128, v126
	v_pk_mul_f32 v[134:135], v[56:57], v[56:57]
	v_add_f32_e32 v130, v132, v130
	v_add_f32_e32 v126, v127, v126
	v_add_f32_e32 v127, v136, v137
	v_add_f32_e32 v130, v131, v130
	v_add_f32_e32 v127, v127, v134
	v_pk_mul_f32 v[142:143], v[50:51], v[50:51]
	v_add_f32_e32 v126, v126, v130
	v_add_f32_e32 v127, v135, v127
	v_pk_mul_f32 v[140:141], v[52:53], v[52:53]
	v_add_f32_e32 v126, v126, v127
	v_add_f32_e32 v127, v142, v143
	v_mov_b32_e32 v150, v39
	v_mov_b32_e32 v151, v35
	v_add_f32_e32 v127, v127, v140
	v_mov_b32_e32 v144, v49
	v_mov_b32_e32 v145, v45
	v_mov_b32_e32 v148, v38
	v_mov_b32_e32 v149, v34
	v_pk_mul_f32 v[150:151], v[150:151], v[150:151]
	v_add_f32_e32 v127, v141, v127
	v_pk_fma_f32 v[144:145], v[144:145], v[144:145], v[146:147]
	v_pk_fma_f32 v[148:149], v[148:149], v[148:149], v[150:151]
	v_mov_b32_e32 v150, v40
	v_mov_b32_e32 v151, v36
	v_add_f32_e32 v126, v126, v127
	v_mov_b32_e32 v146, v41
	v_mov_b32_e32 v147, v37
	v_pk_fma_f32 v[148:149], v[150:151], v[150:151], v[148:149]
	v_add_f32_e32 v126, v126, v144
	v_pk_fma_f32 v[146:147], v[146:147], v[146:147], v[148:149]
	v_add_f32_e32 v126, v126, v145
	v_add_f32_e32 v126, v126, v146
	v_add_f32_e32 v126, v126, v147
	ds_bpermute_b32 v127, v1, v126
	v_lshl_add_u64 v[96:97], v[96:97], 0, s[14:15]
	v_lshl_add_u64 v[72:73], v[72:73], 0, s[14:15]
	v_add_u32_e32 v98, s11, v98
	v_mov_b32_e32 v141, v66
	s_waitcnt lgkmcnt(0)
	v_add_f32_e32 v126, v126, v127
	ds_bpermute_b32 v127, v104, v126
	v_mov_b32_e32 v139, v111
	v_mov_b32_e32 v136, v113
	v_mov_b32_e32 v134, v115
	v_mov_b32_e32 v132, v117
	s_waitcnt lgkmcnt(0)
	v_add_f32_e32 v126, v126, v127
	ds_bpermute_b32 v127, v105, v126
	v_mov_b32_e32 v130, v119
	v_mov_b32_e32 v128, v121
	v_mov_b32_e32 v142, v110
	v_mov_b32_e32 v140, v112
	s_waitcnt lgkmcnt(0)
	v_add_f32_e32 v126, v126, v127
	ds_bpermute_b32 v127, v106, v126
	v_mov_b32_e32 v137, v114
	v_mov_b32_e32 v135, v116
	v_mov_b32_e32 v133, v118
	v_mov_b32_e32 v131, v120
	s_waitcnt lgkmcnt(0)
	v_add_f32_e32 v126, v126, v127
	ds_bpermute_b32 v127, v107, v126
	v_mov_b32_e32 v129, v122
	s_waitcnt lgkmcnt(0)
	v_add_f32_e32 v126, v126, v127
	ds_bpermute_b32 v127, v108, v126
	s_waitcnt lgkmcnt(0)
	v_add_f32_e32 v126, v126, v127
	v_fmamk_f32 v126, v126, 0x3a000000, v109
	v_mul_f32_e32 v127, 0x4b800000, v126
	v_cmp_gt_f32_e64 s[0:1], s25, v126
	s_nop 1
	v_cndmask_b32_e64 v126, v126, v127, s[0:1]
	v_rsq_f32_e32 v126, v126
	s_nop 0
	v_mul_f32_e32 v127, 0x45800000, v126
	v_cndmask_b32_e64 v143, v126, v127, s[0:1]
	v_mul_f32_e32 v62, v62, v143
	v_mul_f32_e32 v63, v63, v143
	v_mul_f32_e32 v62, v100, v62
	v_mul_f32_e32 v63, v101, v63
	v_mov_b32_e32 v100, 0
	v_cvt_pk_fp8_f32 v100, v62, v63
	v_mul_f32_e32 v64, v64, v143
	v_mul_f32_e32 v63, v65, v143
	v_mul_f32_e32 v62, v102, v64
	v_mul_f32_e32 v63, v103, v63
	v_cvt_pk_fp8_f32 v100, v62, v63 op_sel:[0,0,1]
	v_mul_f32_e32 v58, v58, v143
	v_mul_f32_e32 v59, v59, v143
	v_mul_f32_e32 v60, v60, v143
	global_store_dword v[94:95], v100, off
	v_mov_b64_e32 v[62:63], v[164:165]
	v_mov_b64_e32 v[64:65], v[166:167]
	v_mul_f32_e32 v54, v54, v143
	v_mul_f32_e32 v55, v55, v143
	v_mul_f32_e32 v56, v56, v143
	v_mul_f32_e32 v50, v50, v143
	v_mul_f32_e32 v51, v51, v143
	v_mul_f32_e32 v52, v52, v143
	v_mul_f32_e32 v46, v46, v143
	v_mul_f32_e32 v47, v47, v143
	v_mul_f32_e32 v48, v48, v143
	v_mul_f32_e32 v42, v42, v143
	v_mul_f32_e32 v43, v43, v143
	v_mul_f32_e32 v44, v44, v143
	v_mul_f32_e32 v38, v38, v143
	v_mul_f32_e32 v39, v39, v143
	v_mul_f32_e32 v40, v40, v143
	v_mul_f32_e32 v34, v34, v143
	v_mul_f32_e32 v35, v35, v143
	v_mov_b32_e32 v102, 0
	v_mul_f32_e32 v36, v36, v143
	s_and_b64 s[0:1], exec, vcc
	v_mov_b32_e32 v126, v123
	v_mov_b32_e32 v127, v124
	v_mov_b32_e32 v100, v138
	v_mov_b32_e32 v101, v99
	s_or_b64 s[16:17], s[0:1], s[16:17]
	v_mul_f32_e32 v58, v62, v58
	v_mul_f32_e32 v59, v63, v59
	v_mov_b32_e32 v62, 0
	v_cvt_pk_fp8_f32 v62, v58, v59
	v_mul_f32_e32 v59, v61, v143
	v_mul_f32_e32 v58, v64, v60
	v_mul_f32_e32 v59, v65, v59
	v_cvt_pk_fp8_f32 v62, v58, v59 op_sel:[0,0,1]
	global_store_dword v[94:95], v62, off offset:256
	v_mov_b64_e32 v[58:59], v[168:169]
	v_mov_b64_e32 v[60:61], v[170:171]
	v_mov_b32_e32 v62, 0
	v_mul_f32_e32 v54, v58, v54
	v_mul_f32_e32 v55, v59, v55
	v_cvt_pk_fp8_f32 v62, v54, v55
	v_mul_f32_e32 v54, v57, v143
	v_mul_f32_e32 v55, v60, v56
	v_mul_f32_e32 v54, v61, v54
	v_cvt_pk_fp8_f32 v62, v55, v54 op_sel:[0,0,1]
	v_mov_b32_e32 v58, 0
	global_store_dword v[94:95], v62, off offset:512
	v_mov_b64_e32 v[54:55], v[172:173]
	v_mov_b64_e32 v[56:57], v[174:175]
	v_mov_b64_e32 v[64:65], v[4:5]
	v_mov_b64_e32 v[62:63], v[2:3]
	v_mul_f32_e32 v50, v50, v54
	v_mul_f32_e32 v51, v51, v55
	v_cvt_pk_fp8_f32 v58, v50, v51
	v_mul_f32_e32 v50, v53, v143
	v_mul_f32_e32 v51, v52, v56
	v_mul_f32_e32 v50, v50, v57
	v_cvt_pk_fp8_f32 v58, v51, v50 op_sel:[0,0,1]
	v_mov_b32_e32 v54, 0
	global_store_dword v[94:95], v58, off offset:768
	v_mov_b64_e32 v[50:51], v[176:177]
	v_mov_b64_e32 v[52:53], v[178:179]
	v_mov_b64_e32 v[60:61], v[8:9]
	v_mov_b64_e32 v[58:59], v[6:7]
	v_mul_f32_e32 v46, v46, v50
	v_mul_f32_e32 v47, v47, v51
	v_cvt_pk_fp8_f32 v54, v46, v47
	v_mul_f32_e32 v46, v49, v143
	v_mul_f32_e32 v47, v48, v52
	v_mul_f32_e32 v46, v46, v53
	v_cvt_pk_fp8_f32 v54, v47, v46 op_sel:[0,0,1]
	v_mov_b32_e32 v50, 0
	global_store_dword v[94:95], v54, off offset:1024
	v_mov_b64_e32 v[46:47], v[180:181]
	v_mov_b64_e32 v[48:49], v[182:183]
	v_mov_b64_e32 v[56:57], v[12:13]
	v_mov_b64_e32 v[54:55], v[10:11]
	v_mul_f32_e32 v42, v42, v46
	v_mul_f32_e32 v43, v43, v47
	v_cvt_pk_fp8_f32 v50, v42, v43
	v_mul_f32_e32 v42, v45, v143
	v_mul_f32_e32 v43, v44, v48
	v_mul_f32_e32 v42, v42, v49
	v_cvt_pk_fp8_f32 v50, v43, v42 op_sel:[0,0,1]
	v_mov_b32_e32 v46, 0
	global_store_dword v[94:95], v50, off offset:1280
	v_mov_b64_e32 v[42:43], v[184:185]
	v_mov_b64_e32 v[44:45], v[186:187]
	v_mov_b64_e32 v[52:53], v[16:17]
	v_mov_b64_e32 v[50:51], v[14:15]
	v_mul_f32_e32 v38, v38, v42
	v_mul_f32_e32 v39, v39, v43
	v_cvt_pk_fp8_f32 v46, v38, v39
	v_mul_f32_e32 v38, v41, v143
	v_mul_f32_e32 v39, v40, v44
	v_mul_f32_e32 v38, v38, v45
	v_cvt_pk_fp8_f32 v46, v39, v38 op_sel:[0,0,1]
	v_mov_b64_e32 v[44:45], v[24:25]
	v_mov_b64_e32 v[42:43], v[22:23]
	global_store_dword v[94:95], v46, off offset:1536
	v_mov_b64_e32 v[38:39], v[188:189]
	v_mov_b64_e32 v[40:41], v[190:191]
	v_mov_b64_e32 v[48:49], v[20:21]
	v_mov_b64_e32 v[46:47], v[18:19]
	v_mul_f32_e32 v34, v34, v38
	v_mul_f32_e32 v35, v35, v39
	v_cvt_pk_fp8_f32 v102, v34, v35
	v_mul_f32_e32 v34, v37, v143
	v_mul_f32_e32 v35, v36, v40
	v_mul_f32_e32 v34, v34, v41
	v_cvt_pk_fp8_f32 v102, v35, v34 op_sel:[0,0,1]
	v_mov_b64_e32 v[40:41], v[28:29]
	v_mov_b64_e32 v[36:37], v[32:33]
	v_mov_b64_e32 v[38:39], v[26:27]
	v_mov_b64_e32 v[34:35], v[30:31]
	global_store_dword v[94:95], v102, off offset:1792
	v_lshl_add_u64 v[94:95], v[94:95], 0, s[12:13]
	v_mov_b32_e32 v102, v125
	s_andn2_b64 exec, exec, s[16:17]
	s_cbranch_execz .LBB0_1786

.LBB0_2143:
	v_ashrrev_i32_e32 v2, 6, v1
	v_add_u32_e32 v252, s20, v2
	v_lshl_add_u32 v3, v2, 2, s33
	v_ashrrev_i32_e32 v253, 31, v252
	ds_read_b32 v230, v3
	ds_read_b32 v231, v3 offset:32
	ds_read_b32 v232, v3 offset:64
	ds_read_b32 v233, v3 offset:96
	ds_read_b32 v234, v3 offset:128
	ds_read_b32 v235, v3 offset:160
	ds_read_b32 v236, v3 offset:192
	ds_read_b32 v237, v3 offset:224
	ds_read_b32 v238, v3 offset:256
	ds_read_b32 v239, v3 offset:288
	ds_read_b32 v240, v3 offset:320
	ds_read_b32 v241, v3 offset:352
	ds_read_b32 v242, v3 offset:384
	ds_read_b32 v243, v3 offset:416
	ds_read_b32 v244, v3 offset:448
	ds_read_b32 v245, v3 offset:480
	v_lshlrev_b64 v[250:251], 12, v[252:253]
	v_lshlrev_b64 v[246:247], 13, v[252:253]
	v_mad_i64_i32 v[248:249], s[2:3], v252, s15, v[16:17]
	v_lshl_add_u64 v[250:251], v[20:21], 0, v[250:251]
	v_add_co_u32_e32 v248, vcc, s18, v248
	v_lshl_add_u64 v[246:247], v[14:15], 0, v[246:247]
	s_nop 0
	v_addc_co_u32_e32 v249, vcc, 0, v249, vcc
	s_mov_b32 s36, 0x10000
	s_mov_b32 s37, 0
	s_mov_b32 s38, 0x30000
	s_mov_b32 s39, 0
	s_mov_b32 s40, 0x8000
	s_mov_b32 s41, 0
	global_load_dwordx4 v[28:31], v[18:19], off
	global_load_dwordx4 v[22:25], v[18:19], off offset:16
	global_load_dwordx4 v[34:37], v[246:247], off
	global_load_dwordx4 v[38:41], v[248:249], off
	v_lshl_add_u64 v[246:247], v[246:247], 0, s[36:37]
	v_lshl_add_u64 v[248:249], v[248:249], 0, s[38:39]
	global_load_dwordx4 v[42:45], v[246:247], off
	global_load_dwordx4 v[46:49], v[248:249], off
	v_lshl_add_u64 v[246:247], v[246:247], 0, s[36:37]
	v_lshl_add_u64 v[248:249], v[248:249], 0, s[38:39]
	global_load_dwordx4 v[56:59], v[246:247], off
	global_load_dwordx4 v[60:63], v[248:249], off
	v_lshl_add_u64 v[246:247], v[246:247], 0, s[36:37]
	v_lshl_add_u64 v[248:249], v[248:249], 0, s[38:39]
	global_load_dwordx4 v[64:67], v[246:247], off
	global_load_dwordx4 v[68:71], v[248:249], off
	v_lshl_add_u64 v[246:247], v[246:247], 0, s[36:37]
	v_lshl_add_u64 v[248:249], v[248:249], 0, s[38:39]
	global_load_dwordx4 v[72:75], v[246:247], off
	global_load_dwordx4 v[76:79], v[248:249], off
	v_lshl_add_u64 v[246:247], v[246:247], 0, s[36:37]
	v_lshl_add_u64 v[248:249], v[248:249], 0, s[38:39]
	global_load_dwordx4 v[126:129], v[246:247], off
	global_load_dwordx4 v[130:133], v[248:249], off
	v_lshl_add_u64 v[246:247], v[246:247], 0, s[36:37]
	v_lshl_add_u64 v[248:249], v[248:249], 0, s[38:39]
	global_load_dwordx4 v[134:137], v[246:247], off
	global_load_dwordx4 v[138:141], v[248:249], off
	v_lshl_add_u64 v[246:247], v[246:247], 0, s[36:37]
	v_lshl_add_u64 v[248:249], v[248:249], 0, s[38:39]
	global_load_dwordx4 v[150:153], v[246:247], off
	global_load_dwordx4 v[154:157], v[248:249], off
	v_lshl_add_u64 v[246:247], v[246:247], 0, s[36:37]
	v_lshl_add_u64 v[248:249], v[248:249], 0, s[38:39]
	global_load_dwordx4 v[158:161], v[246:247], off
	global_load_dwordx4 v[162:165], v[248:249], off
	v_lshl_add_u64 v[246:247], v[246:247], 0, s[36:37]
	v_lshl_add_u64 v[248:249], v[248:249], 0, s[38:39]
	global_load_dwordx4 v[166:169], v[246:247], off
	global_load_dwordx4 v[170:173], v[248:249], off
	v_lshl_add_u64 v[246:247], v[246:247], 0, s[36:37]
	v_lshl_add_u64 v[248:249], v[248:249], 0, s[38:39]
	global_load_dwordx4 v[182:185], v[246:247], off
	global_load_dwordx4 v[186:189], v[248:249], off
	v_lshl_add_u64 v[246:247], v[246:247], 0, s[36:37]
	v_lshl_add_u64 v[248:249], v[248:249], 0, s[38:39]
	global_load_dwordx4 v[190:193], v[246:247], off
	global_load_dwordx4 v[194:197], v[248:249], off
	v_lshl_add_u64 v[246:247], v[246:247], 0, s[36:37]
	v_lshl_add_u64 v[248:249], v[248:249], 0, s[38:39]
	global_load_dwordx4 v[198:201], v[246:247], off
	global_load_dwordx4 v[202:205], v[248:249], off
	v_lshl_add_u64 v[246:247], v[246:247], 0, s[36:37]
	v_lshl_add_u64 v[248:249], v[248:249], 0, s[38:39]
	global_load_dwordx4 v[206:209], v[246:247], off
	global_load_dwordx4 v[210:213], v[248:249], off
	v_lshl_add_u64 v[246:247], v[246:247], 0, s[36:37]
	v_lshl_add_u64 v[248:249], v[248:249], 0, s[38:39]
	global_load_dwordx4 v[214:217], v[246:247], off
	global_load_dwordx4 v[218:221], v[248:249], off
	v_lshl_add_u64 v[246:247], v[246:247], 0, s[36:37]
	v_lshl_add_u64 v[248:249], v[248:249], 0, s[38:39]
	global_load_dwordx4 v[222:225], v[246:247], off
	global_load_dwordx4 v[226:229], v[248:249], off
	s_waitcnt lgkmcnt(0)
	s_waitcnt vmcnt(30)
	v_mov_b32_e32 v32, v51
	v_mov_b32_e32 v33, v51
	v_lshlrev_b32_e32 v2, 16, v38
	v_and_b32_e32 v3, 0xffff0000, v38
	v_lshlrev_b32_e32 v4, 16, v39
	v_and_b32_e32 v5, 0xffff0000, v39
	v_lshlrev_b32_e32 v6, 16, v34
	v_and_b32_e32 v7, 0xffff0000, v34
	v_lshlrev_b32_e32 v8, 16, v35
	v_and_b32_e32 v9, 0xffff0000, v35
	v_mul_f32_e32 v10, 0xbfb8aa3b, v2
	v_mul_f32_e32 v11, 0xbfb8aa3b, v3
	v_mul_f32_e32 v12, 0xbfb8aa3b, v4
	v_mul_f32_e32 v13, 0xbfb8aa3b, v5
	v_exp_f32_e32 v10, v10
	v_exp_f32_e32 v11, v11
	v_exp_f32_e32 v12, v12
	v_exp_f32_e32 v13, v13
	v_add_f32_e32 v10, 1.0, v10
	v_add_f32_e32 v11, 1.0, v11
	v_add_f32_e32 v12, 1.0, v12
	v_add_f32_e32 v13, 1.0, v13
	v_rcp_f32_e32 v10, v10
	v_rcp_f32_e32 v11, v11
	v_rcp_f32_e32 v12, v12
	v_rcp_f32_e32 v13, v13
	v_mul_f32_e32 v6, v230, v6
	v_mul_f32_e32 v7, v230, v7
	v_mul_f32_e32 v8, v230, v8
	v_mul_f32_e32 v9, v230, v9
	v_mul_f32_e32 v2, v10, v2
	v_mul_f32_e32 v3, v11, v3
	v_mul_f32_e32 v4, v12, v4
	v_mul_f32_e32 v5, v13, v5
	v_mul_f32_e32 v6, v28, v6
	v_mul_f32_e32 v7, v29, v7
	v_mul_f32_e32 v8, v30, v8
	v_mul_f32_e32 v9, v31, v9
	v_mul_f32_e32 v6, v6, v2
	v_mul_f32_e32 v7, v7, v3
	v_mul_f32_e32 v8, v8, v4
	v_mul_f32_e32 v9, v9, v5
	v_cvt_pk_fp8_f32 v32, v6, v7
	s_nop 0
	v_cvt_pk_fp8_f32 v32, v8, v9 op_sel:[0,0,1]
	v_lshlrev_b32_e32 v2, 16, v40
	v_and_b32_e32 v3, 0xffff0000, v40
	v_lshlrev_b32_e32 v4, 16, v41
	v_and_b32_e32 v5, 0xffff0000, v41
	v_lshlrev_b32_e32 v6, 16, v36
	v_and_b32_e32 v7, 0xffff0000, v36
	v_lshlrev_b32_e32 v8, 16, v37
	v_and_b32_e32 v9, 0xffff0000, v37
	v_mul_f32_e32 v10, 0xbfb8aa3b, v2
	v_mul_f32_e32 v11, 0xbfb8aa3b, v3
	v_mul_f32_e32 v12, 0xbfb8aa3b, v4
	v_mul_f32_e32 v13, 0xbfb8aa3b, v5
	v_exp_f32_e32 v10, v10
	v_exp_f32_e32 v11, v11
	v_exp_f32_e32 v12, v12
	v_exp_f32_e32 v13, v13
	v_add_f32_e32 v10, 1.0, v10
	v_add_f32_e32 v11, 1.0, v11
	v_add_f32_e32 v12, 1.0, v12
	v_add_f32_e32 v13, 1.0, v13
	v_rcp_f32_e32 v10, v10
	v_rcp_f32_e32 v11, v11
	v_rcp_f32_e32 v12, v12
	v_rcp_f32_e32 v13, v13
	v_mul_f32_e32 v6, v230, v6
	v_mul_f32_e32 v7, v230, v7
	v_mul_f32_e32 v8, v230, v8
	v_mul_f32_e32 v9, v230, v9
	v_mul_f32_e32 v2, v10, v2
	v_mul_f32_e32 v3, v11, v3
	v_mul_f32_e32 v4, v12, v4
	v_mul_f32_e32 v5, v13, v5
	v_mul_f32_e32 v6, v22, v6
	v_mul_f32_e32 v7, v23, v7
	v_mul_f32_e32 v8, v24, v8
	v_mul_f32_e32 v9, v25, v9
	v_mul_f32_e32 v6, v6, v2
	v_mul_f32_e32 v7, v7, v3
	v_mul_f32_e32 v8, v8, v4
	v_mul_f32_e32 v9, v9, v5
	v_cvt_pk_fp8_f32 v33, v6, v7
	s_nop 0
	v_cvt_pk_fp8_f32 v33, v8, v9 op_sel:[0,0,1]
	s_nop 1
	global_store_dwordx2 v[250:251], v[32:33], off
	v_lshl_add_u64 v[250:251], v[250:251], 0, s[40:41]
	s_waitcnt vmcnt(29)
	v_mov_b32_e32 v32, v51
	v_mov_b32_e32 v33, v51
	v_lshlrev_b32_e32 v2, 16, v46
	v_and_b32_e32 v3, 0xffff0000, v46
	v_lshlrev_b32_e32 v4, 16, v47
	v_and_b32_e32 v5, 0xffff0000, v47
	v_lshlrev_b32_e32 v6, 16, v42
	v_and_b32_e32 v7, 0xffff0000, v42
	v_lshlrev_b32_e32 v8, 16, v43
	v_and_b32_e32 v9, 0xffff0000, v43
	v_mul_f32_e32 v10, 0xbfb8aa3b, v2
	v_mul_f32_e32 v11, 0xbfb8aa3b, v3
	v_mul_f32_e32 v12, 0xbfb8aa3b, v4
	v_mul_f32_e32 v13, 0xbfb8aa3b, v5
	v_exp_f32_e32 v10, v10
	v_exp_f32_e32 v11, v11
	v_exp_f32_e32 v12, v12
	v_exp_f32_e32 v13, v13
	v_add_f32_e32 v10, 1.0, v10
	v_add_f32_e32 v11, 1.0, v11
	v_add_f32_e32 v12, 1.0, v12
	v_add_f32_e32 v13, 1.0, v13
	v_rcp_f32_e32 v10, v10
	v_rcp_f32_e32 v11, v11
	v_rcp_f32_e32 v12, v12
	v_rcp_f32_e32 v13, v13
	v_mul_f32_e32 v6, v231, v6
	v_mul_f32_e32 v7, v231, v7
	v_mul_f32_e32 v8, v231, v8
	v_mul_f32_e32 v9, v231, v9
	v_mul_f32_e32 v2, v10, v2
	v_mul_f32_e32 v3, v11, v3
	v_mul_f32_e32 v4, v12, v4
	v_mul_f32_e32 v5, v13, v5
	v_mul_f32_e32 v6, v28, v6
	v_mul_f32_e32 v7, v29, v7
	v_mul_f32_e32 v8, v30, v8
	v_mul_f32_e32 v9, v31, v9
	v_mul_f32_e32 v6, v6, v2
	v_mul_f32_e32 v7, v7, v3
	v_mul_f32_e32 v8, v8, v4
	v_mul_f32_e32 v9, v9, v5
	v_cvt_pk_fp8_f32 v32, v6, v7
	s_nop 0
	v_cvt_pk_fp8_f32 v32, v8, v9 op_sel:[0,0,1]
	v_lshlrev_b32_e32 v2, 16, v48
	v_and_b32_e32 v3, 0xffff0000, v48
	v_lshlrev_b32_e32 v4, 16, v49
	v_and_b32_e32 v5, 0xffff0000, v49
	v_lshlrev_b32_e32 v6, 16, v44
	v_and_b32_e32 v7, 0xffff0000, v44
	v_lshlrev_b32_e32 v8, 16, v45
	v_and_b32_e32 v9, 0xffff0000, v45
	v_mul_f32_e32 v10, 0xbfb8aa3b, v2
	v_mul_f32_e32 v11, 0xbfb8aa3b, v3
	v_mul_f32_e32 v12, 0xbfb8aa3b, v4
	v_mul_f32_e32 v13, 0xbfb8aa3b, v5
	v_exp_f32_e32 v10, v10
	v_exp_f32_e32 v11, v11
	v_exp_f32_e32 v12, v12
	v_exp_f32_e32 v13, v13
	v_add_f32_e32 v10, 1.0, v10
	v_add_f32_e32 v11, 1.0, v11
	v_add_f32_e32 v12, 1.0, v12
	v_add_f32_e32 v13, 1.0, v13
	v_rcp_f32_e32 v10, v10
	v_rcp_f32_e32 v11, v11
	v_rcp_f32_e32 v12, v12
	v_rcp_f32_e32 v13, v13
	v_mul_f32_e32 v6, v231, v6
	v_mul_f32_e32 v7, v231, v7
	v_mul_f32_e32 v8, v231, v8
	v_mul_f32_e32 v9, v231, v9
	v_mul_f32_e32 v2, v10, v2
	v_mul_f32_e32 v3, v11, v3
	v_mul_f32_e32 v4, v12, v4
	v_mul_f32_e32 v5, v13, v5
	v_mul_f32_e32 v6, v22, v6
	v_mul_f32_e32 v7, v23, v7
	v_mul_f32_e32 v8, v24, v8
	v_mul_f32_e32 v9, v25, v9
	v_mul_f32_e32 v6, v6, v2
	v_mul_f32_e32 v7, v7, v3
	v_mul_f32_e32 v8, v8, v4
	v_mul_f32_e32 v9, v9, v5
	v_cvt_pk_fp8_f32 v33, v6, v7
	s_nop 0
	v_cvt_pk_fp8_f32 v33, v8, v9 op_sel:[0,0,1]
	s_nop 1
	global_store_dwordx2 v[250:251], v[32:33], off
	v_lshl_add_u64 v[250:251], v[250:251], 0, s[40:41]
	s_waitcnt vmcnt(28)
	v_mov_b32_e32 v32, v51
	v_mov_b32_e32 v33, v51
	v_lshlrev_b32_e32 v2, 16, v60
	v_and_b32_e32 v3, 0xffff0000, v60
	v_lshlrev_b32_e32 v4, 16, v61
	v_and_b32_e32 v5, 0xffff0000, v61
	v_lshlrev_b32_e32 v6, 16, v56
	v_and_b32_e32 v7, 0xffff0000, v56
	v_lshlrev_b32_e32 v8, 16, v57
	v_and_b32_e32 v9, 0xffff0000, v57
	v_mul_f32_e32 v10, 0xbfb8aa3b, v2
	v_mul_f32_e32 v11, 0xbfb8aa3b, v3
	v_mul_f32_e32 v12, 0xbfb8aa3b, v4
	v_mul_f32_e32 v13, 0xbfb8aa3b, v5
	v_exp_f32_e32 v10, v10
	v_exp_f32_e32 v11, v11
	v_exp_f32_e32 v12, v12
	v_exp_f32_e32 v13, v13
	v_add_f32_e32 v10, 1.0, v10
	v_add_f32_e32 v11, 1.0, v11
	v_add_f32_e32 v12, 1.0, v12
	v_add_f32_e32 v13, 1.0, v13
	v_rcp_f32_e32 v10, v10
	v_rcp_f32_e32 v11, v11
	v_rcp_f32_e32 v12, v12
	v_rcp_f32_e32 v13, v13
	v_mul_f32_e32 v6, v232, v6
	v_mul_f32_e32 v7, v232, v7
	v_mul_f32_e32 v8, v232, v8
	v_mul_f32_e32 v9, v232, v9
	v_mul_f32_e32 v2, v10, v2
	v_mul_f32_e32 v3, v11, v3
	v_mul_f32_e32 v4, v12, v4
	v_mul_f32_e32 v5, v13, v5
	v_mul_f32_e32 v6, v28, v6
	v_mul_f32_e32 v7, v29, v7
	v_mul_f32_e32 v8, v30, v8
	v_mul_f32_e32 v9, v31, v9
	v_mul_f32_e32 v6, v6, v2
	v_mul_f32_e32 v7, v7, v3
	v_mul_f32_e32 v8, v8, v4
	v_mul_f32_e32 v9, v9, v5
	v_cvt_pk_fp8_f32 v32, v6, v7
	s_nop 0
	v_cvt_pk_fp8_f32 v32, v8, v9 op_sel:[0,0,1]
	v_lshlrev_b32_e32 v2, 16, v62
	v_and_b32_e32 v3, 0xffff0000, v62
	v_lshlrev_b32_e32 v4, 16, v63
	v_and_b32_e32 v5, 0xffff0000, v63
	v_lshlrev_b32_e32 v6, 16, v58
	v_and_b32_e32 v7, 0xffff0000, v58
	v_lshlrev_b32_e32 v8, 16, v59
	v_and_b32_e32 v9, 0xffff0000, v59
	v_mul_f32_e32 v10, 0xbfb8aa3b, v2
	v_mul_f32_e32 v11, 0xbfb8aa3b, v3
	v_mul_f32_e32 v12, 0xbfb8aa3b, v4
	v_mul_f32_e32 v13, 0xbfb8aa3b, v5
	v_exp_f32_e32 v10, v10
	v_exp_f32_e32 v11, v11
	v_exp_f32_e32 v12, v12
	v_exp_f32_e32 v13, v13
	v_add_f32_e32 v10, 1.0, v10
	v_add_f32_e32 v11, 1.0, v11
	v_add_f32_e32 v12, 1.0, v12
	v_add_f32_e32 v13, 1.0, v13
	v_rcp_f32_e32 v10, v10
	v_rcp_f32_e32 v11, v11
	v_rcp_f32_e32 v12, v12
	v_rcp_f32_e32 v13, v13
	v_mul_f32_e32 v6, v232, v6
	v_mul_f32_e32 v7, v232, v7
	v_mul_f32_e32 v8, v232, v8
	v_mul_f32_e32 v9, v232, v9
	v_mul_f32_e32 v2, v10, v2
	v_mul_f32_e32 v3, v11, v3
	v_mul_f32_e32 v4, v12, v4
	v_mul_f32_e32 v5, v13, v5
	v_mul_f32_e32 v6, v22, v6
	v_mul_f32_e32 v7, v23, v7
	v_mul_f32_e32 v8, v24, v8
	v_mul_f32_e32 v9, v25, v9
	v_mul_f32_e32 v6, v6, v2
	v_mul_f32_e32 v7, v7, v3
	v_mul_f32_e32 v8, v8, v4
	v_mul_f32_e32 v9, v9, v5
	v_cvt_pk_fp8_f32 v33, v6, v7
	s_nop 0
	v_cvt_pk_fp8_f32 v33, v8, v9 op_sel:[0,0,1]
	s_nop 1
	global_store_dwordx2 v[250:251], v[32:33], off
	v_lshl_add_u64 v[250:251], v[250:251], 0, s[40:41]
	s_waitcnt vmcnt(27)
	v_mov_b32_e32 v32, v51
	v_mov_b32_e32 v33, v51
	v_lshlrev_b32_e32 v2, 16, v68
	v_and_b32_e32 v3, 0xffff0000, v68
	v_lshlrev_b32_e32 v4, 16, v69
	v_and_b32_e32 v5, 0xffff0000, v69
	v_lshlrev_b32_e32 v6, 16, v64
	v_and_b32_e32 v7, 0xffff0000, v64
	v_lshlrev_b32_e32 v8, 16, v65
	v_and_b32_e32 v9, 0xffff0000, v65
	v_mul_f32_e32 v10, 0xbfb8aa3b, v2
	v_mul_f32_e32 v11, 0xbfb8aa3b, v3
	v_mul_f32_e32 v12, 0xbfb8aa3b, v4
	v_mul_f32_e32 v13, 0xbfb8aa3b, v5
	v_exp_f32_e32 v10, v10
	v_exp_f32_e32 v11, v11
	v_exp_f32_e32 v12, v12
	v_exp_f32_e32 v13, v13
	v_add_f32_e32 v10, 1.0, v10
	v_add_f32_e32 v11, 1.0, v11
	v_add_f32_e32 v12, 1.0, v12
	v_add_f32_e32 v13, 1.0, v13
	v_rcp_f32_e32 v10, v10
	v_rcp_f32_e32 v11, v11
	v_rcp_f32_e32 v12, v12
	v_rcp_f32_e32 v13, v13
	v_mul_f32_e32 v6, v233, v6
	v_mul_f32_e32 v7, v233, v7
	v_mul_f32_e32 v8, v233, v8
	v_mul_f32_e32 v9, v233, v9
	v_mul_f32_e32 v2, v10, v2
	v_mul_f32_e32 v3, v11, v3
	v_mul_f32_e32 v4, v12, v4
	v_mul_f32_e32 v5, v13, v5
	v_mul_f32_e32 v6, v28, v6
	v_mul_f32_e32 v7, v29, v7
	v_mul_f32_e32 v8, v30, v8
	v_mul_f32_e32 v9, v31, v9
	v_mul_f32_e32 v6, v6, v2
	v_mul_f32_e32 v7, v7, v3
	v_mul_f32_e32 v8, v8, v4
	v_mul_f32_e32 v9, v9, v5
	v_cvt_pk_fp8_f32 v32, v6, v7
	s_nop 0
	v_cvt_pk_fp8_f32 v32, v8, v9 op_sel:[0,0,1]
	v_lshlrev_b32_e32 v2, 16, v70
	v_and_b32_e32 v3, 0xffff0000, v70
	v_lshlrev_b32_e32 v4, 16, v71
	v_and_b32_e32 v5, 0xffff0000, v71
	v_lshlrev_b32_e32 v6, 16, v66
	v_and_b32_e32 v7, 0xffff0000, v66
	v_lshlrev_b32_e32 v8, 16, v67
	v_and_b32_e32 v9, 0xffff0000, v67
	v_mul_f32_e32 v10, 0xbfb8aa3b, v2
	v_mul_f32_e32 v11, 0xbfb8aa3b, v3
	v_mul_f32_e32 v12, 0xbfb8aa3b, v4
	v_mul_f32_e32 v13, 0xbfb8aa3b, v5
	v_exp_f32_e32 v10, v10
	v_exp_f32_e32 v11, v11
	v_exp_f32_e32 v12, v12
	v_exp_f32_e32 v13, v13
	v_add_f32_e32 v10, 1.0, v10
	v_add_f32_e32 v11, 1.0, v11
	v_add_f32_e32 v12, 1.0, v12
	v_add_f32_e32 v13, 1.0, v13
	v_rcp_f32_e32 v10, v10
	v_rcp_f32_e32 v11, v11
	v_rcp_f32_e32 v12, v12
	v_rcp_f32_e32 v13, v13
	v_mul_f32_e32 v6, v233, v6
	v_mul_f32_e32 v7, v233, v7
	v_mul_f32_e32 v8, v233, v8
	v_mul_f32_e32 v9, v233, v9
	v_mul_f32_e32 v2, v10, v2
	v_mul_f32_e32 v3, v11, v3
	v_mul_f32_e32 v4, v12, v4
	v_mul_f32_e32 v5, v13, v5
	v_mul_f32_e32 v6, v22, v6
	v_mul_f32_e32 v7, v23, v7
	v_mul_f32_e32 v8, v24, v8
	v_mul_f32_e32 v9, v25, v9
	v_mul_f32_e32 v6, v6, v2
	v_mul_f32_e32 v7, v7, v3
	v_mul_f32_e32 v8, v8, v4
	v_mul_f32_e32 v9, v9, v5
	v_cvt_pk_fp8_f32 v33, v6, v7
	s_nop 0
	v_cvt_pk_fp8_f32 v33, v8, v9 op_sel:[0,0,1]
	s_nop 1
	global_store_dwordx2 v[250:251], v[32:33], off
	v_lshl_add_u64 v[250:251], v[250:251], 0, s[40:41]
	s_waitcnt vmcnt(26)
	v_mov_b32_e32 v32, v51
	v_mov_b32_e32 v33, v51
	v_lshlrev_b32_e32 v2, 16, v76
	v_and_b32_e32 v3, 0xffff0000, v76
	v_lshlrev_b32_e32 v4, 16, v77
	v_and_b32_e32 v5, 0xffff0000, v77
	v_lshlrev_b32_e32 v6, 16, v72
	v_and_b32_e32 v7, 0xffff0000, v72
	v_lshlrev_b32_e32 v8, 16, v73
	v_and_b32_e32 v9, 0xffff0000, v73
	v_mul_f32_e32 v10, 0xbfb8aa3b, v2
	v_mul_f32_e32 v11, 0xbfb8aa3b, v3
	v_mul_f32_e32 v12, 0xbfb8aa3b, v4
	v_mul_f32_e32 v13, 0xbfb8aa3b, v5
	v_exp_f32_e32 v10, v10
	v_exp_f32_e32 v11, v11
	v_exp_f32_e32 v12, v12
	v_exp_f32_e32 v13, v13
	v_add_f32_e32 v10, 1.0, v10
	v_add_f32_e32 v11, 1.0, v11
	v_add_f32_e32 v12, 1.0, v12
	v_add_f32_e32 v13, 1.0, v13
	v_rcp_f32_e32 v10, v10
	v_rcp_f32_e32 v11, v11
	v_rcp_f32_e32 v12, v12
	v_rcp_f32_e32 v13, v13
	v_mul_f32_e32 v6, v234, v6
	v_mul_f32_e32 v7, v234, v7
	v_mul_f32_e32 v8, v234, v8
	v_mul_f32_e32 v9, v234, v9
	v_mul_f32_e32 v2, v10, v2
	v_mul_f32_e32 v3, v11, v3
	v_mul_f32_e32 v4, v12, v4
	v_mul_f32_e32 v5, v13, v5
	v_mul_f32_e32 v6, v28, v6
	v_mul_f32_e32 v7, v29, v7
	v_mul_f32_e32 v8, v30, v8
	v_mul_f32_e32 v9, v31, v9
	v_mul_f32_e32 v6, v6, v2
	v_mul_f32_e32 v7, v7, v3
	v_mul_f32_e32 v8, v8, v4
	v_mul_f32_e32 v9, v9, v5
	v_cvt_pk_fp8_f32 v32, v6, v7
	s_nop 0
	v_cvt_pk_fp8_f32 v32, v8, v9 op_sel:[0,0,1]
	v_lshlrev_b32_e32 v2, 16, v78
	v_and_b32_e32 v3, 0xffff0000, v78
	v_lshlrev_b32_e32 v4, 16, v79
	v_and_b32_e32 v5, 0xffff0000, v79
	v_lshlrev_b32_e32 v6, 16, v74
	v_and_b32_e32 v7, 0xffff0000, v74
	v_lshlrev_b32_e32 v8, 16, v75
	v_and_b32_e32 v9, 0xffff0000, v75
	v_mul_f32_e32 v10, 0xbfb8aa3b, v2
	v_mul_f32_e32 v11, 0xbfb8aa3b, v3
	v_mul_f32_e32 v12, 0xbfb8aa3b, v4
	v_mul_f32_e32 v13, 0xbfb8aa3b, v5
	v_exp_f32_e32 v10, v10
	v_exp_f32_e32 v11, v11
	v_exp_f32_e32 v12, v12
	v_exp_f32_e32 v13, v13
	v_add_f32_e32 v10, 1.0, v10
	v_add_f32_e32 v11, 1.0, v11
	v_add_f32_e32 v12, 1.0, v12
	v_add_f32_e32 v13, 1.0, v13
	v_rcp_f32_e32 v10, v10
	v_rcp_f32_e32 v11, v11
	v_rcp_f32_e32 v12, v12
	v_rcp_f32_e32 v13, v13
	v_mul_f32_e32 v6, v234, v6
	v_mul_f32_e32 v7, v234, v7
	v_mul_f32_e32 v8, v234, v8
	v_mul_f32_e32 v9, v234, v9
	v_mul_f32_e32 v2, v10, v2
	v_mul_f32_e32 v3, v11, v3
	v_mul_f32_e32 v4, v12, v4
	v_mul_f32_e32 v5, v13, v5
	v_mul_f32_e32 v6, v22, v6
	v_mul_f32_e32 v7, v23, v7
	v_mul_f32_e32 v8, v24, v8
	v_mul_f32_e32 v9, v25, v9
	v_mul_f32_e32 v6, v6, v2
	v_mul_f32_e32 v7, v7, v3
	v_mul_f32_e32 v8, v8, v4
	v_mul_f32_e32 v9, v9, v5
	v_cvt_pk_fp8_f32 v33, v6, v7
	s_nop 0
	v_cvt_pk_fp8_f32 v33, v8, v9 op_sel:[0,0,1]
	s_nop 1
	global_store_dwordx2 v[250:251], v[32:33], off
	v_lshl_add_u64 v[250:251], v[250:251], 0, s[40:41]
	s_waitcnt vmcnt(25)
	v_mov_b32_e32 v32, v51
	v_mov_b32_e32 v33, v51
	v_lshlrev_b32_e32 v2, 16, v130
	v_and_b32_e32 v3, 0xffff0000, v130
	v_lshlrev_b32_e32 v4, 16, v131
	v_and_b32_e32 v5, 0xffff0000, v131
	v_lshlrev_b32_e32 v6, 16, v126
	v_and_b32_e32 v7, 0xffff0000, v126
	v_lshlrev_b32_e32 v8, 16, v127
	v_and_b32_e32 v9, 0xffff0000, v127
	v_mul_f32_e32 v10, 0xbfb8aa3b, v2
	v_mul_f32_e32 v11, 0xbfb8aa3b, v3
	v_mul_f32_e32 v12, 0xbfb8aa3b, v4
	v_mul_f32_e32 v13, 0xbfb8aa3b, v5
	v_exp_f32_e32 v10, v10
	v_exp_f32_e32 v11, v11
	v_exp_f32_e32 v12, v12
	v_exp_f32_e32 v13, v13
	v_add_f32_e32 v10, 1.0, v10
	v_add_f32_e32 v11, 1.0, v11
	v_add_f32_e32 v12, 1.0, v12
	v_add_f32_e32 v13, 1.0, v13
	v_rcp_f32_e32 v10, v10
	v_rcp_f32_e32 v11, v11
	v_rcp_f32_e32 v12, v12
	v_rcp_f32_e32 v13, v13
	v_mul_f32_e32 v6, v235, v6
	v_mul_f32_e32 v7, v235, v7
	v_mul_f32_e32 v8, v235, v8
	v_mul_f32_e32 v9, v235, v9
	v_mul_f32_e32 v2, v10, v2
	v_mul_f32_e32 v3, v11, v3
	v_mul_f32_e32 v4, v12, v4
	v_mul_f32_e32 v5, v13, v5
	v_mul_f32_e32 v6, v28, v6
	v_mul_f32_e32 v7, v29, v7
	v_mul_f32_e32 v8, v30, v8
	v_mul_f32_e32 v9, v31, v9
	v_mul_f32_e32 v6, v6, v2
	v_mul_f32_e32 v7, v7, v3
	v_mul_f32_e32 v8, v8, v4
	v_mul_f32_e32 v9, v9, v5
	v_cvt_pk_fp8_f32 v32, v6, v7
	s_nop 0
	v_cvt_pk_fp8_f32 v32, v8, v9 op_sel:[0,0,1]
	v_lshlrev_b32_e32 v2, 16, v132
	v_and_b32_e32 v3, 0xffff0000, v132
	v_lshlrev_b32_e32 v4, 16, v133
	v_and_b32_e32 v5, 0xffff0000, v133
	v_lshlrev_b32_e32 v6, 16, v128
	v_and_b32_e32 v7, 0xffff0000, v128
	v_lshlrev_b32_e32 v8, 16, v129
	v_and_b32_e32 v9, 0xffff0000, v129
	v_mul_f32_e32 v10, 0xbfb8aa3b, v2
	v_mul_f32_e32 v11, 0xbfb8aa3b, v3
	v_mul_f32_e32 v12, 0xbfb8aa3b, v4
	v_mul_f32_e32 v13, 0xbfb8aa3b, v5
	v_exp_f32_e32 v10, v10
	v_exp_f32_e32 v11, v11
	v_exp_f32_e32 v12, v12
	v_exp_f32_e32 v13, v13
	v_add_f32_e32 v10, 1.0, v10
	v_add_f32_e32 v11, 1.0, v11
	v_add_f32_e32 v12, 1.0, v12
	v_add_f32_e32 v13, 1.0, v13
	v_rcp_f32_e32 v10, v10
	v_rcp_f32_e32 v11, v11
	v_rcp_f32_e32 v12, v12
	v_rcp_f32_e32 v13, v13
	v_mul_f32_e32 v6, v235, v6
	v_mul_f32_e32 v7, v235, v7
	v_mul_f32_e32 v8, v235, v8
	v_mul_f32_e32 v9, v235, v9
	v_mul_f32_e32 v2, v10, v2
	v_mul_f32_e32 v3, v11, v3
	v_mul_f32_e32 v4, v12, v4
	v_mul_f32_e32 v5, v13, v5
	v_mul_f32_e32 v6, v22, v6
	v_mul_f32_e32 v7, v23, v7
	v_mul_f32_e32 v8, v24, v8
	v_mul_f32_e32 v9, v25, v9
	v_mul_f32_e32 v6, v6, v2
	v_mul_f32_e32 v7, v7, v3
	v_mul_f32_e32 v8, v8, v4
	v_mul_f32_e32 v9, v9, v5
	v_cvt_pk_fp8_f32 v33, v6, v7
	s_nop 0
	v_cvt_pk_fp8_f32 v33, v8, v9 op_sel:[0,0,1]
	s_nop 1
	global_store_dwordx2 v[250:251], v[32:33], off
	v_lshl_add_u64 v[250:251], v[250:251], 0, s[40:41]
	s_waitcnt vmcnt(24)
	v_mov_b32_e32 v32, v51
	v_mov_b32_e32 v33, v51
	v_lshlrev_b32_e32 v2, 16, v138
	v_and_b32_e32 v3, 0xffff0000, v138
	v_lshlrev_b32_e32 v4, 16, v139
	v_and_b32_e32 v5, 0xffff0000, v139
	v_lshlrev_b32_e32 v6, 16, v134
	v_and_b32_e32 v7, 0xffff0000, v134
	v_lshlrev_b32_e32 v8, 16, v135
	v_and_b32_e32 v9, 0xffff0000, v135
	v_mul_f32_e32 v10, 0xbfb8aa3b, v2
	v_mul_f32_e32 v11, 0xbfb8aa3b, v3
	v_mul_f32_e32 v12, 0xbfb8aa3b, v4
	v_mul_f32_e32 v13, 0xbfb8aa3b, v5
	v_exp_f32_e32 v10, v10
	v_exp_f32_e32 v11, v11
	v_exp_f32_e32 v12, v12
	v_exp_f32_e32 v13, v13
	v_add_f32_e32 v10, 1.0, v10
	v_add_f32_e32 v11, 1.0, v11
	v_add_f32_e32 v12, 1.0, v12
	v_add_f32_e32 v13, 1.0, v13
	v_rcp_f32_e32 v10, v10
	v_rcp_f32_e32 v11, v11
	v_rcp_f32_e32 v12, v12
	v_rcp_f32_e32 v13, v13
	v_mul_f32_e32 v6, v236, v6
	v_mul_f32_e32 v7, v236, v7
	v_mul_f32_e32 v8, v236, v8
	v_mul_f32_e32 v9, v236, v9
	v_mul_f32_e32 v2, v10, v2
	v_mul_f32_e32 v3, v11, v3
	v_mul_f32_e32 v4, v12, v4
	v_mul_f32_e32 v5, v13, v5
	v_mul_f32_e32 v6, v28, v6
	v_mul_f32_e32 v7, v29, v7
	v_mul_f32_e32 v8, v30, v8
	v_mul_f32_e32 v9, v31, v9
	v_mul_f32_e32 v6, v6, v2
	v_mul_f32_e32 v7, v7, v3
	v_mul_f32_e32 v8, v8, v4
	v_mul_f32_e32 v9, v9, v5
	v_cvt_pk_fp8_f32 v32, v6, v7
	s_nop 0
	v_cvt_pk_fp8_f32 v32, v8, v9 op_sel:[0,0,1]
	v_lshlrev_b32_e32 v2, 16, v140
	v_and_b32_e32 v3, 0xffff0000, v140
	v_lshlrev_b32_e32 v4, 16, v141
	v_and_b32_e32 v5, 0xffff0000, v141
	v_lshlrev_b32_e32 v6, 16, v136
	v_and_b32_e32 v7, 0xffff0000, v136
	v_lshlrev_b32_e32 v8, 16, v137
	v_and_b32_e32 v9, 0xffff0000, v137
	v_mul_f32_e32 v10, 0xbfb8aa3b, v2
	v_mul_f32_e32 v11, 0xbfb8aa3b, v3
	v_mul_f32_e32 v12, 0xbfb8aa3b, v4
	v_mul_f32_e32 v13, 0xbfb8aa3b, v5
	v_exp_f32_e32 v10, v10
	v_exp_f32_e32 v11, v11
	v_exp_f32_e32 v12, v12
	v_exp_f32_e32 v13, v13
	v_add_f32_e32 v10, 1.0, v10
	v_add_f32_e32 v11, 1.0, v11
	v_add_f32_e32 v12, 1.0, v12
	v_add_f32_e32 v13, 1.0, v13
	v_rcp_f32_e32 v10, v10
	v_rcp_f32_e32 v11, v11
	v_rcp_f32_e32 v12, v12
	v_rcp_f32_e32 v13, v13
	v_mul_f32_e32 v6, v236, v6
	v_mul_f32_e32 v7, v236, v7
	v_mul_f32_e32 v8, v236, v8
	v_mul_f32_e32 v9, v236, v9
	v_mul_f32_e32 v2, v10, v2
	v_mul_f32_e32 v3, v11, v3
	v_mul_f32_e32 v4, v12, v4
	v_mul_f32_e32 v5, v13, v5
	v_mul_f32_e32 v6, v22, v6
	v_mul_f32_e32 v7, v23, v7
	v_mul_f32_e32 v8, v24, v8
	v_mul_f32_e32 v9, v25, v9
	v_mul_f32_e32 v6, v6, v2
	v_mul_f32_e32 v7, v7, v3
	v_mul_f32_e32 v8, v8, v4
	v_mul_f32_e32 v9, v9, v5
	v_cvt_pk_fp8_f32 v33, v6, v7
	s_nop 0
	v_cvt_pk_fp8_f32 v33, v8, v9 op_sel:[0,0,1]
	s_nop 1
	global_store_dwordx2 v[250:251], v[32:33], off
	v_lshl_add_u64 v[250:251], v[250:251], 0, s[40:41]
	s_waitcnt vmcnt(23)
	v_mov_b32_e32 v32, v51
	v_mov_b32_e32 v33, v51
	v_lshlrev_b32_e32 v2, 16, v154
	v_and_b32_e32 v3, 0xffff0000, v154
	v_lshlrev_b32_e32 v4, 16, v155
	v_and_b32_e32 v5, 0xffff0000, v155
	v_lshlrev_b32_e32 v6, 16, v150
	v_and_b32_e32 v7, 0xffff0000, v150
	v_lshlrev_b32_e32 v8, 16, v151
	v_and_b32_e32 v9, 0xffff0000, v151
	v_mul_f32_e32 v10, 0xbfb8aa3b, v2
	v_mul_f32_e32 v11, 0xbfb8aa3b, v3
	v_mul_f32_e32 v12, 0xbfb8aa3b, v4
	v_mul_f32_e32 v13, 0xbfb8aa3b, v5
	v_exp_f32_e32 v10, v10
	v_exp_f32_e32 v11, v11
	v_exp_f32_e32 v12, v12
	v_exp_f32_e32 v13, v13
	v_add_f32_e32 v10, 1.0, v10
	v_add_f32_e32 v11, 1.0, v11
	v_add_f32_e32 v12, 1.0, v12
	v_add_f32_e32 v13, 1.0, v13
	v_rcp_f32_e32 v10, v10
	v_rcp_f32_e32 v11, v11
	v_rcp_f32_e32 v12, v12
	v_rcp_f32_e32 v13, v13
	v_mul_f32_e32 v6, v237, v6
	v_mul_f32_e32 v7, v237, v7
	v_mul_f32_e32 v8, v237, v8
	v_mul_f32_e32 v9, v237, v9
	v_mul_f32_e32 v2, v10, v2
	v_mul_f32_e32 v3, v11, v3
	v_mul_f32_e32 v4, v12, v4
	v_mul_f32_e32 v5, v13, v5
	v_mul_f32_e32 v6, v28, v6
	v_mul_f32_e32 v7, v29, v7
	v_mul_f32_e32 v8, v30, v8
	v_mul_f32_e32 v9, v31, v9
	v_mul_f32_e32 v6, v6, v2
	v_mul_f32_e32 v7, v7, v3
	v_mul_f32_e32 v8, v8, v4
	v_mul_f32_e32 v9, v9, v5
	v_cvt_pk_fp8_f32 v32, v6, v7
	s_nop 0
	v_cvt_pk_fp8_f32 v32, v8, v9 op_sel:[0,0,1]
	v_lshlrev_b32_e32 v2, 16, v156
	v_and_b32_e32 v3, 0xffff0000, v156
	v_lshlrev_b32_e32 v4, 16, v157
	v_and_b32_e32 v5, 0xffff0000, v157
	v_lshlrev_b32_e32 v6, 16, v152
	v_and_b32_e32 v7, 0xffff0000, v152
	v_lshlrev_b32_e32 v8, 16, v153
	v_and_b32_e32 v9, 0xffff0000, v153
	v_mul_f32_e32 v10, 0xbfb8aa3b, v2
	v_mul_f32_e32 v11, 0xbfb8aa3b, v3
	v_mul_f32_e32 v12, 0xbfb8aa3b, v4
	v_mul_f32_e32 v13, 0xbfb8aa3b, v5
	v_exp_f32_e32 v10, v10
	v_exp_f32_e32 v11, v11
	v_exp_f32_e32 v12, v12
	v_exp_f32_e32 v13, v13
	v_add_f32_e32 v10, 1.0, v10
	v_add_f32_e32 v11, 1.0, v11
	v_add_f32_e32 v12, 1.0, v12
	v_add_f32_e32 v13, 1.0, v13
	v_rcp_f32_e32 v10, v10
	v_rcp_f32_e32 v11, v11
	v_rcp_f32_e32 v12, v12
	v_rcp_f32_e32 v13, v13
	v_mul_f32_e32 v6, v237, v6
	v_mul_f32_e32 v7, v237, v7
	v_mul_f32_e32 v8, v237, v8
	v_mul_f32_e32 v9, v237, v9
	v_mul_f32_e32 v2, v10, v2
	v_mul_f32_e32 v3, v11, v3
	v_mul_f32_e32 v4, v12, v4
	v_mul_f32_e32 v5, v13, v5
	v_mul_f32_e32 v6, v22, v6
	v_mul_f32_e32 v7, v23, v7
	v_mul_f32_e32 v8, v24, v8
	v_mul_f32_e32 v9, v25, v9
	v_mul_f32_e32 v6, v6, v2
	v_mul_f32_e32 v7, v7, v3
	v_mul_f32_e32 v8, v8, v4
	v_mul_f32_e32 v9, v9, v5
	v_cvt_pk_fp8_f32 v33, v6, v7
	s_nop 0
	v_cvt_pk_fp8_f32 v33, v8, v9 op_sel:[0,0,1]
	s_nop 1
	global_store_dwordx2 v[250:251], v[32:33], off
	v_lshl_add_u64 v[250:251], v[250:251], 0, s[40:41]
	s_waitcnt vmcnt(22)
	v_mov_b32_e32 v32, v51
	v_mov_b32_e32 v33, v51
	v_lshlrev_b32_e32 v2, 16, v162
	v_and_b32_e32 v3, 0xffff0000, v162
	v_lshlrev_b32_e32 v4, 16, v163
	v_and_b32_e32 v5, 0xffff0000, v163
	v_lshlrev_b32_e32 v6, 16, v158
	v_and_b32_e32 v7, 0xffff0000, v158
	v_lshlrev_b32_e32 v8, 16, v159
	v_and_b32_e32 v9, 0xffff0000, v159
	v_mul_f32_e32 v10, 0xbfb8aa3b, v2
	v_mul_f32_e32 v11, 0xbfb8aa3b, v3
	v_mul_f32_e32 v12, 0xbfb8aa3b, v4
	v_mul_f32_e32 v13, 0xbfb8aa3b, v5
	v_exp_f32_e32 v10, v10
	v_exp_f32_e32 v11, v11
	v_exp_f32_e32 v12, v12
	v_exp_f32_e32 v13, v13
	v_add_f32_e32 v10, 1.0, v10
	v_add_f32_e32 v11, 1.0, v11
	v_add_f32_e32 v12, 1.0, v12
	v_add_f32_e32 v13, 1.0, v13
	v_rcp_f32_e32 v10, v10
	v_rcp_f32_e32 v11, v11
	v_rcp_f32_e32 v12, v12
	v_rcp_f32_e32 v13, v13
	v_mul_f32_e32 v6, v238, v6
	v_mul_f32_e32 v7, v238, v7
	v_mul_f32_e32 v8, v238, v8
	v_mul_f32_e32 v9, v238, v9
	v_mul_f32_e32 v2, v10, v2
	v_mul_f32_e32 v3, v11, v3
	v_mul_f32_e32 v4, v12, v4
	v_mul_f32_e32 v5, v13, v5
	v_mul_f32_e32 v6, v28, v6
	v_mul_f32_e32 v7, v29, v7
	v_mul_f32_e32 v8, v30, v8
	v_mul_f32_e32 v9, v31, v9
	v_mul_f32_e32 v6, v6, v2
	v_mul_f32_e32 v7, v7, v3
	v_mul_f32_e32 v8, v8, v4
	v_mul_f32_e32 v9, v9, v5
	v_cvt_pk_fp8_f32 v32, v6, v7
	s_nop 0
	v_cvt_pk_fp8_f32 v32, v8, v9 op_sel:[0,0,1]
	v_lshlrev_b32_e32 v2, 16, v164
	v_and_b32_e32 v3, 0xffff0000, v164
	v_lshlrev_b32_e32 v4, 16, v165
	v_and_b32_e32 v5, 0xffff0000, v165
	v_lshlrev_b32_e32 v6, 16, v160
	v_and_b32_e32 v7, 0xffff0000, v160
	v_lshlrev_b32_e32 v8, 16, v161
	v_and_b32_e32 v9, 0xffff0000, v161
	v_mul_f32_e32 v10, 0xbfb8aa3b, v2
	v_mul_f32_e32 v11, 0xbfb8aa3b, v3
	v_mul_f32_e32 v12, 0xbfb8aa3b, v4
	v_mul_f32_e32 v13, 0xbfb8aa3b, v5
	v_exp_f32_e32 v10, v10
	v_exp_f32_e32 v11, v11
	v_exp_f32_e32 v12, v12
	v_exp_f32_e32 v13, v13
	v_add_f32_e32 v10, 1.0, v10
	v_add_f32_e32 v11, 1.0, v11
	v_add_f32_e32 v12, 1.0, v12
	v_add_f32_e32 v13, 1.0, v13
	v_rcp_f32_e32 v10, v10
	v_rcp_f32_e32 v11, v11
	v_rcp_f32_e32 v12, v12
	v_rcp_f32_e32 v13, v13
	v_mul_f32_e32 v6, v238, v6
	v_mul_f32_e32 v7, v238, v7
	v_mul_f32_e32 v8, v238, v8
	v_mul_f32_e32 v9, v238, v9
	v_mul_f32_e32 v2, v10, v2
	v_mul_f32_e32 v3, v11, v3
	v_mul_f32_e32 v4, v12, v4
	v_mul_f32_e32 v5, v13, v5
	v_mul_f32_e32 v6, v22, v6
	v_mul_f32_e32 v7, v23, v7
	v_mul_f32_e32 v8, v24, v8
	v_mul_f32_e32 v9, v25, v9
	v_mul_f32_e32 v6, v6, v2
	v_mul_f32_e32 v7, v7, v3
	v_mul_f32_e32 v8, v8, v4
	v_mul_f32_e32 v9, v9, v5
	v_cvt_pk_fp8_f32 v33, v6, v7
	s_nop 0
	v_cvt_pk_fp8_f32 v33, v8, v9 op_sel:[0,0,1]
	s_nop 1
	global_store_dwordx2 v[250:251], v[32:33], off
	v_lshl_add_u64 v[250:251], v[250:251], 0, s[40:41]
	s_waitcnt vmcnt(21)
	v_mov_b32_e32 v32, v51
	v_mov_b32_e32 v33, v51
	v_lshlrev_b32_e32 v2, 16, v170
	v_and_b32_e32 v3, 0xffff0000, v170
	v_lshlrev_b32_e32 v4, 16, v171
	v_and_b32_e32 v5, 0xffff0000, v171
	v_lshlrev_b32_e32 v6, 16, v166
	v_and_b32_e32 v7, 0xffff0000, v166
	v_lshlrev_b32_e32 v8, 16, v167
	v_and_b32_e32 v9, 0xffff0000, v167
	v_mul_f32_e32 v10, 0xbfb8aa3b, v2
	v_mul_f32_e32 v11, 0xbfb8aa3b, v3
	v_mul_f32_e32 v12, 0xbfb8aa3b, v4
	v_mul_f32_e32 v13, 0xbfb8aa3b, v5
	v_exp_f32_e32 v10, v10
	v_exp_f32_e32 v11, v11
	v_exp_f32_e32 v12, v12
	v_exp_f32_e32 v13, v13
	v_add_f32_e32 v10, 1.0, v10
	v_add_f32_e32 v11, 1.0, v11
	v_add_f32_e32 v12, 1.0, v12
	v_add_f32_e32 v13, 1.0, v13
	v_rcp_f32_e32 v10, v10
	v_rcp_f32_e32 v11, v11
	v_rcp_f32_e32 v12, v12
	v_rcp_f32_e32 v13, v13
	v_mul_f32_e32 v6, v239, v6
	v_mul_f32_e32 v7, v239, v7
	v_mul_f32_e32 v8, v239, v8
	v_mul_f32_e32 v9, v239, v9
	v_mul_f32_e32 v2, v10, v2
	v_mul_f32_e32 v3, v11, v3
	v_mul_f32_e32 v4, v12, v4
	v_mul_f32_e32 v5, v13, v5
	v_mul_f32_e32 v6, v28, v6
	v_mul_f32_e32 v7, v29, v7
	v_mul_f32_e32 v8, v30, v8
	v_mul_f32_e32 v9, v31, v9
	v_mul_f32_e32 v6, v6, v2
	v_mul_f32_e32 v7, v7, v3
	v_mul_f32_e32 v8, v8, v4
	v_mul_f32_e32 v9, v9, v5
	v_cvt_pk_fp8_f32 v32, v6, v7
	s_nop 0
	v_cvt_pk_fp8_f32 v32, v8, v9 op_sel:[0,0,1]
	v_lshlrev_b32_e32 v2, 16, v172
	v_and_b32_e32 v3, 0xffff0000, v172
	v_lshlrev_b32_e32 v4, 16, v173
	v_and_b32_e32 v5, 0xffff0000, v173
	v_lshlrev_b32_e32 v6, 16, v168
	v_and_b32_e32 v7, 0xffff0000, v168
	v_lshlrev_b32_e32 v8, 16, v169
	v_and_b32_e32 v9, 0xffff0000, v169
	v_mul_f32_e32 v10, 0xbfb8aa3b, v2
	v_mul_f32_e32 v11, 0xbfb8aa3b, v3
	v_mul_f32_e32 v12, 0xbfb8aa3b, v4
	v_mul_f32_e32 v13, 0xbfb8aa3b, v5
	v_exp_f32_e32 v10, v10
	v_exp_f32_e32 v11, v11
	v_exp_f32_e32 v12, v12
	v_exp_f32_e32 v13, v13
	v_add_f32_e32 v10, 1.0, v10
	v_add_f32_e32 v11, 1.0, v11
	v_add_f32_e32 v12, 1.0, v12
	v_add_f32_e32 v13, 1.0, v13
	v_rcp_f32_e32 v10, v10
	v_rcp_f32_e32 v11, v11
	v_rcp_f32_e32 v12, v12
	v_rcp_f32_e32 v13, v13
	v_mul_f32_e32 v6, v239, v6
	v_mul_f32_e32 v7, v239, v7
	v_mul_f32_e32 v8, v239, v8
	v_mul_f32_e32 v9, v239, v9
	v_mul_f32_e32 v2, v10, v2
	v_mul_f32_e32 v3, v11, v3
	v_mul_f32_e32 v4, v12, v4
	v_mul_f32_e32 v5, v13, v5
	v_mul_f32_e32 v6, v22, v6
	v_mul_f32_e32 v7, v23, v7
	v_mul_f32_e32 v8, v24, v8
	v_mul_f32_e32 v9, v25, v9
	v_mul_f32_e32 v6, v6, v2
	v_mul_f32_e32 v7, v7, v3
	v_mul_f32_e32 v8, v8, v4
	v_mul_f32_e32 v9, v9, v5
	v_cvt_pk_fp8_f32 v33, v6, v7
	s_nop 0
	v_cvt_pk_fp8_f32 v33, v8, v9 op_sel:[0,0,1]
	s_nop 1
	global_store_dwordx2 v[250:251], v[32:33], off
	v_lshl_add_u64 v[250:251], v[250:251], 0, s[40:41]
	s_waitcnt vmcnt(20)
	v_mov_b32_e32 v32, v51
	v_mov_b32_e32 v33, v51
	v_lshlrev_b32_e32 v2, 16, v186
	v_and_b32_e32 v3, 0xffff0000, v186
	v_lshlrev_b32_e32 v4, 16, v187
	v_and_b32_e32 v5, 0xffff0000, v187
	v_lshlrev_b32_e32 v6, 16, v182
	v_and_b32_e32 v7, 0xffff0000, v182
	v_lshlrev_b32_e32 v8, 16, v183
	v_and_b32_e32 v9, 0xffff0000, v183
	v_mul_f32_e32 v10, 0xbfb8aa3b, v2
	v_mul_f32_e32 v11, 0xbfb8aa3b, v3
	v_mul_f32_e32 v12, 0xbfb8aa3b, v4
	v_mul_f32_e32 v13, 0xbfb8aa3b, v5
	v_exp_f32_e32 v10, v10
	v_exp_f32_e32 v11, v11
	v_exp_f32_e32 v12, v12
	v_exp_f32_e32 v13, v13
	v_add_f32_e32 v10, 1.0, v10
	v_add_f32_e32 v11, 1.0, v11
	v_add_f32_e32 v12, 1.0, v12
	v_add_f32_e32 v13, 1.0, v13
	v_rcp_f32_e32 v10, v10
	v_rcp_f32_e32 v11, v11
	v_rcp_f32_e32 v12, v12
	v_rcp_f32_e32 v13, v13
	v_mul_f32_e32 v6, v240, v6
	v_mul_f32_e32 v7, v240, v7
	v_mul_f32_e32 v8, v240, v8
	v_mul_f32_e32 v9, v240, v9
	v_mul_f32_e32 v2, v10, v2
	v_mul_f32_e32 v3, v11, v3
	v_mul_f32_e32 v4, v12, v4
	v_mul_f32_e32 v5, v13, v5
	v_mul_f32_e32 v6, v28, v6
	v_mul_f32_e32 v7, v29, v7
	v_mul_f32_e32 v8, v30, v8
	v_mul_f32_e32 v9, v31, v9
	v_mul_f32_e32 v6, v6, v2
	v_mul_f32_e32 v7, v7, v3
	v_mul_f32_e32 v8, v8, v4
	v_mul_f32_e32 v9, v9, v5
	v_cvt_pk_fp8_f32 v32, v6, v7
	s_nop 0
	v_cvt_pk_fp8_f32 v32, v8, v9 op_sel:[0,0,1]
	v_lshlrev_b32_e32 v2, 16, v188
	v_and_b32_e32 v3, 0xffff0000, v188
	v_lshlrev_b32_e32 v4, 16, v189
	v_and_b32_e32 v5, 0xffff0000, v189
	v_lshlrev_b32_e32 v6, 16, v184
	v_and_b32_e32 v7, 0xffff0000, v184
	v_lshlrev_b32_e32 v8, 16, v185
	v_and_b32_e32 v9, 0xffff0000, v185
	v_mul_f32_e32 v10, 0xbfb8aa3b, v2
	v_mul_f32_e32 v11, 0xbfb8aa3b, v3
	v_mul_f32_e32 v12, 0xbfb8aa3b, v4
	v_mul_f32_e32 v13, 0xbfb8aa3b, v5
	v_exp_f32_e32 v10, v10
	v_exp_f32_e32 v11, v11
	v_exp_f32_e32 v12, v12
	v_exp_f32_e32 v13, v13
	v_add_f32_e32 v10, 1.0, v10
	v_add_f32_e32 v11, 1.0, v11
	v_add_f32_e32 v12, 1.0, v12
	v_add_f32_e32 v13, 1.0, v13
	v_rcp_f32_e32 v10, v10
	v_rcp_f32_e32 v11, v11
	v_rcp_f32_e32 v12, v12
	v_rcp_f32_e32 v13, v13
	v_mul_f32_e32 v6, v240, v6
	v_mul_f32_e32 v7, v240, v7
	v_mul_f32_e32 v8, v240, v8
	v_mul_f32_e32 v9, v240, v9
	v_mul_f32_e32 v2, v10, v2
	v_mul_f32_e32 v3, v11, v3
	v_mul_f32_e32 v4, v12, v4
	v_mul_f32_e32 v5, v13, v5
	v_mul_f32_e32 v6, v22, v6
	v_mul_f32_e32 v7, v23, v7
	v_mul_f32_e32 v8, v24, v8
	v_mul_f32_e32 v9, v25, v9
	v_mul_f32_e32 v6, v6, v2
	v_mul_f32_e32 v7, v7, v3
	v_mul_f32_e32 v8, v8, v4
	v_mul_f32_e32 v9, v9, v5
	v_cvt_pk_fp8_f32 v33, v6, v7
	s_nop 0
	v_cvt_pk_fp8_f32 v33, v8, v9 op_sel:[0,0,1]
	s_nop 1
	global_store_dwordx2 v[250:251], v[32:33], off
	v_lshl_add_u64 v[250:251], v[250:251], 0, s[40:41]
	s_waitcnt vmcnt(19)
	v_mov_b32_e32 v32, v51
	v_mov_b32_e32 v33, v51
	v_lshlrev_b32_e32 v2, 16, v194
	v_and_b32_e32 v3, 0xffff0000, v194
	v_lshlrev_b32_e32 v4, 16, v195
	v_and_b32_e32 v5, 0xffff0000, v195
	v_lshlrev_b32_e32 v6, 16, v190
	v_and_b32_e32 v7, 0xffff0000, v190
	v_lshlrev_b32_e32 v8, 16, v191
	v_and_b32_e32 v9, 0xffff0000, v191
	v_mul_f32_e32 v10, 0xbfb8aa3b, v2
	v_mul_f32_e32 v11, 0xbfb8aa3b, v3
	v_mul_f32_e32 v12, 0xbfb8aa3b, v4
	v_mul_f32_e32 v13, 0xbfb8aa3b, v5
	v_exp_f32_e32 v10, v10
	v_exp_f32_e32 v11, v11
	v_exp_f32_e32 v12, v12
	v_exp_f32_e32 v13, v13
	v_add_f32_e32 v10, 1.0, v10
	v_add_f32_e32 v11, 1.0, v11
	v_add_f32_e32 v12, 1.0, v12
	v_add_f32_e32 v13, 1.0, v13
	v_rcp_f32_e32 v10, v10
	v_rcp_f32_e32 v11, v11
	v_rcp_f32_e32 v12, v12
	v_rcp_f32_e32 v13, v13
	v_mul_f32_e32 v6, v241, v6
	v_mul_f32_e32 v7, v241, v7
	v_mul_f32_e32 v8, v241, v8
	v_mul_f32_e32 v9, v241, v9
	v_mul_f32_e32 v2, v10, v2
	v_mul_f32_e32 v3, v11, v3
	v_mul_f32_e32 v4, v12, v4
	v_mul_f32_e32 v5, v13, v5
	v_mul_f32_e32 v6, v28, v6
	v_mul_f32_e32 v7, v29, v7
	v_mul_f32_e32 v8, v30, v8
	v_mul_f32_e32 v9, v31, v9
	v_mul_f32_e32 v6, v6, v2
	v_mul_f32_e32 v7, v7, v3
	v_mul_f32_e32 v8, v8, v4
	v_mul_f32_e32 v9, v9, v5
	v_cvt_pk_fp8_f32 v32, v6, v7
	s_nop 0
	v_cvt_pk_fp8_f32 v32, v8, v9 op_sel:[0,0,1]
	v_lshlrev_b32_e32 v2, 16, v196
	v_and_b32_e32 v3, 0xffff0000, v196
	v_lshlrev_b32_e32 v4, 16, v197
	v_and_b32_e32 v5, 0xffff0000, v197
	v_lshlrev_b32_e32 v6, 16, v192
	v_and_b32_e32 v7, 0xffff0000, v192
	v_lshlrev_b32_e32 v8, 16, v193
	v_and_b32_e32 v9, 0xffff0000, v193
	v_mul_f32_e32 v10, 0xbfb8aa3b, v2
	v_mul_f32_e32 v11, 0xbfb8aa3b, v3
	v_mul_f32_e32 v12, 0xbfb8aa3b, v4
	v_mul_f32_e32 v13, 0xbfb8aa3b, v5
	v_exp_f32_e32 v10, v10
	v_exp_f32_e32 v11, v11
	v_exp_f32_e32 v12, v12
	v_exp_f32_e32 v13, v13
	v_add_f32_e32 v10, 1.0, v10
	v_add_f32_e32 v11, 1.0, v11
	v_add_f32_e32 v12, 1.0, v12
	v_add_f32_e32 v13, 1.0, v13
	v_rcp_f32_e32 v10, v10
	v_rcp_f32_e32 v11, v11
	v_rcp_f32_e32 v12, v12
	v_rcp_f32_e32 v13, v13
	v_mul_f32_e32 v6, v241, v6
	v_mul_f32_e32 v7, v241, v7
	v_mul_f32_e32 v8, v241, v8
	v_mul_f32_e32 v9, v241, v9
	v_mul_f32_e32 v2, v10, v2
	v_mul_f32_e32 v3, v11, v3
	v_mul_f32_e32 v4, v12, v4
	v_mul_f32_e32 v5, v13, v5
	v_mul_f32_e32 v6, v22, v6
	v_mul_f32_e32 v7, v23, v7
	v_mul_f32_e32 v8, v24, v8
	v_mul_f32_e32 v9, v25, v9
	v_mul_f32_e32 v6, v6, v2
	v_mul_f32_e32 v7, v7, v3
	v_mul_f32_e32 v8, v8, v4
	v_mul_f32_e32 v9, v9, v5
	v_cvt_pk_fp8_f32 v33, v6, v7
	s_nop 0
	v_cvt_pk_fp8_f32 v33, v8, v9 op_sel:[0,0,1]
	s_nop 1
	global_store_dwordx2 v[250:251], v[32:33], off
	v_lshl_add_u64 v[250:251], v[250:251], 0, s[40:41]
	s_waitcnt vmcnt(18)
	v_mov_b32_e32 v32, v51
	v_mov_b32_e32 v33, v51
	v_lshlrev_b32_e32 v2, 16, v202
	v_and_b32_e32 v3, 0xffff0000, v202
	v_lshlrev_b32_e32 v4, 16, v203
	v_and_b32_e32 v5, 0xffff0000, v203
	v_lshlrev_b32_e32 v6, 16, v198
	v_and_b32_e32 v7, 0xffff0000, v198
	v_lshlrev_b32_e32 v8, 16, v199
	v_and_b32_e32 v9, 0xffff0000, v199
	v_mul_f32_e32 v10, 0xbfb8aa3b, v2
	v_mul_f32_e32 v11, 0xbfb8aa3b, v3
	v_mul_f32_e32 v12, 0xbfb8aa3b, v4
	v_mul_f32_e32 v13, 0xbfb8aa3b, v5
	v_exp_f32_e32 v10, v10
	v_exp_f32_e32 v11, v11
	v_exp_f32_e32 v12, v12
	v_exp_f32_e32 v13, v13
	v_add_f32_e32 v10, 1.0, v10
	v_add_f32_e32 v11, 1.0, v11
	v_add_f32_e32 v12, 1.0, v12
	v_add_f32_e32 v13, 1.0, v13
	v_rcp_f32_e32 v10, v10
	v_rcp_f32_e32 v11, v11
	v_rcp_f32_e32 v12, v12
	v_rcp_f32_e32 v13, v13
	v_mul_f32_e32 v6, v242, v6
	v_mul_f32_e32 v7, v242, v7
	v_mul_f32_e32 v8, v242, v8
	v_mul_f32_e32 v9, v242, v9
	v_mul_f32_e32 v2, v10, v2
	v_mul_f32_e32 v3, v11, v3
	v_mul_f32_e32 v4, v12, v4
	v_mul_f32_e32 v5, v13, v5
	v_mul_f32_e32 v6, v28, v6
	v_mul_f32_e32 v7, v29, v7
	v_mul_f32_e32 v8, v30, v8
	v_mul_f32_e32 v9, v31, v9
	v_mul_f32_e32 v6, v6, v2
	v_mul_f32_e32 v7, v7, v3
	v_mul_f32_e32 v8, v8, v4
	v_mul_f32_e32 v9, v9, v5
	v_cvt_pk_fp8_f32 v32, v6, v7
	s_nop 0
	v_cvt_pk_fp8_f32 v32, v8, v9 op_sel:[0,0,1]
	v_lshlrev_b32_e32 v2, 16, v204
	v_and_b32_e32 v3, 0xffff0000, v204
	v_lshlrev_b32_e32 v4, 16, v205
	v_and_b32_e32 v5, 0xffff0000, v205
	v_lshlrev_b32_e32 v6, 16, v200
	v_and_b32_e32 v7, 0xffff0000, v200
	v_lshlrev_b32_e32 v8, 16, v201
	v_and_b32_e32 v9, 0xffff0000, v201
	v_mul_f32_e32 v10, 0xbfb8aa3b, v2
	v_mul_f32_e32 v11, 0xbfb8aa3b, v3
	v_mul_f32_e32 v12, 0xbfb8aa3b, v4
	v_mul_f32_e32 v13, 0xbfb8aa3b, v5
	v_exp_f32_e32 v10, v10
	v_exp_f32_e32 v11, v11
	v_exp_f32_e32 v12, v12
	v_exp_f32_e32 v13, v13
	v_add_f32_e32 v10, 1.0, v10
	v_add_f32_e32 v11, 1.0, v11
	v_add_f32_e32 v12, 1.0, v12
	v_add_f32_e32 v13, 1.0, v13
	v_rcp_f32_e32 v10, v10
	v_rcp_f32_e32 v11, v11
	v_rcp_f32_e32 v12, v12
	v_rcp_f32_e32 v13, v13
	v_mul_f32_e32 v6, v242, v6
	v_mul_f32_e32 v7, v242, v7
	v_mul_f32_e32 v8, v242, v8
	v_mul_f32_e32 v9, v242, v9
	v_mul_f32_e32 v2, v10, v2
	v_mul_f32_e32 v3, v11, v3
	v_mul_f32_e32 v4, v12, v4
	v_mul_f32_e32 v5, v13, v5
	v_mul_f32_e32 v6, v22, v6
	v_mul_f32_e32 v7, v23, v7
	v_mul_f32_e32 v8, v24, v8
	v_mul_f32_e32 v9, v25, v9
	v_mul_f32_e32 v6, v6, v2
	v_mul_f32_e32 v7, v7, v3
	v_mul_f32_e32 v8, v8, v4
	v_mul_f32_e32 v9, v9, v5
	v_cvt_pk_fp8_f32 v33, v6, v7
	s_nop 0
	v_cvt_pk_fp8_f32 v33, v8, v9 op_sel:[0,0,1]
	s_nop 1
	global_store_dwordx2 v[250:251], v[32:33], off
	v_lshl_add_u64 v[250:251], v[250:251], 0, s[40:41]
	s_waitcnt vmcnt(17)
	v_mov_b32_e32 v32, v51
	v_mov_b32_e32 v33, v51
	v_lshlrev_b32_e32 v2, 16, v210
	v_and_b32_e32 v3, 0xffff0000, v210
	v_lshlrev_b32_e32 v4, 16, v211
	v_and_b32_e32 v5, 0xffff0000, v211
	v_lshlrev_b32_e32 v6, 16, v206
	v_and_b32_e32 v7, 0xffff0000, v206
	v_lshlrev_b32_e32 v8, 16, v207
	v_and_b32_e32 v9, 0xffff0000, v207
	v_mul_f32_e32 v10, 0xbfb8aa3b, v2
	v_mul_f32_e32 v11, 0xbfb8aa3b, v3
	v_mul_f32_e32 v12, 0xbfb8aa3b, v4
	v_mul_f32_e32 v13, 0xbfb8aa3b, v5
	v_exp_f32_e32 v10, v10
	v_exp_f32_e32 v11, v11
	v_exp_f32_e32 v12, v12
	v_exp_f32_e32 v13, v13
	v_add_f32_e32 v10, 1.0, v10
	v_add_f32_e32 v11, 1.0, v11
	v_add_f32_e32 v12, 1.0, v12
	v_add_f32_e32 v13, 1.0, v13
	v_rcp_f32_e32 v10, v10
	v_rcp_f32_e32 v11, v11
	v_rcp_f32_e32 v12, v12
	v_rcp_f32_e32 v13, v13
	v_mul_f32_e32 v6, v243, v6
	v_mul_f32_e32 v7, v243, v7
	v_mul_f32_e32 v8, v243, v8
	v_mul_f32_e32 v9, v243, v9
	v_mul_f32_e32 v2, v10, v2
	v_mul_f32_e32 v3, v11, v3
	v_mul_f32_e32 v4, v12, v4
	v_mul_f32_e32 v5, v13, v5
	v_mul_f32_e32 v6, v28, v6
	v_mul_f32_e32 v7, v29, v7
	v_mul_f32_e32 v8, v30, v8
	v_mul_f32_e32 v9, v31, v9
	v_mul_f32_e32 v6, v6, v2
	v_mul_f32_e32 v7, v7, v3
	v_mul_f32_e32 v8, v8, v4
	v_mul_f32_e32 v9, v9, v5
	v_cvt_pk_fp8_f32 v32, v6, v7
	s_nop 0
	v_cvt_pk_fp8_f32 v32, v8, v9 op_sel:[0,0,1]
	v_lshlrev_b32_e32 v2, 16, v212
	v_and_b32_e32 v3, 0xffff0000, v212
	v_lshlrev_b32_e32 v4, 16, v213
	v_and_b32_e32 v5, 0xffff0000, v213
	v_lshlrev_b32_e32 v6, 16, v208
	v_and_b32_e32 v7, 0xffff0000, v208
	v_lshlrev_b32_e32 v8, 16, v209
	v_and_b32_e32 v9, 0xffff0000, v209
	v_mul_f32_e32 v10, 0xbfb8aa3b, v2
	v_mul_f32_e32 v11, 0xbfb8aa3b, v3
	v_mul_f32_e32 v12, 0xbfb8aa3b, v4
	v_mul_f32_e32 v13, 0xbfb8aa3b, v5
	v_exp_f32_e32 v10, v10
	v_exp_f32_e32 v11, v11
	v_exp_f32_e32 v12, v12
	v_exp_f32_e32 v13, v13
	v_add_f32_e32 v10, 1.0, v10
	v_add_f32_e32 v11, 1.0, v11
	v_add_f32_e32 v12, 1.0, v12
	v_add_f32_e32 v13, 1.0, v13
	v_rcp_f32_e32 v10, v10
	v_rcp_f32_e32 v11, v11
	v_rcp_f32_e32 v12, v12
	v_rcp_f32_e32 v13, v13
	v_mul_f32_e32 v6, v243, v6
	v_mul_f32_e32 v7, v243, v7
	v_mul_f32_e32 v8, v243, v8
	v_mul_f32_e32 v9, v243, v9
	v_mul_f32_e32 v2, v10, v2
	v_mul_f32_e32 v3, v11, v3
	v_mul_f32_e32 v4, v12, v4
	v_mul_f32_e32 v5, v13, v5
	v_mul_f32_e32 v6, v22, v6
	v_mul_f32_e32 v7, v23, v7
	v_mul_f32_e32 v8, v24, v8
	v_mul_f32_e32 v9, v25, v9
	v_mul_f32_e32 v6, v6, v2
	v_mul_f32_e32 v7, v7, v3
	v_mul_f32_e32 v8, v8, v4
	v_mul_f32_e32 v9, v9, v5
	v_cvt_pk_fp8_f32 v33, v6, v7
	s_nop 0
	v_cvt_pk_fp8_f32 v33, v8, v9 op_sel:[0,0,1]
	s_nop 1
	global_store_dwordx2 v[250:251], v[32:33], off
	v_lshl_add_u64 v[250:251], v[250:251], 0, s[40:41]
	s_waitcnt vmcnt(16)
	v_mov_b32_e32 v32, v51
	v_mov_b32_e32 v33, v51
	v_lshlrev_b32_e32 v2, 16, v218
	v_and_b32_e32 v3, 0xffff0000, v218
	v_lshlrev_b32_e32 v4, 16, v219
	v_and_b32_e32 v5, 0xffff0000, v219
	v_lshlrev_b32_e32 v6, 16, v214
	v_and_b32_e32 v7, 0xffff0000, v214
	v_lshlrev_b32_e32 v8, 16, v215
	v_and_b32_e32 v9, 0xffff0000, v215
	v_mul_f32_e32 v10, 0xbfb8aa3b, v2
	v_mul_f32_e32 v11, 0xbfb8aa3b, v3
	v_mul_f32_e32 v12, 0xbfb8aa3b, v4
	v_mul_f32_e32 v13, 0xbfb8aa3b, v5
	v_exp_f32_e32 v10, v10
	v_exp_f32_e32 v11, v11
	v_exp_f32_e32 v12, v12
	v_exp_f32_e32 v13, v13
	v_add_f32_e32 v10, 1.0, v10
	v_add_f32_e32 v11, 1.0, v11
	v_add_f32_e32 v12, 1.0, v12
	v_add_f32_e32 v13, 1.0, v13
	v_rcp_f32_e32 v10, v10
	v_rcp_f32_e32 v11, v11
	v_rcp_f32_e32 v12, v12
	v_rcp_f32_e32 v13, v13
	v_mul_f32_e32 v6, v244, v6
	v_mul_f32_e32 v7, v244, v7
	v_mul_f32_e32 v8, v244, v8
	v_mul_f32_e32 v9, v244, v9
	v_mul_f32_e32 v2, v10, v2
	v_mul_f32_e32 v3, v11, v3
	v_mul_f32_e32 v4, v12, v4
	v_mul_f32_e32 v5, v13, v5
	v_mul_f32_e32 v6, v28, v6
	v_mul_f32_e32 v7, v29, v7
	v_mul_f32_e32 v8, v30, v8
	v_mul_f32_e32 v9, v31, v9
	v_mul_f32_e32 v6, v6, v2
	v_mul_f32_e32 v7, v7, v3
	v_mul_f32_e32 v8, v8, v4
	v_mul_f32_e32 v9, v9, v5
	v_cvt_pk_fp8_f32 v32, v6, v7
	s_nop 0
	v_cvt_pk_fp8_f32 v32, v8, v9 op_sel:[0,0,1]
	v_lshlrev_b32_e32 v2, 16, v220
	v_and_b32_e32 v3, 0xffff0000, v220
	v_lshlrev_b32_e32 v4, 16, v221
	v_and_b32_e32 v5, 0xffff0000, v221
	v_lshlrev_b32_e32 v6, 16, v216
	v_and_b32_e32 v7, 0xffff0000, v216
	v_lshlrev_b32_e32 v8, 16, v217
	v_and_b32_e32 v9, 0xffff0000, v217
	v_mul_f32_e32 v10, 0xbfb8aa3b, v2
	v_mul_f32_e32 v11, 0xbfb8aa3b, v3
	v_mul_f32_e32 v12, 0xbfb8aa3b, v4
	v_mul_f32_e32 v13, 0xbfb8aa3b, v5
	v_exp_f32_e32 v10, v10
	v_exp_f32_e32 v11, v11
	v_exp_f32_e32 v12, v12
	v_exp_f32_e32 v13, v13
	v_add_f32_e32 v10, 1.0, v10
	v_add_f32_e32 v11, 1.0, v11
	v_add_f32_e32 v12, 1.0, v12
	v_add_f32_e32 v13, 1.0, v13
	v_rcp_f32_e32 v10, v10
	v_rcp_f32_e32 v11, v11
	v_rcp_f32_e32 v12, v12
	v_rcp_f32_e32 v13, v13
	v_mul_f32_e32 v6, v244, v6
	v_mul_f32_e32 v7, v244, v7
	v_mul_f32_e32 v8, v244, v8
	v_mul_f32_e32 v9, v244, v9
	v_mul_f32_e32 v2, v10, v2
	v_mul_f32_e32 v3, v11, v3
	v_mul_f32_e32 v4, v12, v4
	v_mul_f32_e32 v5, v13, v5
	v_mul_f32_e32 v6, v22, v6
	v_mul_f32_e32 v7, v23, v7
	v_mul_f32_e32 v8, v24, v8
	v_mul_f32_e32 v9, v25, v9
	v_mul_f32_e32 v6, v6, v2
	v_mul_f32_e32 v7, v7, v3
	v_mul_f32_e32 v8, v8, v4
	v_mul_f32_e32 v9, v9, v5
	v_cvt_pk_fp8_f32 v33, v6, v7
	s_nop 0
	v_cvt_pk_fp8_f32 v33, v8, v9 op_sel:[0,0,1]
	s_nop 1
	global_store_dwordx2 v[250:251], v[32:33], off
	v_lshl_add_u64 v[250:251], v[250:251], 0, s[40:41]
	s_waitcnt vmcnt(15)
	v_mov_b32_e32 v32, v51
	v_mov_b32_e32 v33, v51
	v_lshlrev_b32_e32 v2, 16, v226
	v_and_b32_e32 v3, 0xffff0000, v226
	v_lshlrev_b32_e32 v4, 16, v227
	v_and_b32_e32 v5, 0xffff0000, v227
	v_lshlrev_b32_e32 v6, 16, v222
	v_and_b32_e32 v7, 0xffff0000, v222
	v_lshlrev_b32_e32 v8, 16, v223
	v_and_b32_e32 v9, 0xffff0000, v223
	v_mul_f32_e32 v10, 0xbfb8aa3b, v2
	v_mul_f32_e32 v11, 0xbfb8aa3b, v3
	v_mul_f32_e32 v12, 0xbfb8aa3b, v4
	v_mul_f32_e32 v13, 0xbfb8aa3b, v5
	v_exp_f32_e32 v10, v10
	v_exp_f32_e32 v11, v11
	v_exp_f32_e32 v12, v12
	v_exp_f32_e32 v13, v13
	v_add_f32_e32 v10, 1.0, v10
	v_add_f32_e32 v11, 1.0, v11
	v_add_f32_e32 v12, 1.0, v12
	v_add_f32_e32 v13, 1.0, v13
	v_rcp_f32_e32 v10, v10
	v_rcp_f32_e32 v11, v11
	v_rcp_f32_e32 v12, v12
	v_rcp_f32_e32 v13, v13
	v_mul_f32_e32 v6, v245, v6
	v_mul_f32_e32 v7, v245, v7
	v_mul_f32_e32 v8, v245, v8
	v_mul_f32_e32 v9, v245, v9
	v_mul_f32_e32 v2, v10, v2
	v_mul_f32_e32 v3, v11, v3
	v_mul_f32_e32 v4, v12, v4
	v_mul_f32_e32 v5, v13, v5
	v_mul_f32_e32 v6, v28, v6
	v_mul_f32_e32 v7, v29, v7
	v_mul_f32_e32 v8, v30, v8
	v_mul_f32_e32 v9, v31, v9
	v_mul_f32_e32 v6, v6, v2
	v_mul_f32_e32 v7, v7, v3
	v_mul_f32_e32 v8, v8, v4
	v_mul_f32_e32 v9, v9, v5
	v_cvt_pk_fp8_f32 v32, v6, v7
	s_nop 0
	v_cvt_pk_fp8_f32 v32, v8, v9 op_sel:[0,0,1]
	v_lshlrev_b32_e32 v2, 16, v228
	v_and_b32_e32 v3, 0xffff0000, v228
	v_lshlrev_b32_e32 v4, 16, v229
	v_and_b32_e32 v5, 0xffff0000, v229
	v_lshlrev_b32_e32 v6, 16, v224
	v_and_b32_e32 v7, 0xffff0000, v224
	v_lshlrev_b32_e32 v8, 16, v225
	v_and_b32_e32 v9, 0xffff0000, v225
	v_mul_f32_e32 v10, 0xbfb8aa3b, v2
	v_mul_f32_e32 v11, 0xbfb8aa3b, v3
	v_mul_f32_e32 v12, 0xbfb8aa3b, v4
	v_mul_f32_e32 v13, 0xbfb8aa3b, v5
	v_exp_f32_e32 v10, v10
	v_exp_f32_e32 v11, v11
	v_exp_f32_e32 v12, v12
	v_exp_f32_e32 v13, v13
	v_add_f32_e32 v10, 1.0, v10
	v_add_f32_e32 v11, 1.0, v11
	v_add_f32_e32 v12, 1.0, v12
	v_add_f32_e32 v13, 1.0, v13
	v_rcp_f32_e32 v10, v10
	v_rcp_f32_e32 v11, v11
	v_rcp_f32_e32 v12, v12
	v_rcp_f32_e32 v13, v13
	v_mul_f32_e32 v6, v245, v6
	v_mul_f32_e32 v7, v245, v7
	v_mul_f32_e32 v8, v245, v8
	v_mul_f32_e32 v9, v245, v9
	v_mul_f32_e32 v2, v10, v2
	v_mul_f32_e32 v3, v11, v3
	v_mul_f32_e32 v4, v12, v4
	v_mul_f32_e32 v5, v13, v5
	v_mul_f32_e32 v6, v22, v6
	v_mul_f32_e32 v7, v23, v7
	v_mul_f32_e32 v8, v24, v8
	v_mul_f32_e32 v9, v25, v9
	v_mul_f32_e32 v6, v6, v2
	v_mul_f32_e32 v7, v7, v3
	v_mul_f32_e32 v8, v8, v4
	v_mul_f32_e32 v9, v9, v5
	v_cvt_pk_fp8_f32 v33, v6, v7
	s_nop 0
	v_cvt_pk_fp8_f32 v33, v8, v9 op_sel:[0,0,1]
	s_nop 1
	global_store_dwordx2 v[250:251], v[32:33], off
	s_add_i32 s19, s19, s92
	s_add_i32 s7, s7, s10
	s_add_i32 s11, s11, s12
	s_cmpk_gt_i32 s19, 0x3ff
	v_lshl_add_u64 v[54:55], v[54:55], 0, s[82:83]
	s_cbranch_scc0 .LBB0_2123
	v_readlane_b32 s94, v254, 37
	v_readlane_b32 s93, v254, 36
	v_readlane_b32 s95, v254, 38

.LBB0_2398:
	ds_read_b128 v[148:151], v143
	ds_read_b128 v[152:155], v143 offset:1024
	ds_read_b128 v[156:159], v143 offset:2048
	ds_read_b128 v[160:163], v143 offset:3072
	s_add_u32 s48, s77, s44
	s_addc_u32 s49, s78, s45
	s_add_u32 s46, s44, 0x100
	s_addc_u32 s47, s45, 0
	s_cmp_eq_u32 s79, 12
	s_cselect_b32 s49, s37, s49
	s_cselect_b32 s48, s39, s48
	s_cselect_b32 s80, 0, s46
	s_cselect_b32 s81, s9, s3
	s_add_i32 m0, s56, 0xc000
	ds_read_b128 v[168:171], v144 offset:1024
	ds_read_b128 v[172:175], v144 offset:2048
	ds_read_b128 v[164:167], v144
	ds_read_b32 v66, v136 offset:512
	ds_read_b128 v[176:179], v144 offset:3072
	ds_read_b128 v[180:183], v144 offset:4096
	ds_read_b128 v[184:187], v144 offset:5120
	ds_read_b128 v[188:191], v144 offset:6144
	ds_read_b128 v[192:195], v144 offset:7168
	s_add_u32 s44, s26, s44
	s_waitcnt lgkmcnt(0)
	v_add_u32_e32 v66, v66, v1
	s_addc_u32 s45, s27, s45
	global_load_lds_dwordx4 v66, s[44:45]
	ds_read_b32 v66, v136 offset:768
	s_add_i32 m0, s56, 0xe000
	s_waitcnt lgkmcnt(0)
	v_add_u32_e32 v66, v66, v1
	global_load_lds_dwordx4 v66, s[44:45]
	s_waitcnt lgkmcnt(8)
	s_barrier
	s_waitcnt lgkmcnt(0)
	s_setprio 1
	v_mfma_scale_f32_16x16x128_f8f6f4 v[126:129], v[148:155], v[164:171], v[126:129], v145, v145 op_sel_hi:[0,0,0]
	v_mfma_scale_f32_16x16x128_f8f6f4 v[118:121], v[156:163], v[164:171], v[118:121], v145, v145 op_sel_hi:[0,0,0]
	v_mfma_scale_f32_16x16x128_f8f6f4 v[110:113], v[148:155], v[172:179], v[110:113], v145, v145 op_sel_hi:[0,0,0]
	v_mfma_scale_f32_16x16x128_f8f6f4 v[102:105], v[156:163], v[172:179], v[102:105], v145, v145 op_sel_hi:[0,0,0]
	v_mfma_scale_f32_16x16x128_f8f6f4 v[212:215], v[148:155], v[180:187], v[94:97], v145, v145 op_sel_hi:[0,0,0]
	v_mfma_scale_f32_16x16x128_f8f6f4 v[216:219], v[156:163], v[180:187], v[86:89], v145, v145 op_sel_hi:[0,0,0]
	v_mfma_scale_f32_16x16x128_f8f6f4 v[220:223], v[148:155], v[188:195], v[78:81], v145, v145 op_sel_hi:[0,0,0]
	v_mfma_scale_f32_16x16x128_f8f6f4 v[224:227], v[156:163], v[188:195], v[204:207], v145, v145 op_sel_hi:[0,0,0]
	s_setprio 0
	s_barrier
	s_add_i32 s44, s68, s55
	v_lshl_add_u64 v[134:135], s[48:49], 0, v[130:131]
	s_mov_b32 m0, s44
	ds_read_b128 v[196:199], v146
	ds_read_b128 v[200:203], v146 offset:1024
	ds_read_b128 v[204:207], v146 offset:2048
	ds_read_b128 v[208:211], v146 offset:3072
	global_load_lds_dwordx4 v[134:135], off
	v_lshl_add_u64 v[66:67], v[134:135], 0, s[10:11]
	s_add_i32 m0, s44, 0x2000
	s_nop 0
	global_load_lds_dwordx4 v[66:67], off
	s_barrier
	s_waitcnt lgkmcnt(0)
	s_setprio 1
	s_waitcnt lgkmcnt(0)
	v_mfma_scale_f32_16x16x128_f8f6f4 v[122:125], v[196:203], v[164:171], v[122:125], v145, v145 op_sel_hi:[0,0,0]
	v_mfma_scale_f32_16x16x128_f8f6f4 v[114:117], v[204:211], v[164:171], v[114:117], v145, v145 op_sel_hi:[0,0,0]
	v_mfma_scale_f32_16x16x128_f8f6f4 v[106:109], v[196:203], v[172:179], v[106:109], v145, v145 op_sel_hi:[0,0,0]
	v_mfma_scale_f32_16x16x128_f8f6f4 v[98:101], v[204:211], v[172:179], v[98:101], v145, v145 op_sel_hi:[0,0,0]
	v_mfma_scale_f32_16x16x128_f8f6f4 v[172:175], v[196:203], v[180:187], v[90:93], v145, v145 op_sel_hi:[0,0,0]
	v_mfma_scale_f32_16x16x128_f8f6f4 v[176:179], v[204:211], v[180:187], v[82:85], v145, v145 op_sel_hi:[0,0,0]
	v_mfma_scale_f32_16x16x128_f8f6f4 v[180:183], v[196:203], v[188:195], v[74:77], v145, v145 op_sel_hi:[0,0,0]
	v_mfma_scale_f32_16x16x128_f8f6f4 v[184:187], v[204:211], v[188:195], v[10:13], v145, v145 op_sel_hi:[0,0,0]
	s_setprio 0
	v_lshl_add_u32 v137, s81, 2, v253
	s_barrier
	ds_read_b128 v[66:69], v144 offset:16384
	ds_read_b128 v[70:73], v144 offset:17408
	s_nop 0
	ds_read_b128 v[74:77], v144 offset:18432
	ds_read_b128 v[78:81], v144 offset:19456
	ds_read_b128 v[82:85], v144 offset:20480
	ds_read_b128 v[86:89], v144 offset:21504
	ds_read_b32 v10, v137
	ds_read_b128 v[90:93], v144 offset:22528
	ds_read_b128 v[94:97], v144 offset:23552
	s_add_u32 s44, s96, s80
	s_addc_u32 s45, s97, 0
	s_waitcnt lgkmcnt(0)
	v_add_u32_e32 v10, v10, v1
	s_mov_b32 m0, s56
	s_nop 0
	global_load_lds_dwordx4 v10, s[44:45]
	ds_read_b32 v10, v137 offset:256
	s_mov_b32 m0, s58
	s_waitcnt lgkmcnt(0)
	v_add_u32_e32 v10, v10, v1
	global_load_lds_dwordx4 v10, s[44:45]
	s_barrier
	s_waitcnt lgkmcnt(0)
	s_setprio 1
	v_mfma_scale_f32_16x16x128_f8f6f4 v[62:65], v[148:155], v[66:73], v[62:65], v145, v145 op_sel_hi:[0,0,0]
	v_mfma_scale_f32_16x16x128_f8f6f4 v[54:57], v[156:163], v[66:73], v[54:57], v145, v145 op_sel_hi:[0,0,0]
	v_mfma_scale_f32_16x16x128_f8f6f4 v[46:49], v[148:155], v[74:81], v[46:49], v145, v145 op_sel_hi:[0,0,0]
	v_mfma_scale_f32_16x16x128_f8f6f4 v[244:247], v[156:163], v[90:97], v[244:247], v145, v145 op_sel_hi:[0,0,0]
	v_mfma_scale_f32_16x16x128_f8f6f4 v[228:231], v[156:163], v[74:81], v[38:41], v145, v145 op_sel_hi:[0,0,0]
	v_mfma_scale_f32_16x16x128_f8f6f4 v[232:235], v[148:155], v[82:89], v[30:33], v145, v145 op_sel_hi:[0,0,0]
	v_mfma_scale_f32_16x16x128_f8f6f4 v[236:239], v[156:163], v[82:89], v[22:25], v145, v145 op_sel_hi:[0,0,0]
	v_mfma_scale_f32_16x16x128_f8f6f4 v[240:243], v[148:155], v[90:97], v[14:17], v145, v145 op_sel_hi:[0,0,0]
	s_setprio 0
	s_barrier
	s_add_i32 s48, s69, s55
	v_lshl_add_u64 v[10:11], v[134:135], 0, s[12:13]
	s_mov_b32 m0, s48
	s_nop 0
	global_load_lds_dwordx4 v[10:11], off
	v_lshl_add_u64 v[10:11], v[134:135], 0, s[14:15]
	s_add_i32 m0, s48, 0x2000
	s_nop 0
	global_load_lds_dwordx4 v[10:11], off
	s_waitcnt vmcnt(6)
	s_barrier
	s_setprio 1
	v_mfma_scale_f32_16x16x128_f8f6f4 v[58:61], v[196:203], v[66:73], v[58:61], v145, v145 op_sel_hi:[0,0,0]
	v_mfma_scale_f32_16x16x128_f8f6f4 v[50:53], v[204:211], v[66:73], v[50:53], v145, v145 op_sel_hi:[0,0,0]
	v_mfma_scale_f32_16x16x128_f8f6f4 v[42:45], v[196:203], v[74:81], v[42:45], v145, v145 op_sel_hi:[0,0,0]
	v_mfma_scale_f32_16x16x128_f8f6f4 v[248:251], v[204:211], v[74:81], v[34:37], v145, v145 op_sel_hi:[0,0,0]
	v_mfma_scale_f32_16x16x128_f8f6f4 v[138:141], v[196:203], v[82:89], v[26:29], v145, v145 op_sel_hi:[0,0,0]
	v_mfma_scale_f32_16x16x128_f8f6f4 v[66:69], v[204:211], v[82:89], v[18:21], v145, v145 op_sel_hi:[0,0,0]
	v_mfma_scale_f32_16x16x128_f8f6f4 v[70:73], v[196:203], v[90:97], v[6:9], v145, v145 op_sel_hi:[0,0,0]
	v_mfma_scale_f32_16x16x128_f8f6f4 v[208:211], v[204:211], v[90:97], v[2:5], v145, v145 op_sel_hi:[0,0,0]
	s_setprio 0
	s_add_i32 s48, 0, 0x18000
	v_add_u32_e32 v10, s48, v142
	s_barrier
	s_nop 2
	ds_read_b128 v[2:5], v10
	ds_read_b128 v[6:9], v10 offset:1024
	ds_read_b128 v[148:151], v10 offset:2048
	ds_read_b128 v[152:155], v10 offset:3072
	ds_read_b128 v[10:13], v144 offset:32768
	ds_read_b128 v[14:17], v144 offset:33792
	ds_read_b128 v[18:21], v144 offset:34816
	ds_read_b128 v[22:25], v144 offset:35840
	ds_read_b32 v74, v137 offset:512
	ds_read_b128 v[26:29], v144 offset:36864
	ds_read_b128 v[30:33], v144 offset:37888
	ds_read_b128 v[34:37], v144 offset:38912
	ds_read_b128 v[38:41], v144 offset:39936
	s_waitcnt lgkmcnt(0)
	v_add_u32_e32 v74, v74, v1
	s_mov_b32 m0, s59
	s_nop 0
	global_load_lds_dwordx4 v74, s[44:45]
	ds_read_b32 v74, v137 offset:768
	s_mov_b32 m0, s60
	s_waitcnt lgkmcnt(0)
	v_add_u32_e32 v74, v74, v1
	global_load_lds_dwordx4 v74, s[44:45]
	s_waitcnt lgkmcnt(8)
	s_barrier
	s_waitcnt lgkmcnt(0)
	s_setprio 1
	v_mfma_scale_f32_16x16x128_f8f6f4 v[126:129], v[2:9], v[10:17], v[126:129], v145, v145 op_sel_hi:[0,0,0]
	v_mfma_scale_f32_16x16x128_f8f6f4 v[118:121], v[148:155], v[10:17], v[118:121], v145, v145 op_sel_hi:[0,0,0]
	v_mfma_scale_f32_16x16x128_f8f6f4 v[110:113], v[2:9], v[18:25], v[110:113], v145, v145 op_sel_hi:[0,0,0]
	v_mfma_scale_f32_16x16x128_f8f6f4 v[102:105], v[148:155], v[18:25], v[102:105], v145, v145 op_sel_hi:[0,0,0]
	v_mfma_scale_f32_16x16x128_f8f6f4 v[94:97], v[2:9], v[26:33], v[212:215], v145, v145 op_sel_hi:[0,0,0]
	v_mfma_scale_f32_16x16x128_f8f6f4 v[86:89], v[148:155], v[26:33], v[216:219], v145, v145 op_sel_hi:[0,0,0]
	v_mfma_scale_f32_16x16x128_f8f6f4 v[78:81], v[2:9], v[34:41], v[220:223], v145, v145 op_sel_hi:[0,0,0]
	v_mfma_scale_f32_16x16x128_f8f6f4 v[204:207], v[148:155], v[34:41], v[224:227], v145, v145 op_sel_hi:[0,0,0]
	s_setprio 0
	s_barrier
	s_add_i32 s49, 0, 0x1c000
	v_add_u32_e32 v74, s49, v142
	s_add_i32 s48, s48, s55
	ds_read_b128 v[156:159], v74
	ds_read_b128 v[160:163], v74 offset:1024
	ds_read_b128 v[164:167], v74 offset:2048
	ds_read_b128 v[168:171], v74 offset:3072
	v_lshl_add_u64 v[74:75], v[134:135], 0, s[22:23]
	s_mov_b32 m0, s48
	s_nop 0
	global_load_lds_dwordx4 v[74:75], off
	v_lshl_add_u64 v[74:75], v[134:135], 0, s[24:25]
	s_add_i32 m0, s48, 0x2000
	s_nop 0
	global_load_lds_dwordx4 v[74:75], off
	s_barrier
	s_waitcnt lgkmcnt(0)
	s_setprio 1
	s_waitcnt lgkmcnt(0)
	v_mfma_scale_f32_16x16x128_f8f6f4 v[122:125], v[156:163], v[10:17], v[122:125], v145, v145 op_sel_hi:[0,0,0]
	v_mfma_scale_f32_16x16x128_f8f6f4 v[114:117], v[164:171], v[10:17], v[114:117], v145, v145 op_sel_hi:[0,0,0]
	v_mfma_scale_f32_16x16x128_f8f6f4 v[106:109], v[156:163], v[18:25], v[106:109], v145, v145 op_sel_hi:[0,0,0]
	v_mfma_scale_f32_16x16x128_f8f6f4 v[98:101], v[164:171], v[18:25], v[98:101], v145, v145 op_sel_hi:[0,0,0]
	v_mfma_scale_f32_16x16x128_f8f6f4 v[90:93], v[156:163], v[26:33], v[172:175], v145, v145 op_sel_hi:[0,0,0]
	v_mfma_scale_f32_16x16x128_f8f6f4 v[82:85], v[164:171], v[26:33], v[176:179], v145, v145 op_sel_hi:[0,0,0]
	v_mfma_scale_f32_16x16x128_f8f6f4 v[74:77], v[156:163], v[34:41], v[180:183], v145, v145 op_sel_hi:[0,0,0]
	v_mfma_scale_f32_16x16x128_f8f6f4 v[10:13], v[164:171], v[34:41], v[184:187], v145, v145 op_sel_hi:[0,0,0]
	s_setprio 0
	s_barrier
	s_nop 1
	ds_read_b128 v[172:175], v144 offset:49152
	ds_read_b128 v[176:179], v144 offset:50176
	ds_read_b128 v[180:183], v144 offset:51200
	ds_read_b128 v[184:187], v144 offset:52224
	ds_read_b32 v14, v137
	ds_read_b128 v[188:191], v144 offset:53248
	ds_read_b128 v[192:195], v144 offset:54272
	ds_read_b128 v[196:199], v144 offset:55296
	ds_read_b128 v[200:203], v144 offset:56320
	s_waitcnt lgkmcnt(0)
	v_add_u32_e32 v132, v14, v1
	v_lshl_add_u64 v[14:15], s[44:45], 0, v[132:133]
	v_lshl_add_u64 v[14:15], v[14:15], 0, s[22:23]
	s_mov_b32 m0, s62
	s_nop 0
	global_load_lds_dwordx4 v[14:15], off
	ds_read_b32 v14, v137 offset:256
	s_mov_b32 m0, s63
	s_waitcnt lgkmcnt(0)
	v_add_u32_e32 v132, v14, v1
	v_lshl_add_u64 v[14:15], s[44:45], 0, v[132:133]
	v_lshl_add_u64 v[14:15], v[14:15], 0, s[22:23]
	global_load_lds_dwordx4 v[14:15], off
	s_barrier
	s_waitcnt lgkmcnt(0)
	s_setprio 1
	v_mfma_scale_f32_16x16x128_f8f6f4 v[62:65], v[2:9], v[172:179], v[62:65], v145, v145 op_sel_hi:[0,0,0]
	v_mfma_scale_f32_16x16x128_f8f6f4 v[54:57], v[148:155], v[172:179], v[54:57], v145, v145 op_sel_hi:[0,0,0]
	v_mfma_scale_f32_16x16x128_f8f6f4 v[46:49], v[2:9], v[180:187], v[46:49], v145, v145 op_sel_hi:[0,0,0]
	v_mfma_scale_f32_16x16x128_f8f6f4 v[38:41], v[148:155], v[180:187], v[228:231], v145, v145 op_sel_hi:[0,0,0]
	v_mfma_scale_f32_16x16x128_f8f6f4 v[30:33], v[2:9], v[188:195], v[232:235], v145, v145 op_sel_hi:[0,0,0]
	v_mfma_scale_f32_16x16x128_f8f6f4 v[22:25], v[148:155], v[188:195], v[236:239], v145, v145 op_sel_hi:[0,0,0]
	v_mfma_scale_f32_16x16x128_f8f6f4 v[14:17], v[2:9], v[196:203], v[240:243], v145, v145 op_sel_hi:[0,0,0]
	v_mfma_scale_f32_16x16x128_f8f6f4 v[244:247], v[148:155], v[196:203], v[244:247], v145, v145 op_sel_hi:[0,0,0]
	s_setprio 0
	s_barrier
	s_add_i32 s44, s49, s55
	v_lshl_add_u64 v[2:3], v[134:135], 0, s[28:29]
	s_mov_b32 m0, s44
	s_nop 0
	global_load_lds_dwordx4 v[2:3], off
	v_lshl_add_u64 v[2:3], v[134:135], 0, s[30:31]
	s_add_i32 m0, s44, 0x2000
	s_nop 0
	global_load_lds_dwordx4 v[2:3], off
	s_waitcnt vmcnt(6)
	s_barrier
	s_setprio 1
	v_mfma_scale_f32_16x16x128_f8f6f4 v[58:61], v[156:163], v[172:179], v[58:61], v145, v145 op_sel_hi:[0,0,0]
	v_mfma_scale_f32_16x16x128_f8f6f4 v[50:53], v[164:171], v[172:179], v[50:53], v145, v145 op_sel_hi:[0,0,0]
	v_mfma_scale_f32_16x16x128_f8f6f4 v[42:45], v[156:163], v[180:187], v[42:45], v145, v145 op_sel_hi:[0,0,0]
	v_mfma_scale_f32_16x16x128_f8f6f4 v[34:37], v[164:171], v[180:187], v[248:251], v145, v145 op_sel_hi:[0,0,0]
	v_mfma_scale_f32_16x16x128_f8f6f4 v[26:29], v[156:163], v[188:195], v[138:141], v145, v145 op_sel_hi:[0,0,0]
	v_mfma_scale_f32_16x16x128_f8f6f4 v[18:21], v[164:171], v[188:195], v[66:69], v145, v145 op_sel_hi:[0,0,0]
	v_mfma_scale_f32_16x16x128_f8f6f4 v[6:9], v[156:163], v[196:203], v[70:73], v145, v145 op_sel_hi:[0,0,0]
	v_mfma_scale_f32_16x16x128_f8f6f4 v[2:5], v[164:171], v[196:203], v[208:211], v145, v145 op_sel_hi:[0,0,0]
	s_setprio 0
	s_add_i32 s79, s79, 2
	s_cmp_gt_u32 s79, 13
	s_mov_b64 s[44:45], s[46:47]
	s_barrier
	s_cbranch_scc0 .LBB0_2398
	v_mov_b32_e32 v151, v0
	s_lshl_b32 s44, s76, 8
	v_mov_b32_e32 v138, 0
	v_ashrrev_i32_e32 v153, 8, v151
	v_and_b32_e32 v149, 15, v151
	v_lshlrev_b32_e32 v152, 6, v153
	v_or_b32_e32 v136, v152, v149
	v_bfe_u32 v150, v151, 6, 2
	v_bfe_u32 v154, v151, 4, 2
	v_add_u32_e32 v66, s44, v136
	s_waitcnt vmcnt(0)
	v_cmp_lt_i32_e32 vcc, v66, v252
	v_ashrrev_i32_e32 v137, 31, v136
	v_or3_b32 v148, v150, s2, v154
	v_mov_b32_e32 v140, 0
	s_ashr_i32 s9, s8, 31
	s_ashr_i32 s45, s44, 31
	s_lshl_b64 s[48:49], s[8:9], 16
	s_add_u32 s3, s51, s48
	s_addc_u32 s9, s52, s49
	s_lshl_b64 s[48:49], s[44:45], 2
	s_add_u32 s48, s3, s48
	s_addc_u32 s49, s9, s49
	v_lshl_add_u64 v[176:177], v[136:137], 2, s[48:49]
	v_add_u32_e32 v179, s44, v136
	s_mov_b64 s[46:47], exec
	v_add_u32_e32 v178, 0, v179
	v_cmp_lt_i32_e32 vcc, v178, v252
	s_and_b64 exec, s[46:47], vcc
	global_load_dword v160, v[176:177], off
	v_add_u32_e32 v178, 16, v179
	v_cmp_lt_i32_e32 vcc, v178, v252
	s_and_b64 exec, s[46:47], vcc
	global_load_dword v161, v[176:177], off offset:64
	v_add_u32_e32 v178, 32, v179
	v_cmp_lt_i32_e32 vcc, v178, v252
	s_and_b64 exec, s[46:47], vcc
	global_load_dword v162, v[176:177], off offset:128
	v_add_u32_e32 v178, 48, v179
	v_cmp_lt_i32_e32 vcc, v178, v252
	s_and_b64 exec, s[46:47], vcc
	global_load_dword v163, v[176:177], off offset:192
	v_add_u32_e32 v178, 128, v179
	v_cmp_lt_i32_e32 vcc, v178, v252
	s_and_b64 exec, s[46:47], vcc
	global_load_dword v164, v[176:177], off offset:512
	v_add_u32_e32 v178, 144, v179
	v_cmp_lt_i32_e32 vcc, v178, v252
	s_and_b64 exec, s[46:47], vcc
	global_load_dword v165, v[176:177], off offset:576
	v_add_u32_e32 v178, 160, v179
	v_cmp_lt_i32_e32 vcc, v178, v252
	s_and_b64 exec, s[46:47], vcc
	global_load_dword v166, v[176:177], off offset:640
	v_add_u32_e32 v178, 176, v179
	v_cmp_lt_i32_e32 vcc, v178, v252
	s_and_b64 exec, s[46:47], vcc
	global_load_dword v167, v[176:177], off offset:704
	s_mov_b64 exec, s[46:47]
	s_waitcnt vmcnt(0)
	v_add_u32_e32 v178, 0, v179
	v_cmp_lt_i32_e32 vcc, v178, v252
	s_and_b64 exec, s[46:47], vcc
	v_lshrrev_b32_e32 v180, 1, v160
	v_mov_b32_e32 v181, v133
	v_lshl_add_u64 v[180:181], v[180:181], 2, s[18:19]
	global_load_dword v168, v[180:181], off
	v_add_u32_e32 v178, 16, v179
	v_cmp_lt_i32_e32 vcc, v178, v252
	s_and_b64 exec, s[46:47], vcc
	v_lshrrev_b32_e32 v180, 1, v161
	v_mov_b32_e32 v181, v133
	v_lshl_add_u64 v[180:181], v[180:181], 2, s[18:19]
	global_load_dword v169, v[180:181], off
	v_add_u32_e32 v178, 32, v179
	v_cmp_lt_i32_e32 vcc, v178, v252
	s_and_b64 exec, s[46:47], vcc
	v_lshrrev_b32_e32 v180, 1, v162
	v_mov_b32_e32 v181, v133
	v_lshl_add_u64 v[180:181], v[180:181], 2, s[18:19]
	global_load_dword v170, v[180:181], off
	v_add_u32_e32 v178, 48, v179
	v_cmp_lt_i32_e32 vcc, v178, v252
	s_and_b64 exec, s[46:47], vcc
	v_lshrrev_b32_e32 v180, 1, v163
	v_mov_b32_e32 v181, v133
	v_lshl_add_u64 v[180:181], v[180:181], 2, s[18:19]
	global_load_dword v171, v[180:181], off
	v_add_u32_e32 v178, 128, v179
	v_cmp_lt_i32_e32 vcc, v178, v252
	s_and_b64 exec, s[46:47], vcc
	v_lshrrev_b32_e32 v180, 1, v164
	v_mov_b32_e32 v181, v133
	v_lshl_add_u64 v[180:181], v[180:181], 2, s[18:19]
	global_load_dword v172, v[180:181], off
	v_add_u32_e32 v178, 144, v179
	v_cmp_lt_i32_e32 vcc, v178, v252
	s_and_b64 exec, s[46:47], vcc
	v_lshrrev_b32_e32 v180, 1, v165
	v_mov_b32_e32 v181, v133
	v_lshl_add_u64 v[180:181], v[180:181], 2, s[18:19]
	global_load_dword v173, v[180:181], off
	v_add_u32_e32 v178, 160, v179
	v_cmp_lt_i32_e32 vcc, v178, v252
	s_and_b64 exec, s[46:47], vcc
	v_lshrrev_b32_e32 v180, 1, v166
	v_mov_b32_e32 v181, v133
	v_lshl_add_u64 v[180:181], v[180:181], 2, s[18:19]
	global_load_dword v174, v[180:181], off
	v_add_u32_e32 v178, 176, v179
	v_cmp_lt_i32_e32 vcc, v178, v252
	s_and_b64 exec, s[46:47], vcc
	v_lshrrev_b32_e32 v180, 1, v167
	v_mov_b32_e32 v181, v133
	v_lshl_add_u64 v[180:181], v[180:181], 2, s[18:19]
	global_load_dword v175, v[180:181], off
	s_mov_b64 exec, s[46:47]
	s_waitcnt vmcnt(0)
	v_cmp_lt_i32_e32 vcc, v66, v252
	s_and_saveexec_b64 s[46:47], vcc
	s_cbranch_execz .LBB0_2403
	s_ashr_i32 s9, s8, 31
	s_ashr_i32 s45, s44, 31
	s_lshl_b64 s[48:49], s[8:9], 16
	s_add_u32 s3, s51, s48
	s_addc_u32 s9, s52, s49
	s_lshl_b64 s[48:49], s[44:45], 2
	s_add_u32 s48, s3, s48
	s_addc_u32 s49, s9, s49
	v_lshl_add_u64 v[66:67], v[136:137], 2, s[48:49]
	v_mov_b32_e32 v134, v160
	v_cmp_eq_u32_e32 vcc, 0, v148
	v_lshrrev_b32_e32 v132, 1, v134
	v_lshl_add_u64 v[66:67], v[132:133], 2, s[18:19]
	v_mov_b32_e32 v132, v168
	s_and_saveexec_b64 s[48:49], vcc
	s_cbranch_execz .LBB0_2402
	v_mov_b32_e32 v135, v133
	v_add_u32_e32 v68, s57, v136
	v_lshl_add_u64 v[66:67], v[134:135], 2, s[20:21]
	global_store_dword v[66:67], v68, off
